# accumulator clears with 64-bit moves (all GEMM phases)
# speedup vs baseline: 1.0006x; 1.0006x over previous
; template <class Epi, class Sched, class Prob>
; __device__ __forceinline__ void gemm_phase(LAS unsigned char* lds, LAS unsigned char* lds_epi, const Prob g, const Sched& S, const Epi& E, int wid) {
;     ...
;         const bool has_next = S.next(ui + 1, nxt);
;         const char* nA = has_next ? g.a_base(nxt) : cA; const char* nB = has_next ? g.b_base(nxt) : cB;
; _Pragma("clang loop unroll(disable)")
;         for (int t = 0; t < nt; t += 2) {
;             const bool last = (t == nt - 2);
;             const char* a1 = cA + (size_t)(t + 1) * kstep;
;             const char* a2 = last ? nA : cA + (size_t)(t + 2) * kstep; const char* b2 = last ? nB : cB + (size_t)(t + 2) * kstep;
.LBB0_261:
	s_ashr_i32 s3, s2, 31
	s_lshl_b64 s[48:49], s[2:3], 20
	s_add_u32 s48, s33, s48
	s_addc_u32 s49, s39, s49
	s_and_b64 s[50:51], s[46:47], exec
	s_cselect_b32 s3, s49, s15
	s_cselect_b32 s77, s48, s14
	s_ashr_i32 s45, s44, 31
	s_lshl_b64 s[50:51], s[44:45], 20
	s_add_u32 s50, s56, s50
	s_addc_u32 s51, s57, s51
	s_and_b64 s[54:55], s[46:47], exec
	s_cselect_b32 s45, s51, s53
	s_cselect_b32 s78, s50, s52
	s_add_u32 s14, s14, 0x80
	s_addc_u32 s15, s15, 0
	s_add_u32 s79, s52, 0x100
	v_mov_b32_e32 v44, 0
	s_addc_u32 s80, s53, 0
	s_mov_b32 s81, -2
	v_mov_b32_e32 v45, 0
	v_mov_b64_e32 v[46:47], 0
	v_mov_b64_e32 v[24:25], 0
	v_mov_b64_e32 v[26:27], 0
	v_mov_b64_e32 v[76:77], 0
	v_mov_b64_e32 v[78:79], 0
	v_mov_b64_e32 v[60:61], 0
	v_mov_b64_e32 v[62:63], 0
	v_mov_b64_e32 v[100:101], 0
	v_mov_b64_e32 v[102:103], 0
	v_mov_b64_e32 v[88:89], 0
	v_mov_b64_e32 v[90:91], 0
	v_mov_b64_e32 v[116:117], 0
	v_mov_b64_e32 v[118:119], 0
	v_mov_b64_e32 v[108:109], 0
	v_mov_b64_e32 v[110:111], 0
	v_mov_b64_e32 v[4:5], 0
	v_mov_b64_e32 v[6:7], 0
	v_mov_b64_e32 v[0:1], 0
	v_mov_b64_e32 v[2:3], 0
	v_mov_b64_e32 v[20:21], 0
	v_mov_b64_e32 v[22:23], 0
	v_mov_b64_e32 v[12:13], 0
	v_mov_b64_e32 v[14:15], 0
	v_mov_b64_e32 v[40:41], 0
	v_mov_b64_e32 v[42:43], 0
	v_mov_b64_e32 v[32:33], 0
	v_mov_b64_e32 v[34:35], 0
	v_mov_b64_e32 v[72:73], 0
	v_mov_b64_e32 v[74:75], 0
	v_mov_b64_e32 v[56:57], 0
	v_mov_b64_e32 v[58:59], 0
	v_mov_b64_e32 v[64:65], 0
	v_mov_b64_e32 v[66:67], 0
	v_mov_b64_e32 v[48:49], 0
	v_mov_b64_e32 v[50:51], 0
	v_mov_b64_e32 v[96:97], 0
	v_mov_b64_e32 v[98:99], 0
	v_mov_b64_e32 v[84:85], 0
	v_mov_b64_e32 v[86:87], 0
	v_mov_b64_e32 v[112:113], 0
	v_mov_b64_e32 v[114:115], 0
	v_mov_b64_e32 v[104:105], 0
	v_mov_b64_e32 v[106:107], 0
	v_mov_b64_e32 v[124:125], 0
	v_mov_b64_e32 v[126:127], 0
	v_mov_b64_e32 v[120:121], 0
	v_mov_b64_e32 v[122:123], 0
	v_mov_b64_e32 v[16:17], 0
	v_mov_b64_e32 v[18:19], 0
	v_mov_b64_e32 v[8:9], 0
	v_mov_b64_e32 v[10:11], 0
	v_mov_b64_e32 v[36:37], 0
	v_mov_b64_e32 v[38:39], 0
	v_mov_b64_e32 v[28:29], 0
	v_mov_b64_e32 v[30:31], 0
	v_mov_b64_e32 v[68:69], 0
	v_mov_b64_e32 v[70:71], 0
	v_mov_b64_e32 v[52:53], 0
	v_mov_b64_e32 v[54:55], 0
	v_mov_b64_e32 v[92:93], 0
	v_mov_b64_e32 v[94:95], 0
	v_mov_b64_e32 v[80:81], 0
	v_mov_b64_e32 v[82:83], 0

; template <class Epi, class Sched, class Prob>
; __device__ __forceinline__ void gemm_phase(LAS unsigned char* lds, LAS unsigned char* lds_epi, const Prob g, const Sched& S, const Epi& E, int wid) {
;     ...
;         const bool has_next = S.next(ui + 1, nxt);
;         const char* nA = has_next ? g.a_base(nxt) : cA; const char* nB = has_next ? g.b_base(nxt) : cB;
; _Pragma("clang loop unroll(disable)")
;         for (int t = 0; t < nt; t += 2) {
;             const bool last = (t == nt - 2);
;             const char* a1 = cA + (size_t)(t + 1) * kstep;
;             const char* a2 = last ? nA : cA + (size_t)(t + 2) * kstep; const char* b2 = last ? nB : cB + (size_t)(t + 2) * kstep;
.LBB0_1247:
	s_ashr_i32 s3, s2, 31
	s_lshl_b64 s[24:25], s[2:3], 19
	s_add_u32 s24, s36, s24
	s_addc_u32 s25, s37, s25
	s_and_b64 s[26:27], s[22:23], exec
	s_cselect_b32 s3, s25, s11
	s_cselect_b32 s54, s24, s10
	s_ashr_i32 s21, s20, 31
	s_lshl_b64 s[26:27], s[20:21], 19
	s_add_u32 s26, s40, s26
	s_addc_u32 s27, s41, s27
	s_and_b64 s[34:35], s[22:23], exec
	s_cselect_b32 s21, s27, s31
	s_cselect_b32 s55, s26, s30
	s_add_u32 s10, s10, 0x80
	s_addc_u32 s11, s11, 0
	s_add_u32 s56, s30, 0x100
	v_mov_b32_e32 v32, 0
	s_addc_u32 s58, s31, 0
	s_mov_b32 s59, -2
	v_mov_b32_e32 v33, 0
	v_mov_b64_e32 v[34:35], 0
	v_mov_b64_e32 v[40:41], 0
	v_mov_b64_e32 v[42:43], 0
	v_mov_b64_e32 v[48:49], 0
	v_mov_b64_e32 v[50:51], 0
	v_mov_b64_e32 v[56:57], 0
	v_mov_b64_e32 v[58:59], 0
	v_mov_b64_e32 v[64:65], 0
	v_mov_b64_e32 v[66:67], 0
	v_mov_b64_e32 v[72:73], 0
	v_mov_b64_e32 v[74:75], 0
	v_mov_b64_e32 v[80:81], 0
	v_mov_b64_e32 v[82:83], 0
	v_mov_b64_e32 v[88:89], 0
	v_mov_b64_e32 v[90:91], 0
	v_mov_b64_e32 v[36:37], 0
	v_mov_b64_e32 v[38:39], 0
	v_mov_b64_e32 v[44:45], 0
	v_mov_b64_e32 v[46:47], 0
	v_mov_b64_e32 v[52:53], 0
	v_mov_b64_e32 v[54:55], 0
	v_mov_b64_e32 v[60:61], 0
	v_mov_b64_e32 v[62:63], 0
	v_mov_b64_e32 v[68:69], 0
	v_mov_b64_e32 v[70:71], 0
	v_mov_b64_e32 v[76:77], 0
	v_mov_b64_e32 v[78:79], 0
	v_mov_b64_e32 v[84:85], 0
	v_mov_b64_e32 v[86:87], 0
	v_mov_b64_e32 v[92:93], 0
	v_mov_b64_e32 v[94:95], 0
	v_mov_b64_e32 v[96:97], 0
	v_mov_b64_e32 v[98:99], 0
	v_mov_b64_e32 v[104:105], 0
	v_mov_b64_e32 v[106:107], 0
	v_mov_b64_e32 v[112:113], 0
	v_mov_b64_e32 v[114:115], 0
	v_mov_b64_e32 v[120:121], 0
	v_mov_b64_e32 v[122:123], 0
	v_mov_b64_e32 v[128:129], 0
	v_mov_b64_e32 v[130:131], 0
	v_mov_b64_e32 v[136:137], 0
	v_mov_b64_e32 v[138:139], 0
	v_mov_b64_e32 v[148:149], 0
	v_mov_b64_e32 v[150:151], 0
	v_mov_b64_e32 v[152:153], 0
	v_mov_b64_e32 v[154:155], 0
	v_mov_b64_e32 v[100:101], 0
	v_mov_b64_e32 v[102:103], 0
	v_mov_b64_e32 v[108:109], 0
	v_mov_b64_e32 v[110:111], 0
	v_mov_b64_e32 v[116:117], 0
	v_mov_b64_e32 v[118:119], 0
	v_mov_b64_e32 v[124:125], 0
	v_mov_b64_e32 v[126:127], 0
	v_mov_b64_e32 v[132:133], 0
	v_mov_b64_e32 v[134:135], 0
	v_mov_b64_e32 v[140:141], 0
	v_mov_b64_e32 v[142:143], 0
	v_mov_b64_e32 v[144:145], 0
	v_mov_b64_e32 v[146:147], 0
	v_mov_b64_e32 v[156:157], 0
	v_mov_b64_e32 v[158:159], 0

; template <class Epi, class Sched, class Prob>
; __device__ __forceinline__ void gemm_phase(LAS unsigned char* lds, LAS unsigned char* lds_epi, const Prob g, const Sched& S, const Epi& E, int wid) {
;     ...
;         const bool has_next = S.next(ui + 1, nxt);
;         const char* nA = has_next ? g.a_base(nxt) : cA; const char* nB = has_next ? g.b_base(nxt) : cB;
; _Pragma("clang loop unroll(disable)")
;         for (int t = 0; t < nt; t += 2) {
;             const bool last = (t == nt - 2);
;             const char* a1 = cA + (size_t)(t + 1) * kstep;
;             const char* a2 = last ? nA : cA + (size_t)(t + 2) * kstep; const char* b2 = last ? nB : cB + (size_t)(t + 2) * kstep;
.LBB0_1433:
	s_ashr_i32 s17, s16, 31
	s_lshl_b64 s[40:41], s[16:17], 20
	s_add_u32 s40, s58, s40
	s_addc_u32 s41, s59, s41
	s_and_b64 s[42:43], s[36:37], exec
	s_cselect_b32 s17, s41, s11
	s_cselect_b32 s52, s40, s10
	s_ashr_i32 s35, s34, 31
	s_lshl_b64 s[42:43], s[34:35], 20
	s_add_u32 s42, s60, s42
	s_addc_u32 s43, s61, s43
	s_and_b64 s[48:49], s[36:37], exec
	s_cselect_b32 s35, s43, s47
	s_cselect_b32 s53, s42, s46
	s_add_u32 s54, s46, 0x100
	v_mov_b32_e32 v0, 0
	s_addc_u32 s55, s47, 0
	s_mov_b32 s87, -2
	v_mov_b32_e32 v1, 0
	v_mov_b64_e32 v[2:3], 0
	v_mov_b64_e32 v[4:5], 0
	v_mov_b64_e32 v[6:7], 0
	v_mov_b64_e32 v[8:9], 0
	v_mov_b64_e32 v[10:11], 0
	v_mov_b64_e32 v[12:13], 0
	v_mov_b64_e32 v[14:15], 0
	v_mov_b64_e32 v[24:25], 0
	v_mov_b64_e32 v[26:27], 0
	v_mov_b64_e32 v[28:29], 0
	v_mov_b64_e32 v[30:31], 0
	v_mov_b64_e32 v[40:41], 0
	v_mov_b64_e32 v[42:43], 0
	v_mov_b64_e32 v[44:45], 0
	v_mov_b64_e32 v[46:47], 0
	v_mov_b64_e32 v[16:17], 0
	v_mov_b64_e32 v[18:19], 0
	v_mov_b64_e32 v[20:21], 0
	v_mov_b64_e32 v[22:23], 0
	v_mov_b64_e32 v[32:33], 0
	v_mov_b64_e32 v[34:35], 0
	v_mov_b64_e32 v[36:37], 0
	v_mov_b64_e32 v[38:39], 0
	v_mov_b64_e32 v[48:49], 0
	v_mov_b64_e32 v[50:51], 0
	v_mov_b64_e32 v[52:53], 0
	v_mov_b64_e32 v[54:55], 0
	v_mov_b64_e32 v[56:57], 0
	v_mov_b64_e32 v[58:59], 0
	v_mov_b64_e32 v[60:61], 0
	v_mov_b64_e32 v[62:63], 0
	v_mov_b64_e32 v[64:65], 0
	v_mov_b64_e32 v[66:67], 0
	v_mov_b64_e32 v[68:69], 0
	v_mov_b64_e32 v[70:71], 0
	v_mov_b64_e32 v[72:73], 0
	v_mov_b64_e32 v[74:75], 0
	v_mov_b64_e32 v[76:77], 0
	v_mov_b64_e32 v[78:79], 0
	v_mov_b64_e32 v[80:81], 0
	v_mov_b64_e32 v[82:83], 0
	v_mov_b64_e32 v[88:89], 0
	v_mov_b64_e32 v[90:91], 0
	v_mov_b64_e32 v[96:97], 0
	v_mov_b64_e32 v[98:99], 0
	v_mov_b64_e32 v[104:105], 0
	v_mov_b64_e32 v[106:107], 0
	v_mov_b64_e32 v[84:85], 0
	v_mov_b64_e32 v[86:87], 0
	v_mov_b64_e32 v[92:93], 0
	v_mov_b64_e32 v[94:95], 0
	v_mov_b64_e32 v[100:101], 0
	v_mov_b64_e32 v[102:103], 0
	v_mov_b64_e32 v[108:109], 0
	v_mov_b64_e32 v[110:111], 0
	v_mov_b64_e32 v[112:113], 0
	v_mov_b64_e32 v[114:115], 0
	v_mov_b64_e32 v[116:117], 0
	v_mov_b64_e32 v[118:119], 0
	v_mov_b64_e32 v[120:121], 0
	v_mov_b64_e32 v[122:123], 0
	v_mov_b64_e32 v[124:125], 0
	v_mov_b64_e32 v[126:127], 0

; template <class Epi, class Sched, class Prob>
; __device__ __forceinline__ void gemm_phase(LAS unsigned char* lds, LAS unsigned char* lds_epi, const Prob g, const Sched& S, const Epi& E, int wid) {
;     ...
;         const bool has_next = S.next(ui + 1, nxt);
;         const char* nA = has_next ? g.a_base(nxt) : cA; const char* nB = has_next ? g.b_base(nxt) : cB;
.LBB0_1594:
	s_ashr_i32 s65, s64, 31
	s_lshl_b64 s[14:15], s[64:65], 20
	s_add_u32 s17, s40, s14
	s_addc_u32 s19, s41, s15
	s_ashr_i32 s14, s62, 1
	s_ashr_i32 s15, s14, 31
	s_lshl_b64 s[14:15], s[14:15], 9
	s_add_u32 s68, s17, s14
	s_addc_u32 s69, s19, s15
	s_and_b64 s[14:15], s[66:67], exec
	s_cselect_b32 s17, s69, s9
	s_cselect_b32 s19, s68, s8
	s_ashr_i32 s63, s62, 31
	s_lshl_b64 s[14:15], s[62:63], 17
	s_add_u32 s70, s33, s14
	s_addc_u32 s71, s76, s15
	s_and_b64 s[14:15], s[66:67], exec
	v_mov_b32_e32 v0, 0
	s_cselect_b32 s26, s71, s11
	s_cselect_b32 s27, s70, s10
	s_mov_b64 s[20:21], -1
	s_mov_b64 s[14:15], 0
	v_mov_b32_e32 v1, 0
	v_mov_b64_e32 v[2:3], 0
	v_mov_b64_e32 v[32:33], 0
	v_mov_b64_e32 v[34:35], 0
	v_mov_b64_e32 v[4:5], 0
	v_mov_b64_e32 v[6:7], 0
	v_mov_b64_e32 v[36:37], 0
	v_mov_b64_e32 v[38:39], 0
	v_mov_b64_e32 v[8:9], 0
	v_mov_b64_e32 v[10:11], 0
	v_mov_b64_e32 v[40:41], 0
	v_mov_b64_e32 v[42:43], 0
	v_mov_b64_e32 v[12:13], 0
	v_mov_b64_e32 v[14:15], 0
	v_mov_b64_e32 v[44:45], 0
	v_mov_b64_e32 v[46:47], 0
	v_mov_b64_e32 v[16:17], 0
	v_mov_b64_e32 v[18:19], 0
	v_mov_b64_e32 v[48:49], 0
	v_mov_b64_e32 v[50:51], 0
	v_mov_b64_e32 v[20:21], 0
	v_mov_b64_e32 v[22:23], 0
	v_mov_b64_e32 v[52:53], 0
	v_mov_b64_e32 v[54:55], 0
	v_mov_b64_e32 v[24:25], 0
	v_mov_b64_e32 v[26:27], 0
	v_mov_b64_e32 v[60:61], 0
	v_mov_b64_e32 v[62:63], 0
	v_mov_b64_e32 v[28:29], 0
	v_mov_b64_e32 v[30:31], 0
	v_mov_b64_e32 v[64:65], 0
	v_mov_b64_e32 v[66:67], 0
	v_mov_b64_e32 v[76:77], 0
	v_mov_b64_e32 v[78:79], 0
	v_mov_b64_e32 v[120:121], 0
	v_mov_b64_e32 v[122:123], 0
	v_mov_b64_e32 v[80:81], 0
	v_mov_b64_e32 v[82:83], 0
	v_mov_b64_e32 v[124:125], 0
	v_mov_b64_e32 v[126:127], 0
	v_mov_b64_e32 v[84:85], 0
	v_mov_b64_e32 v[86:87], 0
	v_mov_b64_e32 v[128:129], 0
	v_mov_b64_e32 v[130:131], 0
	v_mov_b64_e32 v[92:93], 0
	v_mov_b64_e32 v[94:95], 0
	v_mov_b64_e32 v[132:133], 0
	v_mov_b64_e32 v[134:135], 0
	v_mov_b64_e32 v[96:97], 0
	v_mov_b64_e32 v[98:99], 0
	v_mov_b64_e32 v[136:137], 0
	v_mov_b64_e32 v[138:139], 0
	v_mov_b64_e32 v[108:109], 0
	v_mov_b64_e32 v[110:111], 0
	v_mov_b64_e32 v[140:141], 0
	v_mov_b64_e32 v[142:143], 0
	v_mov_b64_e32 v[112:113], 0
	v_mov_b64_e32 v[114:115], 0
	v_mov_b64_e32 v[144:145], 0
	v_mov_b64_e32 v[146:147], 0
	v_mov_b64_e32 v[116:117], 0
	v_mov_b64_e32 v[118:119], 0
	v_mov_b64_e32 v[148:149], 0
	v_mov_b64_e32 v[150:151], 0

; #define LAS __attribute__((address_space(3)))
; __global__ void __launch_bounds__(NTHR, 2) fwd_kernel(Args args) {
;     ...
;         for (int c = wg; c < T / 64; c += G) {
;             if (tid < 8) lcnt[tid] = 0;
;             __syncthreads();
;             const int t0 = c * 64 + wave * 8;
;             float acc[8][8], ssq[8];
; #pragma unroll
;             for (int q = 0; q < 8; ++q) { ssq[q] = 0.f;
; #pragma unroll
;                 for (int e = 0; e < 8; ++e) acc[q][e] = 0.f; }
; #pragma unroll 2
;             for (int i = 0; i < 16; ++i) { const int k = 2 * lane + 128 * i; f32x2 rv[8]; unsigned xw[8];
; #pragma unroll
;                 for (int e = 0; e < 8; ++e) rv[e] = *(const LAS f32x2*)(Rg + e * DM + k);
; #pragma unroll
;                 for (int q = 0; q < 8; ++q) xw[q] = *(const unsigned*)(XB + (size_t)(t0 + q) * DM + k);
; #pragma unroll
;                 for (int q = 0; q < 8; ++q) { const float x0 = bflo(xw[q]), x1 = bfhi(xw[q]); ssq[q] += x0 * x0 + x1 * x1;
; #pragma unroll
;                     for (int e = 0; e < 8; ++e) acc[q][e] += x0 * rv[e].x + x1 * rv[e].y; } }
.Lr14_chunk:
	s_waitcnt vmcnt(0)
	v_cmp_gt_u32_e32 vcc, 8, v211
	s_and_saveexec_b64 s[2:3], vcc
	ds_write_b32 v229, v220
	s_mov_b64 exec, s[2:3]
	s_lshl_b32 s13, s12, 6
	s_add_i32 s13, s13, s33
	s_lshl_b32 s14, s13, 12
	s_add_u32 s40, s10, s14
	s_addc_u32 s41, s11, 0
	s_add_u32 s42, s40, 0x1000
	s_addc_u32 s43, s41, 0
	s_add_u32 s44, s42, 0x1000
	s_addc_u32 s45, s43, 0
	s_add_u32 s46, s44, 0x1000
	s_addc_u32 s47, s45, 0
	s_add_u32 s48, s46, 0x1000
	s_addc_u32 s49, s47, 0
	s_add_u32 s50, s48, 0x1000
	s_addc_u32 s51, s49, 0
	s_add_u32 s52, s50, 0x1000
	s_addc_u32 s53, s51, 0
	s_add_u32 s54, s52, 0x1000
	s_addc_u32 s55, s53, 0
	global_load_dwordx4 v[64:67], v208, s[40:41] offset:0
	global_load_dwordx4 v[68:71], v208, s[42:43] offset:0
	global_load_dwordx4 v[72:75], v208, s[44:45] offset:0
	global_load_dwordx4 v[76:79], v208, s[46:47] offset:0
	global_load_dwordx4 v[80:83], v208, s[48:49] offset:0
	global_load_dwordx4 v[84:87], v208, s[50:51] offset:0
	global_load_dwordx4 v[88:91], v208, s[52:53] offset:0
	global_load_dwordx4 v[92:95], v208, s[54:55] offset:0
	global_load_dwordx4 v[96:99], v208, s[40:41] offset:1024
	global_load_dwordx4 v[100:103], v208, s[42:43] offset:1024
	global_load_dwordx4 v[104:107], v208, s[44:45] offset:1024
	global_load_dwordx4 v[108:111], v208, s[46:47] offset:1024
	global_load_dwordx4 v[112:115], v208, s[48:49] offset:1024
	global_load_dwordx4 v[116:119], v208, s[50:51] offset:1024
	global_load_dwordx4 v[120:123], v208, s[52:53] offset:1024
	global_load_dwordx4 v[124:127], v208, s[54:55] offset:1024
	v_mov_b64_e32 v[0:1], 0
	v_mov_b64_e32 v[2:3], 0
	v_mov_b64_e32 v[4:5], 0
	v_mov_b64_e32 v[6:7], 0
	v_mov_b64_e32 v[8:9], 0
	v_mov_b64_e32 v[10:11], 0
	v_mov_b64_e32 v[12:13], 0
	v_mov_b64_e32 v[14:15], 0
	v_mov_b64_e32 v[16:17], 0
	v_mov_b64_e32 v[18:19], 0
	v_mov_b64_e32 v[20:21], 0
	v_mov_b64_e32 v[22:23], 0
	v_mov_b64_e32 v[24:25], 0
	v_mov_b64_e32 v[26:27], 0
	v_mov_b64_e32 v[28:29], 0
	v_mov_b64_e32 v[30:31], 0
	v_mov_b64_e32 v[32:33], 0
	v_mov_b64_e32 v[34:35], 0
	v_mov_b64_e32 v[36:37], 0
	v_mov_b64_e32 v[38:39], 0
	v_mov_b64_e32 v[40:41], 0
	v_mov_b64_e32 v[42:43], 0
	v_mov_b64_e32 v[44:45], 0
	v_mov_b64_e32 v[46:47], 0
	v_mov_b64_e32 v[48:49], 0
	v_mov_b64_e32 v[50:51], 0
	v_mov_b64_e32 v[52:53], 0
	v_mov_b64_e32 v[54:55], 0
	v_mov_b64_e32 v[56:57], 0
	v_mov_b64_e32 v[58:59], 0
	v_mov_b64_e32 v[60:61], 0
	v_mov_b64_e32 v[62:63], 0
	v_mov_b64_e32 v[192:193], 0
	v_mov_b64_e32 v[194:195], 0
	v_mov_b64_e32 v[196:197], 0
	v_mov_b64_e32 v[198:199], 0
	v_mov_b64_e32 v[200:201], 0
	v_mov_b64_e32 v[202:203], 0
	v_mov_b64_e32 v[204:205], 0
	v_mov_b64_e32 v[206:207], 0
	s_waitcnt lgkmcnt(0)
	s_barrier
	ds_read_b128 v[128:131], v208 offset:0
	ds_read_b128 v[132:135], v208 offset:1024
	ds_read_b128 v[136:139], v208 offset:2048
	ds_read_b128 v[140:143], v208 offset:3072
	ds_read_b128 v[144:147], v208 offset:4096
	ds_read_b128 v[148:151], v208 offset:5120
	ds_read_b128 v[152:155], v208 offset:6144
	ds_read_b128 v[156:159], v208 offset:7168
	ds_read_b128 v[160:163], v208 offset:8192
	ds_read_b128 v[164:167], v208 offset:9216
	ds_read_b128 v[168:171], v208 offset:10240
	ds_read_b128 v[172:175], v208 offset:11264
	ds_read_b128 v[176:179], v208 offset:12288
	ds_read_b128 v[180:183], v208 offset:13312
	ds_read_b128 v[184:187], v208 offset:14336
	ds_read_b128 v[188:191], v208 offset:15360
	s_waitcnt vmcnt(8)
	s_waitcnt lgkmcnt(0)
	v_lshlrev_b32_e32 v232, 16, v64
	v_and_b32_e32 v233, s15, v64
	v_lshlrev_b32_e32 v234, 16, v65
	v_and_b32_e32 v235, s15, v65
	v_lshlrev_b32_e32 v236, 16, v66
	v_and_b32_e32 v237, s15, v66
	v_lshlrev_b32_e32 v238, 16, v67
	v_and_b32_e32 v239, s15, v67
	v_pk_fma_f32 v[192:193], v[232:233], v[232:233], v[192:193]
	v_pk_fma_f32 v[192:193], v[234:235], v[234:235], v[192:193]
	v_pk_fma_f32 v[192:193], v[236:237], v[236:237], v[192:193]
	v_pk_fma_f32 v[192:193], v[238:239], v[238:239], v[192:193]
	v_pk_fma_f32 v[0:1], v[232:233], v[128:129], v[0:1] op_sel_hi:[0,1,1]
	v_pk_fma_f32 v[2:3], v[232:233], v[130:131], v[2:3] op_sel_hi:[0,1,1]
	v_pk_fma_f32 v[4:5], v[232:233], v[132:133], v[4:5] op_sel_hi:[0,1,1]
	v_pk_fma_f32 v[6:7], v[232:233], v[134:135], v[6:7] op_sel_hi:[0,1,1]
	v_pk_fma_f32 v[0:1], v[232:233], v[136:137], v[0:1] op_sel:[1,0,0] op_sel_hi:[1,1,1]
	v_pk_fma_f32 v[2:3], v[232:233], v[138:139], v[2:3] op_sel:[1,0,0] op_sel_hi:[1,1,1]
	v_pk_fma_f32 v[4:5], v[232:233], v[140:141], v[4:5] op_sel:[1,0,0] op_sel_hi:[1,1,1]
	v_pk_fma_f32 v[6:7], v[232:233], v[142:143], v[6:7] op_sel:[1,0,0] op_sel_hi:[1,1,1]
	v_pk_fma_f32 v[0:1], v[234:235], v[144:145], v[0:1] op_sel_hi:[0,1,1]
	v_pk_fma_f32 v[2:3], v[234:235], v[146:147], v[2:3] op_sel_hi:[0,1,1]
	v_pk_fma_f32 v[4:5], v[234:235], v[148:149], v[4:5] op_sel_hi:[0,1,1]
	v_pk_fma_f32 v[6:7], v[234:235], v[150:151], v[6:7] op_sel_hi:[0,1,1]
	v_pk_fma_f32 v[0:1], v[234:235], v[152:153], v[0:1] op_sel:[1,0,0] op_sel_hi:[1,1,1]
	v_pk_fma_f32 v[2:3], v[234:235], v[154:155], v[2:3] op_sel:[1,0,0] op_sel_hi:[1,1,1]
	v_pk_fma_f32 v[4:5], v[234:235], v[156:157], v[4:5] op_sel:[1,0,0] op_sel_hi:[1,1,1]
	v_pk_fma_f32 v[6:7], v[234:235], v[158:159], v[6:7] op_sel:[1,0,0] op_sel_hi:[1,1,1]
	v_pk_fma_f32 v[0:1], v[236:237], v[160:161], v[0:1] op_sel_hi:[0,1,1]
	v_pk_fma_f32 v[2:3], v[236:237], v[162:163], v[2:3] op_sel_hi:[0,1,1]
	v_pk_fma_f32 v[4:5], v[236:237], v[164:165], v[4:5] op_sel_hi:[0,1,1]
	v_pk_fma_f32 v[6:7], v[236:237], v[166:167], v[6:7] op_sel_hi:[0,1,1]
	v_pk_fma_f32 v[0:1], v[236:237], v[168:169], v[0:1] op_sel:[1,0,0] op_sel_hi:[1,1,1]
	v_pk_fma_f32 v[2:3], v[236:237], v[170:171], v[2:3] op_sel:[1,0,0] op_sel_hi:[1,1,1]
; #define LAS __attribute__((address_space(3)))
; __global__ void __launch_bounds__(NTHR, 2) fwd_kernel(Args args) {
;     ...
;             for (int i = 0; i < 16; ++i) { const int k = 2 * lane + 128 * i; f32x2 rv[8]; unsigned xw[8];
; #pragma unroll
;                 for (int e = 0; e < 8; ++e) rv[e] = *(const LAS f32x2*)(Rg + e * DM + k);
; #pragma unroll
;                 for (int q = 0; q < 8; ++q) xw[q] = *(const unsigned*)(XB + (size_t)(t0 + q) * DM + k);
; #pragma unroll
;                 for (int q = 0; q < 8; ++q) { const float x0 = bflo(xw[q]), x1 = bfhi(xw[q]); ssq[q] += x0 * x0 + x1 * x1;
; #pragma unroll
;                     for (int e = 0; e < 8; ++e) acc[q][e] += x0 * rv[e].x + x1 * rv[e].y; } }
	v_pk_fma_f32 v[4:5], v[236:237], v[172:173], v[4:5] op_sel:[1,0,0] op_sel_hi:[1,1,1]
	v_pk_fma_f32 v[6:7], v[236:237], v[174:175], v[6:7] op_sel:[1,0,0] op_sel_hi:[1,1,1]
	v_pk_fma_f32 v[0:1], v[238:239], v[176:177], v[0:1] op_sel_hi:[0,1,1]
	v_pk_fma_f32 v[2:3], v[238:239], v[178:179], v[2:3] op_sel_hi:[0,1,1]
	v_pk_fma_f32 v[4:5], v[238:239], v[180:181], v[4:5] op_sel_hi:[0,1,1]
	v_pk_fma_f32 v[6:7], v[238:239], v[182:183], v[6:7] op_sel_hi:[0,1,1]
	v_pk_fma_f32 v[0:1], v[238:239], v[184:185], v[0:1] op_sel:[1,0,0] op_sel_hi:[1,1,1]
	v_pk_fma_f32 v[2:3], v[238:239], v[186:187], v[2:3] op_sel:[1,0,0] op_sel_hi:[1,1,1]
	v_pk_fma_f32 v[4:5], v[238:239], v[188:189], v[4:5] op_sel:[1,0,0] op_sel_hi:[1,1,1]
	v_pk_fma_f32 v[6:7], v[238:239], v[190:191], v[6:7] op_sel:[1,0,0] op_sel_hi:[1,1,1]
	v_lshlrev_b32_e32 v232, 16, v68
	v_and_b32_e32 v233, s15, v68
	v_lshlrev_b32_e32 v234, 16, v69
	v_and_b32_e32 v235, s15, v69
	v_lshlrev_b32_e32 v236, 16, v70
	v_and_b32_e32 v237, s15, v70
	v_lshlrev_b32_e32 v238, 16, v71
	v_and_b32_e32 v239, s15, v71
	v_pk_fma_f32 v[194:195], v[232:233], v[232:233], v[194:195]
	v_pk_fma_f32 v[194:195], v[234:235], v[234:235], v[194:195]
	v_pk_fma_f32 v[194:195], v[236:237], v[236:237], v[194:195]
	v_pk_fma_f32 v[194:195], v[238:239], v[238:239], v[194:195]
	v_pk_fma_f32 v[8:9], v[232:233], v[128:129], v[8:9] op_sel_hi:[0,1,1]
	v_pk_fma_f32 v[10:11], v[232:233], v[130:131], v[10:11] op_sel_hi:[0,1,1]
	v_pk_fma_f32 v[12:13], v[232:233], v[132:133], v[12:13] op_sel_hi:[0,1,1]
	v_pk_fma_f32 v[14:15], v[232:233], v[134:135], v[14:15] op_sel_hi:[0,1,1]
	v_pk_fma_f32 v[8:9], v[232:233], v[136:137], v[8:9] op_sel:[1,0,0] op_sel_hi:[1,1,1]
	v_pk_fma_f32 v[10:11], v[232:233], v[138:139], v[10:11] op_sel:[1,0,0] op_sel_hi:[1,1,1]
	v_pk_fma_f32 v[12:13], v[232:233], v[140:141], v[12:13] op_sel:[1,0,0] op_sel_hi:[1,1,1]
	v_pk_fma_f32 v[14:15], v[232:233], v[142:143], v[14:15] op_sel:[1,0,0] op_sel_hi:[1,1,1]
	v_pk_fma_f32 v[8:9], v[234:235], v[144:145], v[8:9] op_sel_hi:[0,1,1]
	v_pk_fma_f32 v[10:11], v[234:235], v[146:147], v[10:11] op_sel_hi:[0,1,1]
	v_pk_fma_f32 v[12:13], v[234:235], v[148:149], v[12:13] op_sel_hi:[0,1,1]
	v_pk_fma_f32 v[14:15], v[234:235], v[150:151], v[14:15] op_sel_hi:[0,1,1]
	v_pk_fma_f32 v[8:9], v[234:235], v[152:153], v[8:9] op_sel:[1,0,0] op_sel_hi:[1,1,1]
	v_pk_fma_f32 v[10:11], v[234:235], v[154:155], v[10:11] op_sel:[1,0,0] op_sel_hi:[1,1,1]
	v_pk_fma_f32 v[12:13], v[234:235], v[156:157], v[12:13] op_sel:[1,0,0] op_sel_hi:[1,1,1]
	v_pk_fma_f32 v[14:15], v[234:235], v[158:159], v[14:15] op_sel:[1,0,0] op_sel_hi:[1,1,1]
	v_pk_fma_f32 v[8:9], v[236:237], v[160:161], v[8:9] op_sel_hi:[0,1,1]
	v_pk_fma_f32 v[10:11], v[236:237], v[162:163], v[10:11] op_sel_hi:[0,1,1]
	v_pk_fma_f32 v[12:13], v[236:237], v[164:165], v[12:13] op_sel_hi:[0,1,1]
	v_pk_fma_f32 v[14:15], v[236:237], v[166:167], v[14:15] op_sel_hi:[0,1,1]
	v_pk_fma_f32 v[8:9], v[236:237], v[168:169], v[8:9] op_sel:[1,0,0] op_sel_hi:[1,1,1]
	v_pk_fma_f32 v[10:11], v[236:237], v[170:171], v[10:11] op_sel:[1,0,0] op_sel_hi:[1,1,1]
	v_pk_fma_f32 v[12:13], v[236:237], v[172:173], v[12:13] op_sel:[1,0,0] op_sel_hi:[1,1,1]
	v_pk_fma_f32 v[14:15], v[236:237], v[174:175], v[14:15] op_sel:[1,0,0] op_sel_hi:[1,1,1]
	v_pk_fma_f32 v[8:9], v[238:239], v[176:177], v[8:9] op_sel_hi:[0,1,1]
	v_pk_fma_f32 v[10:11], v[238:239], v[178:179], v[10:11] op_sel_hi:[0,1,1]
	v_pk_fma_f32 v[12:13], v[238:239], v[180:181], v[12:13] op_sel_hi:[0,1,1]
	v_pk_fma_f32 v[14:15], v[238:239], v[182:183], v[14:15] op_sel_hi:[0,1,1]
	v_pk_fma_f32 v[8:9], v[238:239], v[184:185], v[8:9] op_sel:[1,0,0] op_sel_hi:[1,1,1]
	v_pk_fma_f32 v[10:11], v[238:239], v[186:187], v[10:11] op_sel:[1,0,0] op_sel_hi:[1,1,1]
	v_pk_fma_f32 v[12:13], v[238:239], v[188:189], v[12:13] op_sel:[1,0,0] op_sel_hi:[1,1,1]
	v_pk_fma_f32 v[14:15], v[238:239], v[190:191], v[14:15] op_sel:[1,0,0] op_sel_hi:[1,1,1]
	v_lshlrev_b32_e32 v232, 16, v72
	v_and_b32_e32 v233, s15, v72
	v_lshlrev_b32_e32 v234, 16, v73
	v_and_b32_e32 v235, s15, v73
	v_lshlrev_b32_e32 v236, 16, v74
	v_and_b32_e32 v237, s15, v74
	v_lshlrev_b32_e32 v238, 16, v75
	v_and_b32_e32 v239, s15, v75
	v_pk_fma_f32 v[196:197], v[232:233], v[232:233], v[196:197]
	v_pk_fma_f32 v[196:197], v[234:235], v[234:235], v[196:197]
	v_pk_fma_f32 v[196:197], v[236:237], v[236:237], v[196:197]
	v_pk_fma_f32 v[196:197], v[238:239], v[238:239], v[196:197]
	v_pk_fma_f32 v[16:17], v[232:233], v[128:129], v[16:17] op_sel_hi:[0,1,1]
	v_pk_fma_f32 v[18:19], v[232:233], v[130:131], v[18:19] op_sel_hi:[0,1,1]
	v_pk_fma_f32 v[20:21], v[232:233], v[132:133], v[20:21] op_sel_hi:[0,1,1]
	v_pk_fma_f32 v[22:23], v[232:233], v[134:135], v[22:23] op_sel_hi:[0,1,1]
	v_pk_fma_f32 v[16:17], v[232:233], v[136:137], v[16:17] op_sel:[1,0,0] op_sel_hi:[1,1,1]
	v_pk_fma_f32 v[18:19], v[232:233], v[138:139], v[18:19] op_sel:[1,0,0] op_sel_hi:[1,1,1]
	v_pk_fma_f32 v[20:21], v[232:233], v[140:141], v[20:21] op_sel:[1,0,0] op_sel_hi:[1,1,1]
	v_pk_fma_f32 v[22:23], v[232:233], v[142:143], v[22:23] op_sel:[1,0,0] op_sel_hi:[1,1,1]
	v_pk_fma_f32 v[16:17], v[234:235], v[144:145], v[16:17] op_sel_hi:[0,1,1]
	v_pk_fma_f32 v[18:19], v[234:235], v[146:147], v[18:19] op_sel_hi:[0,1,1]
	v_pk_fma_f32 v[20:21], v[234:235], v[148:149], v[20:21] op_sel_hi:[0,1,1]
	v_pk_fma_f32 v[22:23], v[234:235], v[150:151], v[22:23] op_sel_hi:[0,1,1]
	v_pk_fma_f32 v[16:17], v[234:235], v[152:153], v[16:17] op_sel:[1,0,0] op_sel_hi:[1,1,1]
	v_pk_fma_f32 v[18:19], v[234:235], v[154:155], v[18:19] op_sel:[1,0,0] op_sel_hi:[1,1,1]
	v_pk_fma_f32 v[20:21], v[234:235], v[156:157], v[20:21] op_sel:[1,0,0] op_sel_hi:[1,1,1]
; #define LAS __attribute__((address_space(3)))
; __global__ void __launch_bounds__(NTHR, 2) fwd_kernel(Args args) {
;     ...
;             for (int i = 0; i < 16; ++i) { const int k = 2 * lane + 128 * i; f32x2 rv[8]; unsigned xw[8];
; #pragma unroll
;                 for (int e = 0; e < 8; ++e) rv[e] = *(const LAS f32x2*)(Rg + e * DM + k);
; #pragma unroll
;                 for (int q = 0; q < 8; ++q) xw[q] = *(const unsigned*)(XB + (size_t)(t0 + q) * DM + k);
; #pragma unroll
;                 for (int q = 0; q < 8; ++q) { const float x0 = bflo(xw[q]), x1 = bfhi(xw[q]); ssq[q] += x0 * x0 + x1 * x1;
; #pragma unroll
;                     for (int e = 0; e < 8; ++e) acc[q][e] += x0 * rv[e].x + x1 * rv[e].y; } }
	v_pk_fma_f32 v[22:23], v[234:235], v[158:159], v[22:23] op_sel:[1,0,0] op_sel_hi:[1,1,1]
	v_pk_fma_f32 v[16:17], v[236:237], v[160:161], v[16:17] op_sel_hi:[0,1,1]
	v_pk_fma_f32 v[18:19], v[236:237], v[162:163], v[18:19] op_sel_hi:[0,1,1]
	v_pk_fma_f32 v[20:21], v[236:237], v[164:165], v[20:21] op_sel_hi:[0,1,1]
	v_pk_fma_f32 v[22:23], v[236:237], v[166:167], v[22:23] op_sel_hi:[0,1,1]
	v_pk_fma_f32 v[16:17], v[236:237], v[168:169], v[16:17] op_sel:[1,0,0] op_sel_hi:[1,1,1]
	v_pk_fma_f32 v[18:19], v[236:237], v[170:171], v[18:19] op_sel:[1,0,0] op_sel_hi:[1,1,1]
	v_pk_fma_f32 v[20:21], v[236:237], v[172:173], v[20:21] op_sel:[1,0,0] op_sel_hi:[1,1,1]
	v_pk_fma_f32 v[22:23], v[236:237], v[174:175], v[22:23] op_sel:[1,0,0] op_sel_hi:[1,1,1]
	v_pk_fma_f32 v[16:17], v[238:239], v[176:177], v[16:17] op_sel_hi:[0,1,1]
	v_pk_fma_f32 v[18:19], v[238:239], v[178:179], v[18:19] op_sel_hi:[0,1,1]
	v_pk_fma_f32 v[20:21], v[238:239], v[180:181], v[20:21] op_sel_hi:[0,1,1]
	v_pk_fma_f32 v[22:23], v[238:239], v[182:183], v[22:23] op_sel_hi:[0,1,1]
	v_pk_fma_f32 v[16:17], v[238:239], v[184:185], v[16:17] op_sel:[1,0,0] op_sel_hi:[1,1,1]
	v_pk_fma_f32 v[18:19], v[238:239], v[186:187], v[18:19] op_sel:[1,0,0] op_sel_hi:[1,1,1]
	v_pk_fma_f32 v[20:21], v[238:239], v[188:189], v[20:21] op_sel:[1,0,0] op_sel_hi:[1,1,1]
	v_pk_fma_f32 v[22:23], v[238:239], v[190:191], v[22:23] op_sel:[1,0,0] op_sel_hi:[1,1,1]
	v_lshlrev_b32_e32 v232, 16, v76
	v_and_b32_e32 v233, s15, v76
	v_lshlrev_b32_e32 v234, 16, v77
	v_and_b32_e32 v235, s15, v77
	v_lshlrev_b32_e32 v236, 16, v78
	v_and_b32_e32 v237, s15, v78
	v_lshlrev_b32_e32 v238, 16, v79
	v_and_b32_e32 v239, s15, v79
	v_pk_fma_f32 v[198:199], v[232:233], v[232:233], v[198:199]
	v_pk_fma_f32 v[198:199], v[234:235], v[234:235], v[198:199]
	v_pk_fma_f32 v[198:199], v[236:237], v[236:237], v[198:199]
	v_pk_fma_f32 v[198:199], v[238:239], v[238:239], v[198:199]
	v_pk_fma_f32 v[24:25], v[232:233], v[128:129], v[24:25] op_sel_hi:[0,1,1]
	v_pk_fma_f32 v[26:27], v[232:233], v[130:131], v[26:27] op_sel_hi:[0,1,1]
	v_pk_fma_f32 v[28:29], v[232:233], v[132:133], v[28:29] op_sel_hi:[0,1,1]
	v_pk_fma_f32 v[30:31], v[232:233], v[134:135], v[30:31] op_sel_hi:[0,1,1]
	v_pk_fma_f32 v[24:25], v[232:233], v[136:137], v[24:25] op_sel:[1,0,0] op_sel_hi:[1,1,1]
	v_pk_fma_f32 v[26:27], v[232:233], v[138:139], v[26:27] op_sel:[1,0,0] op_sel_hi:[1,1,1]
	v_pk_fma_f32 v[28:29], v[232:233], v[140:141], v[28:29] op_sel:[1,0,0] op_sel_hi:[1,1,1]
	v_pk_fma_f32 v[30:31], v[232:233], v[142:143], v[30:31] op_sel:[1,0,0] op_sel_hi:[1,1,1]
	v_pk_fma_f32 v[24:25], v[234:235], v[144:145], v[24:25] op_sel_hi:[0,1,1]
	v_pk_fma_f32 v[26:27], v[234:235], v[146:147], v[26:27] op_sel_hi:[0,1,1]
	v_pk_fma_f32 v[28:29], v[234:235], v[148:149], v[28:29] op_sel_hi:[0,1,1]
	v_pk_fma_f32 v[30:31], v[234:235], v[150:151], v[30:31] op_sel_hi:[0,1,1]
	v_pk_fma_f32 v[24:25], v[234:235], v[152:153], v[24:25] op_sel:[1,0,0] op_sel_hi:[1,1,1]
	v_pk_fma_f32 v[26:27], v[234:235], v[154:155], v[26:27] op_sel:[1,0,0] op_sel_hi:[1,1,1]
	v_pk_fma_f32 v[28:29], v[234:235], v[156:157], v[28:29] op_sel:[1,0,0] op_sel_hi:[1,1,1]
	v_pk_fma_f32 v[30:31], v[234:235], v[158:159], v[30:31] op_sel:[1,0,0] op_sel_hi:[1,1,1]
	v_pk_fma_f32 v[24:25], v[236:237], v[160:161], v[24:25] op_sel_hi:[0,1,1]
	v_pk_fma_f32 v[26:27], v[236:237], v[162:163], v[26:27] op_sel_hi:[0,1,1]
	v_pk_fma_f32 v[28:29], v[236:237], v[164:165], v[28:29] op_sel_hi:[0,1,1]
	v_pk_fma_f32 v[30:31], v[236:237], v[166:167], v[30:31] op_sel_hi:[0,1,1]
	v_pk_fma_f32 v[24:25], v[236:237], v[168:169], v[24:25] op_sel:[1,0,0] op_sel_hi:[1,1,1]
	v_pk_fma_f32 v[26:27], v[236:237], v[170:171], v[26:27] op_sel:[1,0,0] op_sel_hi:[1,1,1]
	v_pk_fma_f32 v[28:29], v[236:237], v[172:173], v[28:29] op_sel:[1,0,0] op_sel_hi:[1,1,1]
	v_pk_fma_f32 v[30:31], v[236:237], v[174:175], v[30:31] op_sel:[1,0,0] op_sel_hi:[1,1,1]
	v_pk_fma_f32 v[24:25], v[238:239], v[176:177], v[24:25] op_sel_hi:[0,1,1]
	v_pk_fma_f32 v[26:27], v[238:239], v[178:179], v[26:27] op_sel_hi:[0,1,1]
	v_pk_fma_f32 v[28:29], v[238:239], v[180:181], v[28:29] op_sel_hi:[0,1,1]
	v_pk_fma_f32 v[30:31], v[238:239], v[182:183], v[30:31] op_sel_hi:[0,1,1]
	v_pk_fma_f32 v[24:25], v[238:239], v[184:185], v[24:25] op_sel:[1,0,0] op_sel_hi:[1,1,1]
	v_pk_fma_f32 v[26:27], v[238:239], v[186:187], v[26:27] op_sel:[1,0,0] op_sel_hi:[1,1,1]
	v_pk_fma_f32 v[28:29], v[238:239], v[188:189], v[28:29] op_sel:[1,0,0] op_sel_hi:[1,1,1]
	v_pk_fma_f32 v[30:31], v[238:239], v[190:191], v[30:31] op_sel:[1,0,0] op_sel_hi:[1,1,1]
	v_lshlrev_b32_e32 v232, 16, v80
	v_and_b32_e32 v233, s15, v80
	v_lshlrev_b32_e32 v234, 16, v81
	v_and_b32_e32 v235, s15, v81
	v_lshlrev_b32_e32 v236, 16, v82
	v_and_b32_e32 v237, s15, v82
	v_lshlrev_b32_e32 v238, 16, v83
	v_and_b32_e32 v239, s15, v83
	v_pk_fma_f32 v[200:201], v[232:233], v[232:233], v[200:201]
	v_pk_fma_f32 v[200:201], v[234:235], v[234:235], v[200:201]
	v_pk_fma_f32 v[200:201], v[236:237], v[236:237], v[200:201]
	v_pk_fma_f32 v[200:201], v[238:239], v[238:239], v[200:201]
	v_pk_fma_f32 v[32:33], v[232:233], v[128:129], v[32:33] op_sel_hi:[0,1,1]
	v_pk_fma_f32 v[34:35], v[232:233], v[130:131], v[34:35] op_sel_hi:[0,1,1]
	v_pk_fma_f32 v[36:37], v[232:233], v[132:133], v[36:37] op_sel_hi:[0,1,1]
	v_pk_fma_f32 v[38:39], v[232:233], v[134:135], v[38:39] op_sel_hi:[0,1,1]
	v_pk_fma_f32 v[32:33], v[232:233], v[136:137], v[32:33] op_sel:[1,0,0] op_sel_hi:[1,1,1]
	v_pk_fma_f32 v[34:35], v[232:233], v[138:139], v[34:35] op_sel:[1,0,0] op_sel_hi:[1,1,1]
	v_pk_fma_f32 v[36:37], v[232:233], v[140:141], v[36:37] op_sel:[1,0,0] op_sel_hi:[1,1,1]
; #define LAS __attribute__((address_space(3)))
; __global__ void __launch_bounds__(NTHR, 2) fwd_kernel(Args args) {
;     ...
;             for (int i = 0; i < 16; ++i) { const int k = 2 * lane + 128 * i; f32x2 rv[8]; unsigned xw[8];
; #pragma unroll
;                 for (int e = 0; e < 8; ++e) rv[e] = *(const LAS f32x2*)(Rg + e * DM + k);
; #pragma unroll
;                 for (int q = 0; q < 8; ++q) xw[q] = *(const unsigned*)(XB + (size_t)(t0 + q) * DM + k);
; #pragma unroll
;                 for (int q = 0; q < 8; ++q) { const float x0 = bflo(xw[q]), x1 = bfhi(xw[q]); ssq[q] += x0 * x0 + x1 * x1;
; #pragma unroll
;                     for (int e = 0; e < 8; ++e) acc[q][e] += x0 * rv[e].x + x1 * rv[e].y; } }
	v_pk_fma_f32 v[38:39], v[232:233], v[142:143], v[38:39] op_sel:[1,0,0] op_sel_hi:[1,1,1]
	v_pk_fma_f32 v[32:33], v[234:235], v[144:145], v[32:33] op_sel_hi:[0,1,1]
	v_pk_fma_f32 v[34:35], v[234:235], v[146:147], v[34:35] op_sel_hi:[0,1,1]
	v_pk_fma_f32 v[36:37], v[234:235], v[148:149], v[36:37] op_sel_hi:[0,1,1]
	v_pk_fma_f32 v[38:39], v[234:235], v[150:151], v[38:39] op_sel_hi:[0,1,1]
	v_pk_fma_f32 v[32:33], v[234:235], v[152:153], v[32:33] op_sel:[1,0,0] op_sel_hi:[1,1,1]
	v_pk_fma_f32 v[34:35], v[234:235], v[154:155], v[34:35] op_sel:[1,0,0] op_sel_hi:[1,1,1]
	v_pk_fma_f32 v[36:37], v[234:235], v[156:157], v[36:37] op_sel:[1,0,0] op_sel_hi:[1,1,1]
	v_pk_fma_f32 v[38:39], v[234:235], v[158:159], v[38:39] op_sel:[1,0,0] op_sel_hi:[1,1,1]
	v_pk_fma_f32 v[32:33], v[236:237], v[160:161], v[32:33] op_sel_hi:[0,1,1]
	v_pk_fma_f32 v[34:35], v[236:237], v[162:163], v[34:35] op_sel_hi:[0,1,1]
	v_pk_fma_f32 v[36:37], v[236:237], v[164:165], v[36:37] op_sel_hi:[0,1,1]
	v_pk_fma_f32 v[38:39], v[236:237], v[166:167], v[38:39] op_sel_hi:[0,1,1]
	v_pk_fma_f32 v[32:33], v[236:237], v[168:169], v[32:33] op_sel:[1,0,0] op_sel_hi:[1,1,1]
	v_pk_fma_f32 v[34:35], v[236:237], v[170:171], v[34:35] op_sel:[1,0,0] op_sel_hi:[1,1,1]
	v_pk_fma_f32 v[36:37], v[236:237], v[172:173], v[36:37] op_sel:[1,0,0] op_sel_hi:[1,1,1]
	v_pk_fma_f32 v[38:39], v[236:237], v[174:175], v[38:39] op_sel:[1,0,0] op_sel_hi:[1,1,1]
	v_pk_fma_f32 v[32:33], v[238:239], v[176:177], v[32:33] op_sel_hi:[0,1,1]
	v_pk_fma_f32 v[34:35], v[238:239], v[178:179], v[34:35] op_sel_hi:[0,1,1]
	v_pk_fma_f32 v[36:37], v[238:239], v[180:181], v[36:37] op_sel_hi:[0,1,1]
	v_pk_fma_f32 v[38:39], v[238:239], v[182:183], v[38:39] op_sel_hi:[0,1,1]
	v_pk_fma_f32 v[32:33], v[238:239], v[184:185], v[32:33] op_sel:[1,0,0] op_sel_hi:[1,1,1]
	v_pk_fma_f32 v[34:35], v[238:239], v[186:187], v[34:35] op_sel:[1,0,0] op_sel_hi:[1,1,1]
	v_pk_fma_f32 v[36:37], v[238:239], v[188:189], v[36:37] op_sel:[1,0,0] op_sel_hi:[1,1,1]
	v_pk_fma_f32 v[38:39], v[238:239], v[190:191], v[38:39] op_sel:[1,0,0] op_sel_hi:[1,1,1]
	v_lshlrev_b32_e32 v232, 16, v84
	v_and_b32_e32 v233, s15, v84
	v_lshlrev_b32_e32 v234, 16, v85
	v_and_b32_e32 v235, s15, v85
	v_lshlrev_b32_e32 v236, 16, v86
	v_and_b32_e32 v237, s15, v86
	v_lshlrev_b32_e32 v238, 16, v87
	v_and_b32_e32 v239, s15, v87
	v_pk_fma_f32 v[202:203], v[232:233], v[232:233], v[202:203]
	v_pk_fma_f32 v[202:203], v[234:235], v[234:235], v[202:203]
	v_pk_fma_f32 v[202:203], v[236:237], v[236:237], v[202:203]
	v_pk_fma_f32 v[202:203], v[238:239], v[238:239], v[202:203]
	v_pk_fma_f32 v[40:41], v[232:233], v[128:129], v[40:41] op_sel_hi:[0,1,1]
	v_pk_fma_f32 v[42:43], v[232:233], v[130:131], v[42:43] op_sel_hi:[0,1,1]
	v_pk_fma_f32 v[44:45], v[232:233], v[132:133], v[44:45] op_sel_hi:[0,1,1]
	v_pk_fma_f32 v[46:47], v[232:233], v[134:135], v[46:47] op_sel_hi:[0,1,1]
	v_pk_fma_f32 v[40:41], v[232:233], v[136:137], v[40:41] op_sel:[1,0,0] op_sel_hi:[1,1,1]
	v_pk_fma_f32 v[42:43], v[232:233], v[138:139], v[42:43] op_sel:[1,0,0] op_sel_hi:[1,1,1]
	v_pk_fma_f32 v[44:45], v[232:233], v[140:141], v[44:45] op_sel:[1,0,0] op_sel_hi:[1,1,1]
	v_pk_fma_f32 v[46:47], v[232:233], v[142:143], v[46:47] op_sel:[1,0,0] op_sel_hi:[1,1,1]
	v_pk_fma_f32 v[40:41], v[234:235], v[144:145], v[40:41] op_sel_hi:[0,1,1]
	v_pk_fma_f32 v[42:43], v[234:235], v[146:147], v[42:43] op_sel_hi:[0,1,1]
	v_pk_fma_f32 v[44:45], v[234:235], v[148:149], v[44:45] op_sel_hi:[0,1,1]
	v_pk_fma_f32 v[46:47], v[234:235], v[150:151], v[46:47] op_sel_hi:[0,1,1]
	v_pk_fma_f32 v[40:41], v[234:235], v[152:153], v[40:41] op_sel:[1,0,0] op_sel_hi:[1,1,1]
	v_pk_fma_f32 v[42:43], v[234:235], v[154:155], v[42:43] op_sel:[1,0,0] op_sel_hi:[1,1,1]
	v_pk_fma_f32 v[44:45], v[234:235], v[156:157], v[44:45] op_sel:[1,0,0] op_sel_hi:[1,1,1]
	v_pk_fma_f32 v[46:47], v[234:235], v[158:159], v[46:47] op_sel:[1,0,0] op_sel_hi:[1,1,1]
	v_pk_fma_f32 v[40:41], v[236:237], v[160:161], v[40:41] op_sel_hi:[0,1,1]
	v_pk_fma_f32 v[42:43], v[236:237], v[162:163], v[42:43] op_sel_hi:[0,1,1]
	v_pk_fma_f32 v[44:45], v[236:237], v[164:165], v[44:45] op_sel_hi:[0,1,1]
	v_pk_fma_f32 v[46:47], v[236:237], v[166:167], v[46:47] op_sel_hi:[0,1,1]
	v_pk_fma_f32 v[40:41], v[236:237], v[168:169], v[40:41] op_sel:[1,0,0] op_sel_hi:[1,1,1]
	v_pk_fma_f32 v[42:43], v[236:237], v[170:171], v[42:43] op_sel:[1,0,0] op_sel_hi:[1,1,1]
	v_pk_fma_f32 v[44:45], v[236:237], v[172:173], v[44:45] op_sel:[1,0,0] op_sel_hi:[1,1,1]
	v_pk_fma_f32 v[46:47], v[236:237], v[174:175], v[46:47] op_sel:[1,0,0] op_sel_hi:[1,1,1]
	v_pk_fma_f32 v[40:41], v[238:239], v[176:177], v[40:41] op_sel_hi:[0,1,1]
	v_pk_fma_f32 v[42:43], v[238:239], v[178:179], v[42:43] op_sel_hi:[0,1,1]
	v_pk_fma_f32 v[44:45], v[238:239], v[180:181], v[44:45] op_sel_hi:[0,1,1]
	v_pk_fma_f32 v[46:47], v[238:239], v[182:183], v[46:47] op_sel_hi:[0,1,1]
	v_pk_fma_f32 v[40:41], v[238:239], v[184:185], v[40:41] op_sel:[1,0,0] op_sel_hi:[1,1,1]
	v_pk_fma_f32 v[42:43], v[238:239], v[186:187], v[42:43] op_sel:[1,0,0] op_sel_hi:[1,1,1]
	v_pk_fma_f32 v[44:45], v[238:239], v[188:189], v[44:45] op_sel:[1,0,0] op_sel_hi:[1,1,1]
	v_pk_fma_f32 v[46:47], v[238:239], v[190:191], v[46:47] op_sel:[1,0,0] op_sel_hi:[1,1,1]
	v_lshlrev_b32_e32 v232, 16, v88
	v_and_b32_e32 v233, s15, v88
	v_lshlrev_b32_e32 v234, 16, v89
	v_and_b32_e32 v235, s15, v89
	v_lshlrev_b32_e32 v236, 16, v90
	v_and_b32_e32 v237, s15, v90
	v_lshlrev_b32_e32 v238, 16, v91
	v_and_b32_e32 v239, s15, v91
	v_pk_fma_f32 v[204:205], v[232:233], v[232:233], v[204:205]
	v_pk_fma_f32 v[204:205], v[234:235], v[234:235], v[204:205]
	v_pk_fma_f32 v[204:205], v[236:237], v[236:237], v[204:205]
; #define LAS __attribute__((address_space(3)))
; __global__ void __launch_bounds__(NTHR, 2) fwd_kernel(Args args) {
;     ...
;             for (int i = 0; i < 16; ++i) { const int k = 2 * lane + 128 * i; f32x2 rv[8]; unsigned xw[8];
; #pragma unroll
;                 for (int e = 0; e < 8; ++e) rv[e] = *(const LAS f32x2*)(Rg + e * DM + k);
; #pragma unroll
;                 for (int q = 0; q < 8; ++q) xw[q] = *(const unsigned*)(XB + (size_t)(t0 + q) * DM + k);
; #pragma unroll
;                 for (int q = 0; q < 8; ++q) { const float x0 = bflo(xw[q]), x1 = bfhi(xw[q]); ssq[q] += x0 * x0 + x1 * x1;
; #pragma unroll
;                     for (int e = 0; e < 8; ++e) acc[q][e] += x0 * rv[e].x + x1 * rv[e].y; } }
	v_pk_fma_f32 v[204:205], v[238:239], v[238:239], v[204:205]
	v_pk_fma_f32 v[48:49], v[232:233], v[128:129], v[48:49] op_sel_hi:[0,1,1]
	v_pk_fma_f32 v[50:51], v[232:233], v[130:131], v[50:51] op_sel_hi:[0,1,1]
	v_pk_fma_f32 v[52:53], v[232:233], v[132:133], v[52:53] op_sel_hi:[0,1,1]
	v_pk_fma_f32 v[54:55], v[232:233], v[134:135], v[54:55] op_sel_hi:[0,1,1]
	v_pk_fma_f32 v[48:49], v[232:233], v[136:137], v[48:49] op_sel:[1,0,0] op_sel_hi:[1,1,1]
	v_pk_fma_f32 v[50:51], v[232:233], v[138:139], v[50:51] op_sel:[1,0,0] op_sel_hi:[1,1,1]
	v_pk_fma_f32 v[52:53], v[232:233], v[140:141], v[52:53] op_sel:[1,0,0] op_sel_hi:[1,1,1]
	v_pk_fma_f32 v[54:55], v[232:233], v[142:143], v[54:55] op_sel:[1,0,0] op_sel_hi:[1,1,1]
	v_pk_fma_f32 v[48:49], v[234:235], v[144:145], v[48:49] op_sel_hi:[0,1,1]
	v_pk_fma_f32 v[50:51], v[234:235], v[146:147], v[50:51] op_sel_hi:[0,1,1]
	v_pk_fma_f32 v[52:53], v[234:235], v[148:149], v[52:53] op_sel_hi:[0,1,1]
	v_pk_fma_f32 v[54:55], v[234:235], v[150:151], v[54:55] op_sel_hi:[0,1,1]
	v_pk_fma_f32 v[48:49], v[234:235], v[152:153], v[48:49] op_sel:[1,0,0] op_sel_hi:[1,1,1]
	v_pk_fma_f32 v[50:51], v[234:235], v[154:155], v[50:51] op_sel:[1,0,0] op_sel_hi:[1,1,1]
	v_pk_fma_f32 v[52:53], v[234:235], v[156:157], v[52:53] op_sel:[1,0,0] op_sel_hi:[1,1,1]
	v_pk_fma_f32 v[54:55], v[234:235], v[158:159], v[54:55] op_sel:[1,0,0] op_sel_hi:[1,1,1]
	v_pk_fma_f32 v[48:49], v[236:237], v[160:161], v[48:49] op_sel_hi:[0,1,1]
	v_pk_fma_f32 v[50:51], v[236:237], v[162:163], v[50:51] op_sel_hi:[0,1,1]
	v_pk_fma_f32 v[52:53], v[236:237], v[164:165], v[52:53] op_sel_hi:[0,1,1]
	v_pk_fma_f32 v[54:55], v[236:237], v[166:167], v[54:55] op_sel_hi:[0,1,1]
	v_pk_fma_f32 v[48:49], v[236:237], v[168:169], v[48:49] op_sel:[1,0,0] op_sel_hi:[1,1,1]
	v_pk_fma_f32 v[50:51], v[236:237], v[170:171], v[50:51] op_sel:[1,0,0] op_sel_hi:[1,1,1]
	v_pk_fma_f32 v[52:53], v[236:237], v[172:173], v[52:53] op_sel:[1,0,0] op_sel_hi:[1,1,1]
	v_pk_fma_f32 v[54:55], v[236:237], v[174:175], v[54:55] op_sel:[1,0,0] op_sel_hi:[1,1,1]
	v_pk_fma_f32 v[48:49], v[238:239], v[176:177], v[48:49] op_sel_hi:[0,1,1]
	v_pk_fma_f32 v[50:51], v[238:239], v[178:179], v[50:51] op_sel_hi:[0,1,1]
	v_pk_fma_f32 v[52:53], v[238:239], v[180:181], v[52:53] op_sel_hi:[0,1,1]
	v_pk_fma_f32 v[54:55], v[238:239], v[182:183], v[54:55] op_sel_hi:[0,1,1]
	v_pk_fma_f32 v[48:49], v[238:239], v[184:185], v[48:49] op_sel:[1,0,0] op_sel_hi:[1,1,1]
	v_pk_fma_f32 v[50:51], v[238:239], v[186:187], v[50:51] op_sel:[1,0,0] op_sel_hi:[1,1,1]
	v_pk_fma_f32 v[52:53], v[238:239], v[188:189], v[52:53] op_sel:[1,0,0] op_sel_hi:[1,1,1]
	v_pk_fma_f32 v[54:55], v[238:239], v[190:191], v[54:55] op_sel:[1,0,0] op_sel_hi:[1,1,1]
	v_lshlrev_b32_e32 v232, 16, v92
	v_and_b32_e32 v233, s15, v92
	v_lshlrev_b32_e32 v234, 16, v93
	v_and_b32_e32 v235, s15, v93
	v_lshlrev_b32_e32 v236, 16, v94
	v_and_b32_e32 v237, s15, v94
	v_lshlrev_b32_e32 v238, 16, v95
	v_and_b32_e32 v239, s15, v95
	v_pk_fma_f32 v[206:207], v[232:233], v[232:233], v[206:207]
	v_pk_fma_f32 v[206:207], v[234:235], v[234:235], v[206:207]
	v_pk_fma_f32 v[206:207], v[236:237], v[236:237], v[206:207]
	v_pk_fma_f32 v[206:207], v[238:239], v[238:239], v[206:207]
	v_pk_fma_f32 v[56:57], v[232:233], v[128:129], v[56:57] op_sel_hi:[0,1,1]
	v_pk_fma_f32 v[58:59], v[232:233], v[130:131], v[58:59] op_sel_hi:[0,1,1]
	v_pk_fma_f32 v[60:61], v[232:233], v[132:133], v[60:61] op_sel_hi:[0,1,1]
	v_pk_fma_f32 v[62:63], v[232:233], v[134:135], v[62:63] op_sel_hi:[0,1,1]
	v_pk_fma_f32 v[56:57], v[232:233], v[136:137], v[56:57] op_sel:[1,0,0] op_sel_hi:[1,1,1]
	v_pk_fma_f32 v[58:59], v[232:233], v[138:139], v[58:59] op_sel:[1,0,0] op_sel_hi:[1,1,1]
	v_pk_fma_f32 v[60:61], v[232:233], v[140:141], v[60:61] op_sel:[1,0,0] op_sel_hi:[1,1,1]
	v_pk_fma_f32 v[62:63], v[232:233], v[142:143], v[62:63] op_sel:[1,0,0] op_sel_hi:[1,1,1]
	v_pk_fma_f32 v[56:57], v[234:235], v[144:145], v[56:57] op_sel_hi:[0,1,1]
	v_pk_fma_f32 v[58:59], v[234:235], v[146:147], v[58:59] op_sel_hi:[0,1,1]
	v_pk_fma_f32 v[60:61], v[234:235], v[148:149], v[60:61] op_sel_hi:[0,1,1]
	v_pk_fma_f32 v[62:63], v[234:235], v[150:151], v[62:63] op_sel_hi:[0,1,1]
	v_pk_fma_f32 v[56:57], v[234:235], v[152:153], v[56:57] op_sel:[1,0,0] op_sel_hi:[1,1,1]
	v_pk_fma_f32 v[58:59], v[234:235], v[154:155], v[58:59] op_sel:[1,0,0] op_sel_hi:[1,1,1]
	v_pk_fma_f32 v[60:61], v[234:235], v[156:157], v[60:61] op_sel:[1,0,0] op_sel_hi:[1,1,1]
	v_pk_fma_f32 v[62:63], v[234:235], v[158:159], v[62:63] op_sel:[1,0,0] op_sel_hi:[1,1,1]
	v_pk_fma_f32 v[56:57], v[236:237], v[160:161], v[56:57] op_sel_hi:[0,1,1]
	v_pk_fma_f32 v[58:59], v[236:237], v[162:163], v[58:59] op_sel_hi:[0,1,1]
	v_pk_fma_f32 v[60:61], v[236:237], v[164:165], v[60:61] op_sel_hi:[0,1,1]
	v_pk_fma_f32 v[62:63], v[236:237], v[166:167], v[62:63] op_sel_hi:[0,1,1]
	v_pk_fma_f32 v[56:57], v[236:237], v[168:169], v[56:57] op_sel:[1,0,0] op_sel_hi:[1,1,1]
	v_pk_fma_f32 v[58:59], v[236:237], v[170:171], v[58:59] op_sel:[1,0,0] op_sel_hi:[1,1,1]
	v_pk_fma_f32 v[60:61], v[236:237], v[172:173], v[60:61] op_sel:[1,0,0] op_sel_hi:[1,1,1]
	v_pk_fma_f32 v[62:63], v[236:237], v[174:175], v[62:63] op_sel:[1,0,0] op_sel_hi:[1,1,1]
	v_pk_fma_f32 v[56:57], v[238:239], v[176:177], v[56:57] op_sel_hi:[0,1,1]
	v_pk_fma_f32 v[58:59], v[238:239], v[178:179], v[58:59] op_sel_hi:[0,1,1]
	v_pk_fma_f32 v[60:61], v[238:239], v[180:181], v[60:61] op_sel_hi:[0,1,1]
	v_pk_fma_f32 v[62:63], v[238:239], v[182:183], v[62:63] op_sel_hi:[0,1,1]
	v_pk_fma_f32 v[56:57], v[238:239], v[184:185], v[56:57] op_sel:[1,0,0] op_sel_hi:[1,1,1]
	v_pk_fma_f32 v[58:59], v[238:239], v[186:187], v[58:59] op_sel:[1,0,0] op_sel_hi:[1,1,1]
	v_pk_fma_f32 v[60:61], v[238:239], v[188:189], v[60:61] op_sel:[1,0,0] op_sel_hi:[1,1,1]
	v_pk_fma_f32 v[62:63], v[238:239], v[190:191], v[62:63] op_sel:[1,0,0] op_sel_hi:[1,1,1]
	global_load_dwordx4 v[64:67], v208, s[40:41] offset:2048
	global_load_dwordx4 v[68:71], v208, s[42:43] offset:2048
	global_load_dwordx4 v[72:75], v208, s[44:45] offset:2048
	global_load_dwordx4 v[76:79], v208, s[46:47] offset:2048
	global_load_dwordx4 v[80:83], v208, s[48:49] offset:2048
	global_load_dwordx4 v[84:87], v208, s[50:51] offset:2048
	global_load_dwordx4 v[88:91], v208, s[52:53] offset:2048
	global_load_dwordx4 v[92:95], v208, s[54:55] offset:2048
	ds_read_b128 v[128:131], v208 offset:16384
	ds_read_b128 v[132:135], v208 offset:17408
	ds_read_b128 v[136:139], v208 offset:18432
	ds_read_b128 v[140:143], v208 offset:19456
	ds_read_b128 v[144:147], v208 offset:20480
	ds_read_b128 v[148:151], v208 offset:21504
	ds_read_b128 v[152:155], v208 offset:22528
	ds_read_b128 v[156:159], v208 offset:23552
	ds_read_b128 v[160:163], v208 offset:24576
	ds_read_b128 v[164:167], v208 offset:25600
	ds_read_b128 v[168:171], v208 offset:26624
	ds_read_b128 v[172:175], v208 offset:27648
	ds_read_b128 v[176:179], v208 offset:28672
	ds_read_b128 v[180:183], v208 offset:29696
	ds_read_b128 v[184:187], v208 offset:30720
	ds_read_b128 v[188:191], v208 offset:31744
	s_waitcnt vmcnt(8)
; #define LAS __attribute__((address_space(3)))
; __global__ void __launch_bounds__(NTHR, 2) fwd_kernel(Args args) {
;     ...
;             for (int i = 0; i < 16; ++i) { const int k = 2 * lane + 128 * i; f32x2 rv[8]; unsigned xw[8];
; #pragma unroll
;                 for (int e = 0; e < 8; ++e) rv[e] = *(const LAS f32x2*)(Rg + e * DM + k);
; #pragma unroll
;                 for (int q = 0; q < 8; ++q) xw[q] = *(const unsigned*)(XB + (size_t)(t0 + q) * DM + k);
; #pragma unroll
;                 for (int q = 0; q < 8; ++q) { const float x0 = bflo(xw[q]), x1 = bfhi(xw[q]); ssq[q] += x0 * x0 + x1 * x1;
; #pragma unroll
;                     for (int e = 0; e < 8; ++e) acc[q][e] += x0 * rv[e].x + x1 * rv[e].y; } }
	s_waitcnt lgkmcnt(0)
	v_lshlrev_b32_e32 v232, 16, v96
	v_and_b32_e32 v233, s15, v96
	v_lshlrev_b32_e32 v234, 16, v97
	v_and_b32_e32 v235, s15, v97
	v_lshlrev_b32_e32 v236, 16, v98
	v_and_b32_e32 v237, s15, v98
	v_lshlrev_b32_e32 v238, 16, v99
	v_and_b32_e32 v239, s15, v99
	v_pk_fma_f32 v[192:193], v[232:233], v[232:233], v[192:193]
	v_pk_fma_f32 v[192:193], v[234:235], v[234:235], v[192:193]
	v_pk_fma_f32 v[192:193], v[236:237], v[236:237], v[192:193]
	v_pk_fma_f32 v[192:193], v[238:239], v[238:239], v[192:193]
	v_pk_fma_f32 v[0:1], v[232:233], v[128:129], v[0:1] op_sel_hi:[0,1,1]
	v_pk_fma_f32 v[2:3], v[232:233], v[130:131], v[2:3] op_sel_hi:[0,1,1]
	v_pk_fma_f32 v[4:5], v[232:233], v[132:133], v[4:5] op_sel_hi:[0,1,1]
	v_pk_fma_f32 v[6:7], v[232:233], v[134:135], v[6:7] op_sel_hi:[0,1,1]
	v_pk_fma_f32 v[0:1], v[232:233], v[136:137], v[0:1] op_sel:[1,0,0] op_sel_hi:[1,1,1]
	v_pk_fma_f32 v[2:3], v[232:233], v[138:139], v[2:3] op_sel:[1,0,0] op_sel_hi:[1,1,1]
	v_pk_fma_f32 v[4:5], v[232:233], v[140:141], v[4:5] op_sel:[1,0,0] op_sel_hi:[1,1,1]
	v_pk_fma_f32 v[6:7], v[232:233], v[142:143], v[6:7] op_sel:[1,0,0] op_sel_hi:[1,1,1]
	v_pk_fma_f32 v[0:1], v[234:235], v[144:145], v[0:1] op_sel_hi:[0,1,1]
	v_pk_fma_f32 v[2:3], v[234:235], v[146:147], v[2:3] op_sel_hi:[0,1,1]
	v_pk_fma_f32 v[4:5], v[234:235], v[148:149], v[4:5] op_sel_hi:[0,1,1]
	v_pk_fma_f32 v[6:7], v[234:235], v[150:151], v[6:7] op_sel_hi:[0,1,1]
	v_pk_fma_f32 v[0:1], v[234:235], v[152:153], v[0:1] op_sel:[1,0,0] op_sel_hi:[1,1,1]
	v_pk_fma_f32 v[2:3], v[234:235], v[154:155], v[2:3] op_sel:[1,0,0] op_sel_hi:[1,1,1]
	v_pk_fma_f32 v[4:5], v[234:235], v[156:157], v[4:5] op_sel:[1,0,0] op_sel_hi:[1,1,1]
	v_pk_fma_f32 v[6:7], v[234:235], v[158:159], v[6:7] op_sel:[1,0,0] op_sel_hi:[1,1,1]
	v_pk_fma_f32 v[0:1], v[236:237], v[160:161], v[0:1] op_sel_hi:[0,1,1]
	v_pk_fma_f32 v[2:3], v[236:237], v[162:163], v[2:3] op_sel_hi:[0,1,1]
	v_pk_fma_f32 v[4:5], v[236:237], v[164:165], v[4:5] op_sel_hi:[0,1,1]
	v_pk_fma_f32 v[6:7], v[236:237], v[166:167], v[6:7] op_sel_hi:[0,1,1]
	v_pk_fma_f32 v[0:1], v[236:237], v[168:169], v[0:1] op_sel:[1,0,0] op_sel_hi:[1,1,1]
	v_pk_fma_f32 v[2:3], v[236:237], v[170:171], v[2:3] op_sel:[1,0,0] op_sel_hi:[1,1,1]
	v_pk_fma_f32 v[4:5], v[236:237], v[172:173], v[4:5] op_sel:[1,0,0] op_sel_hi:[1,1,1]
	v_pk_fma_f32 v[6:7], v[236:237], v[174:175], v[6:7] op_sel:[1,0,0] op_sel_hi:[1,1,1]
	v_pk_fma_f32 v[0:1], v[238:239], v[176:177], v[0:1] op_sel_hi:[0,1,1]
	v_pk_fma_f32 v[2:3], v[238:239], v[178:179], v[2:3] op_sel_hi:[0,1,1]
	v_pk_fma_f32 v[4:5], v[238:239], v[180:181], v[4:5] op_sel_hi:[0,1,1]
	v_pk_fma_f32 v[6:7], v[238:239], v[182:183], v[6:7] op_sel_hi:[0,1,1]
	v_pk_fma_f32 v[0:1], v[238:239], v[184:185], v[0:1] op_sel:[1,0,0] op_sel_hi:[1,1,1]
	v_pk_fma_f32 v[2:3], v[238:239], v[186:187], v[2:3] op_sel:[1,0,0] op_sel_hi:[1,1,1]
	v_pk_fma_f32 v[4:5], v[238:239], v[188:189], v[4:5] op_sel:[1,0,0] op_sel_hi:[1,1,1]
	v_pk_fma_f32 v[6:7], v[238:239], v[190:191], v[6:7] op_sel:[1,0,0] op_sel_hi:[1,1,1]
	v_lshlrev_b32_e32 v232, 16, v100
	v_and_b32_e32 v233, s15, v100
	v_lshlrev_b32_e32 v234, 16, v101
	v_and_b32_e32 v235, s15, v101
	v_lshlrev_b32_e32 v236, 16, v102
	v_and_b32_e32 v237, s15, v102
	v_lshlrev_b32_e32 v238, 16, v103
	v_and_b32_e32 v239, s15, v103
	v_pk_fma_f32 v[194:195], v[232:233], v[232:233], v[194:195]
	v_pk_fma_f32 v[194:195], v[234:235], v[234:235], v[194:195]
	v_pk_fma_f32 v[194:195], v[236:237], v[236:237], v[194:195]
	v_pk_fma_f32 v[194:195], v[238:239], v[238:239], v[194:195]
	v_pk_fma_f32 v[8:9], v[232:233], v[128:129], v[8:9] op_sel_hi:[0,1,1]
	v_pk_fma_f32 v[10:11], v[232:233], v[130:131], v[10:11] op_sel_hi:[0,1,1]
	v_pk_fma_f32 v[12:13], v[232:233], v[132:133], v[12:13] op_sel_hi:[0,1,1]
	v_pk_fma_f32 v[14:15], v[232:233], v[134:135], v[14:15] op_sel_hi:[0,1,1]
	v_pk_fma_f32 v[8:9], v[232:233], v[136:137], v[8:9] op_sel:[1,0,0] op_sel_hi:[1,1,1]
	v_pk_fma_f32 v[10:11], v[232:233], v[138:139], v[10:11] op_sel:[1,0,0] op_sel_hi:[1,1,1]
	v_pk_fma_f32 v[12:13], v[232:233], v[140:141], v[12:13] op_sel:[1,0,0] op_sel_hi:[1,1,1]
	v_pk_fma_f32 v[14:15], v[232:233], v[142:143], v[14:15] op_sel:[1,0,0] op_sel_hi:[1,1,1]
	v_pk_fma_f32 v[8:9], v[234:235], v[144:145], v[8:9] op_sel_hi:[0,1,1]
	v_pk_fma_f32 v[10:11], v[234:235], v[146:147], v[10:11] op_sel_hi:[0,1,1]
	v_pk_fma_f32 v[12:13], v[234:235], v[148:149], v[12:13] op_sel_hi:[0,1,1]
	v_pk_fma_f32 v[14:15], v[234:235], v[150:151], v[14:15] op_sel_hi:[0,1,1]
	v_pk_fma_f32 v[8:9], v[234:235], v[152:153], v[8:9] op_sel:[1,0,0] op_sel_hi:[1,1,1]
	v_pk_fma_f32 v[10:11], v[234:235], v[154:155], v[10:11] op_sel:[1,0,0] op_sel_hi:[1,1,1]
	v_pk_fma_f32 v[12:13], v[234:235], v[156:157], v[12:13] op_sel:[1,0,0] op_sel_hi:[1,1,1]
	v_pk_fma_f32 v[14:15], v[234:235], v[158:159], v[14:15] op_sel:[1,0,0] op_sel_hi:[1,1,1]
	v_pk_fma_f32 v[8:9], v[236:237], v[160:161], v[8:9] op_sel_hi:[0,1,1]
	v_pk_fma_f32 v[10:11], v[236:237], v[162:163], v[10:11] op_sel_hi:[0,1,1]
	v_pk_fma_f32 v[12:13], v[236:237], v[164:165], v[12:13] op_sel_hi:[0,1,1]
	v_pk_fma_f32 v[14:15], v[236:237], v[166:167], v[14:15] op_sel_hi:[0,1,1]
	v_pk_fma_f32 v[8:9], v[236:237], v[168:169], v[8:9] op_sel:[1,0,0] op_sel_hi:[1,1,1]
	v_pk_fma_f32 v[10:11], v[236:237], v[170:171], v[10:11] op_sel:[1,0,0] op_sel_hi:[1,1,1]
	v_pk_fma_f32 v[12:13], v[236:237], v[172:173], v[12:13] op_sel:[1,0,0] op_sel_hi:[1,1,1]
	v_pk_fma_f32 v[14:15], v[236:237], v[174:175], v[14:15] op_sel:[1,0,0] op_sel_hi:[1,1,1]
	v_pk_fma_f32 v[8:9], v[238:239], v[176:177], v[8:9] op_sel_hi:[0,1,1]
	v_pk_fma_f32 v[10:11], v[238:239], v[178:179], v[10:11] op_sel_hi:[0,1,1]
; #define LAS __attribute__((address_space(3)))
; __global__ void __launch_bounds__(NTHR, 2) fwd_kernel(Args args) {
;     ...
;             for (int i = 0; i < 16; ++i) { const int k = 2 * lane + 128 * i; f32x2 rv[8]; unsigned xw[8];
; #pragma unroll
;                 for (int e = 0; e < 8; ++e) rv[e] = *(const LAS f32x2*)(Rg + e * DM + k);
; #pragma unroll
;                 for (int q = 0; q < 8; ++q) xw[q] = *(const unsigned*)(XB + (size_t)(t0 + q) * DM + k);
; #pragma unroll
;                 for (int q = 0; q < 8; ++q) { const float x0 = bflo(xw[q]), x1 = bfhi(xw[q]); ssq[q] += x0 * x0 + x1 * x1;
; #pragma unroll
;                     for (int e = 0; e < 8; ++e) acc[q][e] += x0 * rv[e].x + x1 * rv[e].y; } }
	v_pk_fma_f32 v[12:13], v[238:239], v[180:181], v[12:13] op_sel_hi:[0,1,1]
	v_pk_fma_f32 v[14:15], v[238:239], v[182:183], v[14:15] op_sel_hi:[0,1,1]
	v_pk_fma_f32 v[8:9], v[238:239], v[184:185], v[8:9] op_sel:[1,0,0] op_sel_hi:[1,1,1]
	v_pk_fma_f32 v[10:11], v[238:239], v[186:187], v[10:11] op_sel:[1,0,0] op_sel_hi:[1,1,1]
	v_pk_fma_f32 v[12:13], v[238:239], v[188:189], v[12:13] op_sel:[1,0,0] op_sel_hi:[1,1,1]
	v_pk_fma_f32 v[14:15], v[238:239], v[190:191], v[14:15] op_sel:[1,0,0] op_sel_hi:[1,1,1]
	v_lshlrev_b32_e32 v232, 16, v104
	v_and_b32_e32 v233, s15, v104
	v_lshlrev_b32_e32 v234, 16, v105
	v_and_b32_e32 v235, s15, v105
	v_lshlrev_b32_e32 v236, 16, v106
	v_and_b32_e32 v237, s15, v106
	v_lshlrev_b32_e32 v238, 16, v107
	v_and_b32_e32 v239, s15, v107
	v_pk_fma_f32 v[196:197], v[232:233], v[232:233], v[196:197]
	v_pk_fma_f32 v[196:197], v[234:235], v[234:235], v[196:197]
	v_pk_fma_f32 v[196:197], v[236:237], v[236:237], v[196:197]
	v_pk_fma_f32 v[196:197], v[238:239], v[238:239], v[196:197]
	v_pk_fma_f32 v[16:17], v[232:233], v[128:129], v[16:17] op_sel_hi:[0,1,1]
	v_pk_fma_f32 v[18:19], v[232:233], v[130:131], v[18:19] op_sel_hi:[0,1,1]
	v_pk_fma_f32 v[20:21], v[232:233], v[132:133], v[20:21] op_sel_hi:[0,1,1]
	v_pk_fma_f32 v[22:23], v[232:233], v[134:135], v[22:23] op_sel_hi:[0,1,1]
	v_pk_fma_f32 v[16:17], v[232:233], v[136:137], v[16:17] op_sel:[1,0,0] op_sel_hi:[1,1,1]
	v_pk_fma_f32 v[18:19], v[232:233], v[138:139], v[18:19] op_sel:[1,0,0] op_sel_hi:[1,1,1]
	v_pk_fma_f32 v[20:21], v[232:233], v[140:141], v[20:21] op_sel:[1,0,0] op_sel_hi:[1,1,1]
	v_pk_fma_f32 v[22:23], v[232:233], v[142:143], v[22:23] op_sel:[1,0,0] op_sel_hi:[1,1,1]
	v_pk_fma_f32 v[16:17], v[234:235], v[144:145], v[16:17] op_sel_hi:[0,1,1]
	v_pk_fma_f32 v[18:19], v[234:235], v[146:147], v[18:19] op_sel_hi:[0,1,1]
	v_pk_fma_f32 v[20:21], v[234:235], v[148:149], v[20:21] op_sel_hi:[0,1,1]
	v_pk_fma_f32 v[22:23], v[234:235], v[150:151], v[22:23] op_sel_hi:[0,1,1]
	v_pk_fma_f32 v[16:17], v[234:235], v[152:153], v[16:17] op_sel:[1,0,0] op_sel_hi:[1,1,1]
	v_pk_fma_f32 v[18:19], v[234:235], v[154:155], v[18:19] op_sel:[1,0,0] op_sel_hi:[1,1,1]
	v_pk_fma_f32 v[20:21], v[234:235], v[156:157], v[20:21] op_sel:[1,0,0] op_sel_hi:[1,1,1]
	v_pk_fma_f32 v[22:23], v[234:235], v[158:159], v[22:23] op_sel:[1,0,0] op_sel_hi:[1,1,1]
	v_pk_fma_f32 v[16:17], v[236:237], v[160:161], v[16:17] op_sel_hi:[0,1,1]
	v_pk_fma_f32 v[18:19], v[236:237], v[162:163], v[18:19] op_sel_hi:[0,1,1]
	v_pk_fma_f32 v[20:21], v[236:237], v[164:165], v[20:21] op_sel_hi:[0,1,1]
	v_pk_fma_f32 v[22:23], v[236:237], v[166:167], v[22:23] op_sel_hi:[0,1,1]
	v_pk_fma_f32 v[16:17], v[236:237], v[168:169], v[16:17] op_sel:[1,0,0] op_sel_hi:[1,1,1]
	v_pk_fma_f32 v[18:19], v[236:237], v[170:171], v[18:19] op_sel:[1,0,0] op_sel_hi:[1,1,1]
	v_pk_fma_f32 v[20:21], v[236:237], v[172:173], v[20:21] op_sel:[1,0,0] op_sel_hi:[1,1,1]
	v_pk_fma_f32 v[22:23], v[236:237], v[174:175], v[22:23] op_sel:[1,0,0] op_sel_hi:[1,1,1]
	v_pk_fma_f32 v[16:17], v[238:239], v[176:177], v[16:17] op_sel_hi:[0,1,1]
	v_pk_fma_f32 v[18:19], v[238:239], v[178:179], v[18:19] op_sel_hi:[0,1,1]
	v_pk_fma_f32 v[20:21], v[238:239], v[180:181], v[20:21] op_sel_hi:[0,1,1]
	v_pk_fma_f32 v[22:23], v[238:239], v[182:183], v[22:23] op_sel_hi:[0,1,1]
	v_pk_fma_f32 v[16:17], v[238:239], v[184:185], v[16:17] op_sel:[1,0,0] op_sel_hi:[1,1,1]
	v_pk_fma_f32 v[18:19], v[238:239], v[186:187], v[18:19] op_sel:[1,0,0] op_sel_hi:[1,1,1]
	v_pk_fma_f32 v[20:21], v[238:239], v[188:189], v[20:21] op_sel:[1,0,0] op_sel_hi:[1,1,1]
	v_pk_fma_f32 v[22:23], v[238:239], v[190:191], v[22:23] op_sel:[1,0,0] op_sel_hi:[1,1,1]
	v_lshlrev_b32_e32 v232, 16, v108
	v_and_b32_e32 v233, s15, v108
	v_lshlrev_b32_e32 v234, 16, v109
	v_and_b32_e32 v235, s15, v109
	v_lshlrev_b32_e32 v236, 16, v110
	v_and_b32_e32 v237, s15, v110
	v_lshlrev_b32_e32 v238, 16, v111
	v_and_b32_e32 v239, s15, v111
	v_pk_fma_f32 v[198:199], v[232:233], v[232:233], v[198:199]
	v_pk_fma_f32 v[198:199], v[234:235], v[234:235], v[198:199]
	v_pk_fma_f32 v[198:199], v[236:237], v[236:237], v[198:199]
	v_pk_fma_f32 v[198:199], v[238:239], v[238:239], v[198:199]
	v_pk_fma_f32 v[24:25], v[232:233], v[128:129], v[24:25] op_sel_hi:[0,1,1]
	v_pk_fma_f32 v[26:27], v[232:233], v[130:131], v[26:27] op_sel_hi:[0,1,1]
	v_pk_fma_f32 v[28:29], v[232:233], v[132:133], v[28:29] op_sel_hi:[0,1,1]
	v_pk_fma_f32 v[30:31], v[232:233], v[134:135], v[30:31] op_sel_hi:[0,1,1]
	v_pk_fma_f32 v[24:25], v[232:233], v[136:137], v[24:25] op_sel:[1,0,0] op_sel_hi:[1,1,1]
	v_pk_fma_f32 v[26:27], v[232:233], v[138:139], v[26:27] op_sel:[1,0,0] op_sel_hi:[1,1,1]
	v_pk_fma_f32 v[28:29], v[232:233], v[140:141], v[28:29] op_sel:[1,0,0] op_sel_hi:[1,1,1]
	v_pk_fma_f32 v[30:31], v[232:233], v[142:143], v[30:31] op_sel:[1,0,0] op_sel_hi:[1,1,1]
	v_pk_fma_f32 v[24:25], v[234:235], v[144:145], v[24:25] op_sel_hi:[0,1,1]
	v_pk_fma_f32 v[26:27], v[234:235], v[146:147], v[26:27] op_sel_hi:[0,1,1]
	v_pk_fma_f32 v[28:29], v[234:235], v[148:149], v[28:29] op_sel_hi:[0,1,1]
	v_pk_fma_f32 v[30:31], v[234:235], v[150:151], v[30:31] op_sel_hi:[0,1,1]
	v_pk_fma_f32 v[24:25], v[234:235], v[152:153], v[24:25] op_sel:[1,0,0] op_sel_hi:[1,1,1]
	v_pk_fma_f32 v[26:27], v[234:235], v[154:155], v[26:27] op_sel:[1,0,0] op_sel_hi:[1,1,1]
	v_pk_fma_f32 v[28:29], v[234:235], v[156:157], v[28:29] op_sel:[1,0,0] op_sel_hi:[1,1,1]
	v_pk_fma_f32 v[30:31], v[234:235], v[158:159], v[30:31] op_sel:[1,0,0] op_sel_hi:[1,1,1]
	v_pk_fma_f32 v[24:25], v[236:237], v[160:161], v[24:25] op_sel_hi:[0,1,1]
	v_pk_fma_f32 v[26:27], v[236:237], v[162:163], v[26:27] op_sel_hi:[0,1,1]
; #define LAS __attribute__((address_space(3)))
; __global__ void __launch_bounds__(NTHR, 2) fwd_kernel(Args args) {
;     ...
;             for (int i = 0; i < 16; ++i) { const int k = 2 * lane + 128 * i; f32x2 rv[8]; unsigned xw[8];
; #pragma unroll
;                 for (int e = 0; e < 8; ++e) rv[e] = *(const LAS f32x2*)(Rg + e * DM + k);
; #pragma unroll
;                 for (int q = 0; q < 8; ++q) xw[q] = *(const unsigned*)(XB + (size_t)(t0 + q) * DM + k);
; #pragma unroll
;                 for (int q = 0; q < 8; ++q) { const float x0 = bflo(xw[q]), x1 = bfhi(xw[q]); ssq[q] += x0 * x0 + x1 * x1;
; #pragma unroll
;                     for (int e = 0; e < 8; ++e) acc[q][e] += x0 * rv[e].x + x1 * rv[e].y; } }
	v_pk_fma_f32 v[28:29], v[236:237], v[164:165], v[28:29] op_sel_hi:[0,1,1]
	v_pk_fma_f32 v[30:31], v[236:237], v[166:167], v[30:31] op_sel_hi:[0,1,1]
	v_pk_fma_f32 v[24:25], v[236:237], v[168:169], v[24:25] op_sel:[1,0,0] op_sel_hi:[1,1,1]
	v_pk_fma_f32 v[26:27], v[236:237], v[170:171], v[26:27] op_sel:[1,0,0] op_sel_hi:[1,1,1]
	v_pk_fma_f32 v[28:29], v[236:237], v[172:173], v[28:29] op_sel:[1,0,0] op_sel_hi:[1,1,1]
	v_pk_fma_f32 v[30:31], v[236:237], v[174:175], v[30:31] op_sel:[1,0,0] op_sel_hi:[1,1,1]
	v_pk_fma_f32 v[24:25], v[238:239], v[176:177], v[24:25] op_sel_hi:[0,1,1]
	v_pk_fma_f32 v[26:27], v[238:239], v[178:179], v[26:27] op_sel_hi:[0,1,1]
	v_pk_fma_f32 v[28:29], v[238:239], v[180:181], v[28:29] op_sel_hi:[0,1,1]
	v_pk_fma_f32 v[30:31], v[238:239], v[182:183], v[30:31] op_sel_hi:[0,1,1]
	v_pk_fma_f32 v[24:25], v[238:239], v[184:185], v[24:25] op_sel:[1,0,0] op_sel_hi:[1,1,1]
	v_pk_fma_f32 v[26:27], v[238:239], v[186:187], v[26:27] op_sel:[1,0,0] op_sel_hi:[1,1,1]
	v_pk_fma_f32 v[28:29], v[238:239], v[188:189], v[28:29] op_sel:[1,0,0] op_sel_hi:[1,1,1]
	v_pk_fma_f32 v[30:31], v[238:239], v[190:191], v[30:31] op_sel:[1,0,0] op_sel_hi:[1,1,1]
	v_lshlrev_b32_e32 v232, 16, v112
	v_and_b32_e32 v233, s15, v112
	v_lshlrev_b32_e32 v234, 16, v113
	v_and_b32_e32 v235, s15, v113
	v_lshlrev_b32_e32 v236, 16, v114
	v_and_b32_e32 v237, s15, v114
	v_lshlrev_b32_e32 v238, 16, v115
	v_and_b32_e32 v239, s15, v115
	v_pk_fma_f32 v[200:201], v[232:233], v[232:233], v[200:201]
	v_pk_fma_f32 v[200:201], v[234:235], v[234:235], v[200:201]
	v_pk_fma_f32 v[200:201], v[236:237], v[236:237], v[200:201]
	v_pk_fma_f32 v[200:201], v[238:239], v[238:239], v[200:201]
	v_pk_fma_f32 v[32:33], v[232:233], v[128:129], v[32:33] op_sel_hi:[0,1,1]
	v_pk_fma_f32 v[34:35], v[232:233], v[130:131], v[34:35] op_sel_hi:[0,1,1]
	v_pk_fma_f32 v[36:37], v[232:233], v[132:133], v[36:37] op_sel_hi:[0,1,1]
	v_pk_fma_f32 v[38:39], v[232:233], v[134:135], v[38:39] op_sel_hi:[0,1,1]
	v_pk_fma_f32 v[32:33], v[232:233], v[136:137], v[32:33] op_sel:[1,0,0] op_sel_hi:[1,1,1]
	v_pk_fma_f32 v[34:35], v[232:233], v[138:139], v[34:35] op_sel:[1,0,0] op_sel_hi:[1,1,1]
	v_pk_fma_f32 v[36:37], v[232:233], v[140:141], v[36:37] op_sel:[1,0,0] op_sel_hi:[1,1,1]
	v_pk_fma_f32 v[38:39], v[232:233], v[142:143], v[38:39] op_sel:[1,0,0] op_sel_hi:[1,1,1]
	v_pk_fma_f32 v[32:33], v[234:235], v[144:145], v[32:33] op_sel_hi:[0,1,1]
	v_pk_fma_f32 v[34:35], v[234:235], v[146:147], v[34:35] op_sel_hi:[0,1,1]
	v_pk_fma_f32 v[36:37], v[234:235], v[148:149], v[36:37] op_sel_hi:[0,1,1]
	v_pk_fma_f32 v[38:39], v[234:235], v[150:151], v[38:39] op_sel_hi:[0,1,1]
	v_pk_fma_f32 v[32:33], v[234:235], v[152:153], v[32:33] op_sel:[1,0,0] op_sel_hi:[1,1,1]
	v_pk_fma_f32 v[34:35], v[234:235], v[154:155], v[34:35] op_sel:[1,0,0] op_sel_hi:[1,1,1]
	v_pk_fma_f32 v[36:37], v[234:235], v[156:157], v[36:37] op_sel:[1,0,0] op_sel_hi:[1,1,1]
	v_pk_fma_f32 v[38:39], v[234:235], v[158:159], v[38:39] op_sel:[1,0,0] op_sel_hi:[1,1,1]
	v_pk_fma_f32 v[32:33], v[236:237], v[160:161], v[32:33] op_sel_hi:[0,1,1]
	v_pk_fma_f32 v[34:35], v[236:237], v[162:163], v[34:35] op_sel_hi:[0,1,1]
	v_pk_fma_f32 v[36:37], v[236:237], v[164:165], v[36:37] op_sel_hi:[0,1,1]
	v_pk_fma_f32 v[38:39], v[236:237], v[166:167], v[38:39] op_sel_hi:[0,1,1]
	v_pk_fma_f32 v[32:33], v[236:237], v[168:169], v[32:33] op_sel:[1,0,0] op_sel_hi:[1,1,1]
	v_pk_fma_f32 v[34:35], v[236:237], v[170:171], v[34:35] op_sel:[1,0,0] op_sel_hi:[1,1,1]
	v_pk_fma_f32 v[36:37], v[236:237], v[172:173], v[36:37] op_sel:[1,0,0] op_sel_hi:[1,1,1]
	v_pk_fma_f32 v[38:39], v[236:237], v[174:175], v[38:39] op_sel:[1,0,0] op_sel_hi:[1,1,1]
	v_pk_fma_f32 v[32:33], v[238:239], v[176:177], v[32:33] op_sel_hi:[0,1,1]
	v_pk_fma_f32 v[34:35], v[238:239], v[178:179], v[34:35] op_sel_hi:[0,1,1]
	v_pk_fma_f32 v[36:37], v[238:239], v[180:181], v[36:37] op_sel_hi:[0,1,1]
	v_pk_fma_f32 v[38:39], v[238:239], v[182:183], v[38:39] op_sel_hi:[0,1,1]
	v_pk_fma_f32 v[32:33], v[238:239], v[184:185], v[32:33] op_sel:[1,0,0] op_sel_hi:[1,1,1]
	v_pk_fma_f32 v[34:35], v[238:239], v[186:187], v[34:35] op_sel:[1,0,0] op_sel_hi:[1,1,1]
	v_pk_fma_f32 v[36:37], v[238:239], v[188:189], v[36:37] op_sel:[1,0,0] op_sel_hi:[1,1,1]
	v_pk_fma_f32 v[38:39], v[238:239], v[190:191], v[38:39] op_sel:[1,0,0] op_sel_hi:[1,1,1]
	v_lshlrev_b32_e32 v232, 16, v116
	v_and_b32_e32 v233, s15, v116
	v_lshlrev_b32_e32 v234, 16, v117
	v_and_b32_e32 v235, s15, v117
	v_lshlrev_b32_e32 v236, 16, v118
	v_and_b32_e32 v237, s15, v118
	v_lshlrev_b32_e32 v238, 16, v119
	v_and_b32_e32 v239, s15, v119
	v_pk_fma_f32 v[202:203], v[232:233], v[232:233], v[202:203]
	v_pk_fma_f32 v[202:203], v[234:235], v[234:235], v[202:203]
	v_pk_fma_f32 v[202:203], v[236:237], v[236:237], v[202:203]
	v_pk_fma_f32 v[202:203], v[238:239], v[238:239], v[202:203]
	v_pk_fma_f32 v[40:41], v[232:233], v[128:129], v[40:41] op_sel_hi:[0,1,1]
	v_pk_fma_f32 v[42:43], v[232:233], v[130:131], v[42:43] op_sel_hi:[0,1,1]
	v_pk_fma_f32 v[44:45], v[232:233], v[132:133], v[44:45] op_sel_hi:[0,1,1]
	v_pk_fma_f32 v[46:47], v[232:233], v[134:135], v[46:47] op_sel_hi:[0,1,1]
	v_pk_fma_f32 v[40:41], v[232:233], v[136:137], v[40:41] op_sel:[1,0,0] op_sel_hi:[1,1,1]
	v_pk_fma_f32 v[42:43], v[232:233], v[138:139], v[42:43] op_sel:[1,0,0] op_sel_hi:[1,1,1]
	v_pk_fma_f32 v[44:45], v[232:233], v[140:141], v[44:45] op_sel:[1,0,0] op_sel_hi:[1,1,1]
	v_pk_fma_f32 v[46:47], v[232:233], v[142:143], v[46:47] op_sel:[1,0,0] op_sel_hi:[1,1,1]
	v_pk_fma_f32 v[40:41], v[234:235], v[144:145], v[40:41] op_sel_hi:[0,1,1]
	v_pk_fma_f32 v[42:43], v[234:235], v[146:147], v[42:43] op_sel_hi:[0,1,1]
; #define LAS __attribute__((address_space(3)))
; __global__ void __launch_bounds__(NTHR, 2) fwd_kernel(Args args) {
;     ...
;             for (int i = 0; i < 16; ++i) { const int k = 2 * lane + 128 * i; f32x2 rv[8]; unsigned xw[8];
; #pragma unroll
;                 for (int e = 0; e < 8; ++e) rv[e] = *(const LAS f32x2*)(Rg + e * DM + k);
; #pragma unroll
;                 for (int q = 0; q < 8; ++q) xw[q] = *(const unsigned*)(XB + (size_t)(t0 + q) * DM + k);
; #pragma unroll
;                 for (int q = 0; q < 8; ++q) { const float x0 = bflo(xw[q]), x1 = bfhi(xw[q]); ssq[q] += x0 * x0 + x1 * x1;
; #pragma unroll
;                     for (int e = 0; e < 8; ++e) acc[q][e] += x0 * rv[e].x + x1 * rv[e].y; } }
	v_pk_fma_f32 v[44:45], v[234:235], v[148:149], v[44:45] op_sel_hi:[0,1,1]
	v_pk_fma_f32 v[46:47], v[234:235], v[150:151], v[46:47] op_sel_hi:[0,1,1]
	v_pk_fma_f32 v[40:41], v[234:235], v[152:153], v[40:41] op_sel:[1,0,0] op_sel_hi:[1,1,1]
	v_pk_fma_f32 v[42:43], v[234:235], v[154:155], v[42:43] op_sel:[1,0,0] op_sel_hi:[1,1,1]
	v_pk_fma_f32 v[44:45], v[234:235], v[156:157], v[44:45] op_sel:[1,0,0] op_sel_hi:[1,1,1]
	v_pk_fma_f32 v[46:47], v[234:235], v[158:159], v[46:47] op_sel:[1,0,0] op_sel_hi:[1,1,1]
	v_pk_fma_f32 v[40:41], v[236:237], v[160:161], v[40:41] op_sel_hi:[0,1,1]
	v_pk_fma_f32 v[42:43], v[236:237], v[162:163], v[42:43] op_sel_hi:[0,1,1]
	v_pk_fma_f32 v[44:45], v[236:237], v[164:165], v[44:45] op_sel_hi:[0,1,1]
	v_pk_fma_f32 v[46:47], v[236:237], v[166:167], v[46:47] op_sel_hi:[0,1,1]
	v_pk_fma_f32 v[40:41], v[236:237], v[168:169], v[40:41] op_sel:[1,0,0] op_sel_hi:[1,1,1]
	v_pk_fma_f32 v[42:43], v[236:237], v[170:171], v[42:43] op_sel:[1,0,0] op_sel_hi:[1,1,1]
	v_pk_fma_f32 v[44:45], v[236:237], v[172:173], v[44:45] op_sel:[1,0,0] op_sel_hi:[1,1,1]
	v_pk_fma_f32 v[46:47], v[236:237], v[174:175], v[46:47] op_sel:[1,0,0] op_sel_hi:[1,1,1]
	v_pk_fma_f32 v[40:41], v[238:239], v[176:177], v[40:41] op_sel_hi:[0,1,1]
	v_pk_fma_f32 v[42:43], v[238:239], v[178:179], v[42:43] op_sel_hi:[0,1,1]
	v_pk_fma_f32 v[44:45], v[238:239], v[180:181], v[44:45] op_sel_hi:[0,1,1]
	v_pk_fma_f32 v[46:47], v[238:239], v[182:183], v[46:47] op_sel_hi:[0,1,1]
	v_pk_fma_f32 v[40:41], v[238:239], v[184:185], v[40:41] op_sel:[1,0,0] op_sel_hi:[1,1,1]
	v_pk_fma_f32 v[42:43], v[238:239], v[186:187], v[42:43] op_sel:[1,0,0] op_sel_hi:[1,1,1]
	v_pk_fma_f32 v[44:45], v[238:239], v[188:189], v[44:45] op_sel:[1,0,0] op_sel_hi:[1,1,1]
	v_pk_fma_f32 v[46:47], v[238:239], v[190:191], v[46:47] op_sel:[1,0,0] op_sel_hi:[1,1,1]
	v_lshlrev_b32_e32 v232, 16, v120
	v_and_b32_e32 v233, s15, v120
	v_lshlrev_b32_e32 v234, 16, v121
	v_and_b32_e32 v235, s15, v121
	v_lshlrev_b32_e32 v236, 16, v122
	v_and_b32_e32 v237, s15, v122
	v_lshlrev_b32_e32 v238, 16, v123
	v_and_b32_e32 v239, s15, v123
	v_pk_fma_f32 v[204:205], v[232:233], v[232:233], v[204:205]
	v_pk_fma_f32 v[204:205], v[234:235], v[234:235], v[204:205]
	v_pk_fma_f32 v[204:205], v[236:237], v[236:237], v[204:205]
	v_pk_fma_f32 v[204:205], v[238:239], v[238:239], v[204:205]
	v_pk_fma_f32 v[48:49], v[232:233], v[128:129], v[48:49] op_sel_hi:[0,1,1]
	v_pk_fma_f32 v[50:51], v[232:233], v[130:131], v[50:51] op_sel_hi:[0,1,1]
	v_pk_fma_f32 v[52:53], v[232:233], v[132:133], v[52:53] op_sel_hi:[0,1,1]
	v_pk_fma_f32 v[54:55], v[232:233], v[134:135], v[54:55] op_sel_hi:[0,1,1]
	v_pk_fma_f32 v[48:49], v[232:233], v[136:137], v[48:49] op_sel:[1,0,0] op_sel_hi:[1,1,1]
	v_pk_fma_f32 v[50:51], v[232:233], v[138:139], v[50:51] op_sel:[1,0,0] op_sel_hi:[1,1,1]
	v_pk_fma_f32 v[52:53], v[232:233], v[140:141], v[52:53] op_sel:[1,0,0] op_sel_hi:[1,1,1]
	v_pk_fma_f32 v[54:55], v[232:233], v[142:143], v[54:55] op_sel:[1,0,0] op_sel_hi:[1,1,1]
	v_pk_fma_f32 v[48:49], v[234:235], v[144:145], v[48:49] op_sel_hi:[0,1,1]
	v_pk_fma_f32 v[50:51], v[234:235], v[146:147], v[50:51] op_sel_hi:[0,1,1]
	v_pk_fma_f32 v[52:53], v[234:235], v[148:149], v[52:53] op_sel_hi:[0,1,1]
	v_pk_fma_f32 v[54:55], v[234:235], v[150:151], v[54:55] op_sel_hi:[0,1,1]
	v_pk_fma_f32 v[48:49], v[234:235], v[152:153], v[48:49] op_sel:[1,0,0] op_sel_hi:[1,1,1]
	v_pk_fma_f32 v[50:51], v[234:235], v[154:155], v[50:51] op_sel:[1,0,0] op_sel_hi:[1,1,1]
	v_pk_fma_f32 v[52:53], v[234:235], v[156:157], v[52:53] op_sel:[1,0,0] op_sel_hi:[1,1,1]
	v_pk_fma_f32 v[54:55], v[234:235], v[158:159], v[54:55] op_sel:[1,0,0] op_sel_hi:[1,1,1]
	v_pk_fma_f32 v[48:49], v[236:237], v[160:161], v[48:49] op_sel_hi:[0,1,1]
	v_pk_fma_f32 v[50:51], v[236:237], v[162:163], v[50:51] op_sel_hi:[0,1,1]
	v_pk_fma_f32 v[52:53], v[236:237], v[164:165], v[52:53] op_sel_hi:[0,1,1]
	v_pk_fma_f32 v[54:55], v[236:237], v[166:167], v[54:55] op_sel_hi:[0,1,1]
	v_pk_fma_f32 v[48:49], v[236:237], v[168:169], v[48:49] op_sel:[1,0,0] op_sel_hi:[1,1,1]
	v_pk_fma_f32 v[50:51], v[236:237], v[170:171], v[50:51] op_sel:[1,0,0] op_sel_hi:[1,1,1]
	v_pk_fma_f32 v[52:53], v[236:237], v[172:173], v[52:53] op_sel:[1,0,0] op_sel_hi:[1,1,1]
	v_pk_fma_f32 v[54:55], v[236:237], v[174:175], v[54:55] op_sel:[1,0,0] op_sel_hi:[1,1,1]
	v_pk_fma_f32 v[48:49], v[238:239], v[176:177], v[48:49] op_sel_hi:[0,1,1]
	v_pk_fma_f32 v[50:51], v[238:239], v[178:179], v[50:51] op_sel_hi:[0,1,1]
	v_pk_fma_f32 v[52:53], v[238:239], v[180:181], v[52:53] op_sel_hi:[0,1,1]
	v_pk_fma_f32 v[54:55], v[238:239], v[182:183], v[54:55] op_sel_hi:[0,1,1]
	v_pk_fma_f32 v[48:49], v[238:239], v[184:185], v[48:49] op_sel:[1,0,0] op_sel_hi:[1,1,1]
	v_pk_fma_f32 v[50:51], v[238:239], v[186:187], v[50:51] op_sel:[1,0,0] op_sel_hi:[1,1,1]
	v_pk_fma_f32 v[52:53], v[238:239], v[188:189], v[52:53] op_sel:[1,0,0] op_sel_hi:[1,1,1]
	v_pk_fma_f32 v[54:55], v[238:239], v[190:191], v[54:55] op_sel:[1,0,0] op_sel_hi:[1,1,1]
	v_lshlrev_b32_e32 v232, 16, v124
	v_and_b32_e32 v233, s15, v124
	v_lshlrev_b32_e32 v234, 16, v125
	v_and_b32_e32 v235, s15, v125
	v_lshlrev_b32_e32 v236, 16, v126
	v_and_b32_e32 v237, s15, v126
	v_lshlrev_b32_e32 v238, 16, v127
	v_and_b32_e32 v239, s15, v127
	v_pk_fma_f32 v[206:207], v[232:233], v[232:233], v[206:207]
	v_pk_fma_f32 v[206:207], v[234:235], v[234:235], v[206:207]
	v_pk_fma_f32 v[206:207], v[236:237], v[236:237], v[206:207]
	v_pk_fma_f32 v[206:207], v[238:239], v[238:239], v[206:207]
	v_pk_fma_f32 v[56:57], v[232:233], v[128:129], v[56:57] op_sel_hi:[0,1,1]
	v_pk_fma_f32 v[58:59], v[232:233], v[130:131], v[58:59] op_sel_hi:[0,1,1]
; #define LAS __attribute__((address_space(3)))
; __global__ void __launch_bounds__(NTHR, 2) fwd_kernel(Args args) {
;     ...
;             for (int i = 0; i < 16; ++i) { const int k = 2 * lane + 128 * i; f32x2 rv[8]; unsigned xw[8];
; #pragma unroll
;                 for (int e = 0; e < 8; ++e) rv[e] = *(const LAS f32x2*)(Rg + e * DM + k);
; #pragma unroll
;                 for (int q = 0; q < 8; ++q) xw[q] = *(const unsigned*)(XB + (size_t)(t0 + q) * DM + k);
; #pragma unroll
;                 for (int q = 0; q < 8; ++q) { const float x0 = bflo(xw[q]), x1 = bfhi(xw[q]); ssq[q] += x0 * x0 + x1 * x1;
; #pragma unroll
;                     for (int e = 0; e < 8; ++e) acc[q][e] += x0 * rv[e].x + x1 * rv[e].y; } }
	v_pk_fma_f32 v[60:61], v[232:233], v[132:133], v[60:61] op_sel_hi:[0,1,1]
	v_pk_fma_f32 v[62:63], v[232:233], v[134:135], v[62:63] op_sel_hi:[0,1,1]
	v_pk_fma_f32 v[56:57], v[232:233], v[136:137], v[56:57] op_sel:[1,0,0] op_sel_hi:[1,1,1]
	v_pk_fma_f32 v[58:59], v[232:233], v[138:139], v[58:59] op_sel:[1,0,0] op_sel_hi:[1,1,1]
	v_pk_fma_f32 v[60:61], v[232:233], v[140:141], v[60:61] op_sel:[1,0,0] op_sel_hi:[1,1,1]
	v_pk_fma_f32 v[62:63], v[232:233], v[142:143], v[62:63] op_sel:[1,0,0] op_sel_hi:[1,1,1]
	v_pk_fma_f32 v[56:57], v[234:235], v[144:145], v[56:57] op_sel_hi:[0,1,1]
	v_pk_fma_f32 v[58:59], v[234:235], v[146:147], v[58:59] op_sel_hi:[0,1,1]
	v_pk_fma_f32 v[60:61], v[234:235], v[148:149], v[60:61] op_sel_hi:[0,1,1]
	v_pk_fma_f32 v[62:63], v[234:235], v[150:151], v[62:63] op_sel_hi:[0,1,1]
	v_pk_fma_f32 v[56:57], v[234:235], v[152:153], v[56:57] op_sel:[1,0,0] op_sel_hi:[1,1,1]
	v_pk_fma_f32 v[58:59], v[234:235], v[154:155], v[58:59] op_sel:[1,0,0] op_sel_hi:[1,1,1]
	v_pk_fma_f32 v[60:61], v[234:235], v[156:157], v[60:61] op_sel:[1,0,0] op_sel_hi:[1,1,1]
	v_pk_fma_f32 v[62:63], v[234:235], v[158:159], v[62:63] op_sel:[1,0,0] op_sel_hi:[1,1,1]
	v_pk_fma_f32 v[56:57], v[236:237], v[160:161], v[56:57] op_sel_hi:[0,1,1]
	v_pk_fma_f32 v[58:59], v[236:237], v[162:163], v[58:59] op_sel_hi:[0,1,1]
	v_pk_fma_f32 v[60:61], v[236:237], v[164:165], v[60:61] op_sel_hi:[0,1,1]
	v_pk_fma_f32 v[62:63], v[236:237], v[166:167], v[62:63] op_sel_hi:[0,1,1]
	v_pk_fma_f32 v[56:57], v[236:237], v[168:169], v[56:57] op_sel:[1,0,0] op_sel_hi:[1,1,1]
	v_pk_fma_f32 v[58:59], v[236:237], v[170:171], v[58:59] op_sel:[1,0,0] op_sel_hi:[1,1,1]
	v_pk_fma_f32 v[60:61], v[236:237], v[172:173], v[60:61] op_sel:[1,0,0] op_sel_hi:[1,1,1]
	v_pk_fma_f32 v[62:63], v[236:237], v[174:175], v[62:63] op_sel:[1,0,0] op_sel_hi:[1,1,1]
	v_pk_fma_f32 v[56:57], v[238:239], v[176:177], v[56:57] op_sel_hi:[0,1,1]
	v_pk_fma_f32 v[58:59], v[238:239], v[178:179], v[58:59] op_sel_hi:[0,1,1]
	v_pk_fma_f32 v[60:61], v[238:239], v[180:181], v[60:61] op_sel_hi:[0,1,1]
	v_pk_fma_f32 v[62:63], v[238:239], v[182:183], v[62:63] op_sel_hi:[0,1,1]
	v_pk_fma_f32 v[56:57], v[238:239], v[184:185], v[56:57] op_sel:[1,0,0] op_sel_hi:[1,1,1]
	v_pk_fma_f32 v[58:59], v[238:239], v[186:187], v[58:59] op_sel:[1,0,0] op_sel_hi:[1,1,1]
	v_pk_fma_f32 v[60:61], v[238:239], v[188:189], v[60:61] op_sel:[1,0,0] op_sel_hi:[1,1,1]
	v_pk_fma_f32 v[62:63], v[238:239], v[190:191], v[62:63] op_sel:[1,0,0] op_sel_hi:[1,1,1]
	global_load_dwordx4 v[96:99], v208, s[40:41] offset:3072
	global_load_dwordx4 v[100:103], v208, s[42:43] offset:3072
	global_load_dwordx4 v[104:107], v208, s[44:45] offset:3072
	global_load_dwordx4 v[108:111], v208, s[46:47] offset:3072
	global_load_dwordx4 v[112:115], v208, s[48:49] offset:3072
	global_load_dwordx4 v[116:119], v208, s[50:51] offset:3072
	global_load_dwordx4 v[120:123], v208, s[52:53] offset:3072
	global_load_dwordx4 v[124:127], v208, s[54:55] offset:3072
	ds_read_b128 v[128:131], v208 offset:32768
	ds_read_b128 v[132:135], v208 offset:33792
	ds_read_b128 v[136:139], v208 offset:34816
	ds_read_b128 v[140:143], v208 offset:35840
	ds_read_b128 v[144:147], v208 offset:36864
	ds_read_b128 v[148:151], v208 offset:37888
	ds_read_b128 v[152:155], v208 offset:38912
	ds_read_b128 v[156:159], v208 offset:39936
	ds_read_b128 v[160:163], v208 offset:40960
	ds_read_b128 v[164:167], v208 offset:41984
	ds_read_b128 v[168:171], v208 offset:43008
	ds_read_b128 v[172:175], v208 offset:44032
	ds_read_b128 v[176:179], v208 offset:45056
	ds_read_b128 v[180:183], v208 offset:46080
	ds_read_b128 v[184:187], v208 offset:47104
	ds_read_b128 v[188:191], v208 offset:48128
	s_waitcnt vmcnt(8)
	s_waitcnt lgkmcnt(0)
	v_lshlrev_b32_e32 v232, 16, v64
	v_and_b32_e32 v233, s15, v64
	v_lshlrev_b32_e32 v234, 16, v65
	v_and_b32_e32 v235, s15, v65
	v_lshlrev_b32_e32 v236, 16, v66
	v_and_b32_e32 v237, s15, v66
	v_lshlrev_b32_e32 v238, 16, v67
	v_and_b32_e32 v239, s15, v67
	v_pk_fma_f32 v[192:193], v[232:233], v[232:233], v[192:193]
	v_pk_fma_f32 v[192:193], v[234:235], v[234:235], v[192:193]
	v_pk_fma_f32 v[192:193], v[236:237], v[236:237], v[192:193]
	v_pk_fma_f32 v[192:193], v[238:239], v[238:239], v[192:193]
	v_pk_fma_f32 v[0:1], v[232:233], v[128:129], v[0:1] op_sel_hi:[0,1,1]
	v_pk_fma_f32 v[2:3], v[232:233], v[130:131], v[2:3] op_sel_hi:[0,1,1]
	v_pk_fma_f32 v[4:5], v[232:233], v[132:133], v[4:5] op_sel_hi:[0,1,1]
	v_pk_fma_f32 v[6:7], v[232:233], v[134:135], v[6:7] op_sel_hi:[0,1,1]
	v_pk_fma_f32 v[0:1], v[232:233], v[136:137], v[0:1] op_sel:[1,0,0] op_sel_hi:[1,1,1]
	v_pk_fma_f32 v[2:3], v[232:233], v[138:139], v[2:3] op_sel:[1,0,0] op_sel_hi:[1,1,1]
	v_pk_fma_f32 v[4:5], v[232:233], v[140:141], v[4:5] op_sel:[1,0,0] op_sel_hi:[1,1,1]
	v_pk_fma_f32 v[6:7], v[232:233], v[142:143], v[6:7] op_sel:[1,0,0] op_sel_hi:[1,1,1]
	v_pk_fma_f32 v[0:1], v[234:235], v[144:145], v[0:1] op_sel_hi:[0,1,1]
	v_pk_fma_f32 v[2:3], v[234:235], v[146:147], v[2:3] op_sel_hi:[0,1,1]
	v_pk_fma_f32 v[4:5], v[234:235], v[148:149], v[4:5] op_sel_hi:[0,1,1]
	v_pk_fma_f32 v[6:7], v[234:235], v[150:151], v[6:7] op_sel_hi:[0,1,1]
	v_pk_fma_f32 v[0:1], v[234:235], v[152:153], v[0:1] op_sel:[1,0,0] op_sel_hi:[1,1,1]
	v_pk_fma_f32 v[2:3], v[234:235], v[154:155], v[2:3] op_sel:[1,0,0] op_sel_hi:[1,1,1]
	v_pk_fma_f32 v[4:5], v[234:235], v[156:157], v[4:5] op_sel:[1,0,0] op_sel_hi:[1,1,1]
	v_pk_fma_f32 v[6:7], v[234:235], v[158:159], v[6:7] op_sel:[1,0,0] op_sel_hi:[1,1,1]
	v_pk_fma_f32 v[0:1], v[236:237], v[160:161], v[0:1] op_sel_hi:[0,1,1]
	v_pk_fma_f32 v[2:3], v[236:237], v[162:163], v[2:3] op_sel_hi:[0,1,1]
; #define LAS __attribute__((address_space(3)))
; __global__ void __launch_bounds__(NTHR, 2) fwd_kernel(Args args) {
;     ...
;             for (int i = 0; i < 16; ++i) { const int k = 2 * lane + 128 * i; f32x2 rv[8]; unsigned xw[8];
; #pragma unroll
;                 for (int e = 0; e < 8; ++e) rv[e] = *(const LAS f32x2*)(Rg + e * DM + k);
; #pragma unroll
;                 for (int q = 0; q < 8; ++q) xw[q] = *(const unsigned*)(XB + (size_t)(t0 + q) * DM + k);
; #pragma unroll
;                 for (int q = 0; q < 8; ++q) { const float x0 = bflo(xw[q]), x1 = bfhi(xw[q]); ssq[q] += x0 * x0 + x1 * x1;
; #pragma unroll
;                     for (int e = 0; e < 8; ++e) acc[q][e] += x0 * rv[e].x + x1 * rv[e].y; } }
	v_pk_fma_f32 v[4:5], v[236:237], v[164:165], v[4:5] op_sel_hi:[0,1,1]
	v_pk_fma_f32 v[6:7], v[236:237], v[166:167], v[6:7] op_sel_hi:[0,1,1]
	v_pk_fma_f32 v[0:1], v[236:237], v[168:169], v[0:1] op_sel:[1,0,0] op_sel_hi:[1,1,1]
	v_pk_fma_f32 v[2:3], v[236:237], v[170:171], v[2:3] op_sel:[1,0,0] op_sel_hi:[1,1,1]
	v_pk_fma_f32 v[4:5], v[236:237], v[172:173], v[4:5] op_sel:[1,0,0] op_sel_hi:[1,1,1]
	v_pk_fma_f32 v[6:7], v[236:237], v[174:175], v[6:7] op_sel:[1,0,0] op_sel_hi:[1,1,1]
	v_pk_fma_f32 v[0:1], v[238:239], v[176:177], v[0:1] op_sel_hi:[0,1,1]
	v_pk_fma_f32 v[2:3], v[238:239], v[178:179], v[2:3] op_sel_hi:[0,1,1]
	v_pk_fma_f32 v[4:5], v[238:239], v[180:181], v[4:5] op_sel_hi:[0,1,1]
	v_pk_fma_f32 v[6:7], v[238:239], v[182:183], v[6:7] op_sel_hi:[0,1,1]
	v_pk_fma_f32 v[0:1], v[238:239], v[184:185], v[0:1] op_sel:[1,0,0] op_sel_hi:[1,1,1]
	v_pk_fma_f32 v[2:3], v[238:239], v[186:187], v[2:3] op_sel:[1,0,0] op_sel_hi:[1,1,1]
	v_pk_fma_f32 v[4:5], v[238:239], v[188:189], v[4:5] op_sel:[1,0,0] op_sel_hi:[1,1,1]
	v_pk_fma_f32 v[6:7], v[238:239], v[190:191], v[6:7] op_sel:[1,0,0] op_sel_hi:[1,1,1]
	v_lshlrev_b32_e32 v232, 16, v68
	v_and_b32_e32 v233, s15, v68
	v_lshlrev_b32_e32 v234, 16, v69
	v_and_b32_e32 v235, s15, v69
	v_lshlrev_b32_e32 v236, 16, v70
	v_and_b32_e32 v237, s15, v70
	v_lshlrev_b32_e32 v238, 16, v71
	v_and_b32_e32 v239, s15, v71
	v_pk_fma_f32 v[194:195], v[232:233], v[232:233], v[194:195]
	v_pk_fma_f32 v[194:195], v[234:235], v[234:235], v[194:195]
	v_pk_fma_f32 v[194:195], v[236:237], v[236:237], v[194:195]
	v_pk_fma_f32 v[194:195], v[238:239], v[238:239], v[194:195]
	v_pk_fma_f32 v[8:9], v[232:233], v[128:129], v[8:9] op_sel_hi:[0,1,1]
	v_pk_fma_f32 v[10:11], v[232:233], v[130:131], v[10:11] op_sel_hi:[0,1,1]
	v_pk_fma_f32 v[12:13], v[232:233], v[132:133], v[12:13] op_sel_hi:[0,1,1]
	v_pk_fma_f32 v[14:15], v[232:233], v[134:135], v[14:15] op_sel_hi:[0,1,1]
	v_pk_fma_f32 v[8:9], v[232:233], v[136:137], v[8:9] op_sel:[1,0,0] op_sel_hi:[1,1,1]
	v_pk_fma_f32 v[10:11], v[232:233], v[138:139], v[10:11] op_sel:[1,0,0] op_sel_hi:[1,1,1]
	v_pk_fma_f32 v[12:13], v[232:233], v[140:141], v[12:13] op_sel:[1,0,0] op_sel_hi:[1,1,1]
	v_pk_fma_f32 v[14:15], v[232:233], v[142:143], v[14:15] op_sel:[1,0,0] op_sel_hi:[1,1,1]
	v_pk_fma_f32 v[8:9], v[234:235], v[144:145], v[8:9] op_sel_hi:[0,1,1]
	v_pk_fma_f32 v[10:11], v[234:235], v[146:147], v[10:11] op_sel_hi:[0,1,1]
	v_pk_fma_f32 v[12:13], v[234:235], v[148:149], v[12:13] op_sel_hi:[0,1,1]
	v_pk_fma_f32 v[14:15], v[234:235], v[150:151], v[14:15] op_sel_hi:[0,1,1]
	v_pk_fma_f32 v[8:9], v[234:235], v[152:153], v[8:9] op_sel:[1,0,0] op_sel_hi:[1,1,1]
	v_pk_fma_f32 v[10:11], v[234:235], v[154:155], v[10:11] op_sel:[1,0,0] op_sel_hi:[1,1,1]
	v_pk_fma_f32 v[12:13], v[234:235], v[156:157], v[12:13] op_sel:[1,0,0] op_sel_hi:[1,1,1]
	v_pk_fma_f32 v[14:15], v[234:235], v[158:159], v[14:15] op_sel:[1,0,0] op_sel_hi:[1,1,1]
	v_pk_fma_f32 v[8:9], v[236:237], v[160:161], v[8:9] op_sel_hi:[0,1,1]
	v_pk_fma_f32 v[10:11], v[236:237], v[162:163], v[10:11] op_sel_hi:[0,1,1]
	v_pk_fma_f32 v[12:13], v[236:237], v[164:165], v[12:13] op_sel_hi:[0,1,1]
	v_pk_fma_f32 v[14:15], v[236:237], v[166:167], v[14:15] op_sel_hi:[0,1,1]
	v_pk_fma_f32 v[8:9], v[236:237], v[168:169], v[8:9] op_sel:[1,0,0] op_sel_hi:[1,1,1]
	v_pk_fma_f32 v[10:11], v[236:237], v[170:171], v[10:11] op_sel:[1,0,0] op_sel_hi:[1,1,1]
	v_pk_fma_f32 v[12:13], v[236:237], v[172:173], v[12:13] op_sel:[1,0,0] op_sel_hi:[1,1,1]
	v_pk_fma_f32 v[14:15], v[236:237], v[174:175], v[14:15] op_sel:[1,0,0] op_sel_hi:[1,1,1]
	v_pk_fma_f32 v[8:9], v[238:239], v[176:177], v[8:9] op_sel_hi:[0,1,1]
	v_pk_fma_f32 v[10:11], v[238:239], v[178:179], v[10:11] op_sel_hi:[0,1,1]
	v_pk_fma_f32 v[12:13], v[238:239], v[180:181], v[12:13] op_sel_hi:[0,1,1]
	v_pk_fma_f32 v[14:15], v[238:239], v[182:183], v[14:15] op_sel_hi:[0,1,1]
	v_pk_fma_f32 v[8:9], v[238:239], v[184:185], v[8:9] op_sel:[1,0,0] op_sel_hi:[1,1,1]
	v_pk_fma_f32 v[10:11], v[238:239], v[186:187], v[10:11] op_sel:[1,0,0] op_sel_hi:[1,1,1]
	v_pk_fma_f32 v[12:13], v[238:239], v[188:189], v[12:13] op_sel:[1,0,0] op_sel_hi:[1,1,1]
	v_pk_fma_f32 v[14:15], v[238:239], v[190:191], v[14:15] op_sel:[1,0,0] op_sel_hi:[1,1,1]
	v_lshlrev_b32_e32 v232, 16, v72
	v_and_b32_e32 v233, s15, v72
	v_lshlrev_b32_e32 v234, 16, v73
	v_and_b32_e32 v235, s15, v73
	v_lshlrev_b32_e32 v236, 16, v74
	v_and_b32_e32 v237, s15, v74
	v_lshlrev_b32_e32 v238, 16, v75
	v_and_b32_e32 v239, s15, v75
	v_pk_fma_f32 v[196:197], v[232:233], v[232:233], v[196:197]
	v_pk_fma_f32 v[196:197], v[234:235], v[234:235], v[196:197]
	v_pk_fma_f32 v[196:197], v[236:237], v[236:237], v[196:197]
	v_pk_fma_f32 v[196:197], v[238:239], v[238:239], v[196:197]
	v_pk_fma_f32 v[16:17], v[232:233], v[128:129], v[16:17] op_sel_hi:[0,1,1]
	v_pk_fma_f32 v[18:19], v[232:233], v[130:131], v[18:19] op_sel_hi:[0,1,1]
	v_pk_fma_f32 v[20:21], v[232:233], v[132:133], v[20:21] op_sel_hi:[0,1,1]
	v_pk_fma_f32 v[22:23], v[232:233], v[134:135], v[22:23] op_sel_hi:[0,1,1]
	v_pk_fma_f32 v[16:17], v[232:233], v[136:137], v[16:17] op_sel:[1,0,0] op_sel_hi:[1,1,1]
	v_pk_fma_f32 v[18:19], v[232:233], v[138:139], v[18:19] op_sel:[1,0,0] op_sel_hi:[1,1,1]
	v_pk_fma_f32 v[20:21], v[232:233], v[140:141], v[20:21] op_sel:[1,0,0] op_sel_hi:[1,1,1]
	v_pk_fma_f32 v[22:23], v[232:233], v[142:143], v[22:23] op_sel:[1,0,0] op_sel_hi:[1,1,1]
	v_pk_fma_f32 v[16:17], v[234:235], v[144:145], v[16:17] op_sel_hi:[0,1,1]
	v_pk_fma_f32 v[18:19], v[234:235], v[146:147], v[18:19] op_sel_hi:[0,1,1]
	v_pk_fma_f32 v[20:21], v[234:235], v[148:149], v[20:21] op_sel_hi:[0,1,1]
	v_pk_fma_f32 v[22:23], v[234:235], v[150:151], v[22:23] op_sel_hi:[0,1,1]
; #define LAS __attribute__((address_space(3)))
; __global__ void __launch_bounds__(NTHR, 2) fwd_kernel(Args args) {
;     ...
;             for (int i = 0; i < 16; ++i) { const int k = 2 * lane + 128 * i; f32x2 rv[8]; unsigned xw[8];
; #pragma unroll
;                 for (int e = 0; e < 8; ++e) rv[e] = *(const LAS f32x2*)(Rg + e * DM + k);
; #pragma unroll
;                 for (int q = 0; q < 8; ++q) xw[q] = *(const unsigned*)(XB + (size_t)(t0 + q) * DM + k);
; #pragma unroll
;                 for (int q = 0; q < 8; ++q) { const float x0 = bflo(xw[q]), x1 = bfhi(xw[q]); ssq[q] += x0 * x0 + x1 * x1;
; #pragma unroll
;                     for (int e = 0; e < 8; ++e) acc[q][e] += x0 * rv[e].x + x1 * rv[e].y; } }
	v_pk_fma_f32 v[16:17], v[234:235], v[152:153], v[16:17] op_sel:[1,0,0] op_sel_hi:[1,1,1]
	v_pk_fma_f32 v[18:19], v[234:235], v[154:155], v[18:19] op_sel:[1,0,0] op_sel_hi:[1,1,1]
	v_pk_fma_f32 v[20:21], v[234:235], v[156:157], v[20:21] op_sel:[1,0,0] op_sel_hi:[1,1,1]
	v_pk_fma_f32 v[22:23], v[234:235], v[158:159], v[22:23] op_sel:[1,0,0] op_sel_hi:[1,1,1]
	v_pk_fma_f32 v[16:17], v[236:237], v[160:161], v[16:17] op_sel_hi:[0,1,1]
	v_pk_fma_f32 v[18:19], v[236:237], v[162:163], v[18:19] op_sel_hi:[0,1,1]
	v_pk_fma_f32 v[20:21], v[236:237], v[164:165], v[20:21] op_sel_hi:[0,1,1]
	v_pk_fma_f32 v[22:23], v[236:237], v[166:167], v[22:23] op_sel_hi:[0,1,1]
	v_pk_fma_f32 v[16:17], v[236:237], v[168:169], v[16:17] op_sel:[1,0,0] op_sel_hi:[1,1,1]
	v_pk_fma_f32 v[18:19], v[236:237], v[170:171], v[18:19] op_sel:[1,0,0] op_sel_hi:[1,1,1]
	v_pk_fma_f32 v[20:21], v[236:237], v[172:173], v[20:21] op_sel:[1,0,0] op_sel_hi:[1,1,1]
	v_pk_fma_f32 v[22:23], v[236:237], v[174:175], v[22:23] op_sel:[1,0,0] op_sel_hi:[1,1,1]
	v_pk_fma_f32 v[16:17], v[238:239], v[176:177], v[16:17] op_sel_hi:[0,1,1]
	v_pk_fma_f32 v[18:19], v[238:239], v[178:179], v[18:19] op_sel_hi:[0,1,1]
	v_pk_fma_f32 v[20:21], v[238:239], v[180:181], v[20:21] op_sel_hi:[0,1,1]
	v_pk_fma_f32 v[22:23], v[238:239], v[182:183], v[22:23] op_sel_hi:[0,1,1]
	v_pk_fma_f32 v[16:17], v[238:239], v[184:185], v[16:17] op_sel:[1,0,0] op_sel_hi:[1,1,1]
	v_pk_fma_f32 v[18:19], v[238:239], v[186:187], v[18:19] op_sel:[1,0,0] op_sel_hi:[1,1,1]
	v_pk_fma_f32 v[20:21], v[238:239], v[188:189], v[20:21] op_sel:[1,0,0] op_sel_hi:[1,1,1]
	v_pk_fma_f32 v[22:23], v[238:239], v[190:191], v[22:23] op_sel:[1,0,0] op_sel_hi:[1,1,1]
	v_lshlrev_b32_e32 v232, 16, v76
	v_and_b32_e32 v233, s15, v76
	v_lshlrev_b32_e32 v234, 16, v77
	v_and_b32_e32 v235, s15, v77
	v_lshlrev_b32_e32 v236, 16, v78
	v_and_b32_e32 v237, s15, v78
	v_lshlrev_b32_e32 v238, 16, v79
	v_and_b32_e32 v239, s15, v79
	v_pk_fma_f32 v[198:199], v[232:233], v[232:233], v[198:199]
	v_pk_fma_f32 v[198:199], v[234:235], v[234:235], v[198:199]
	v_pk_fma_f32 v[198:199], v[236:237], v[236:237], v[198:199]
	v_pk_fma_f32 v[198:199], v[238:239], v[238:239], v[198:199]
	v_pk_fma_f32 v[24:25], v[232:233], v[128:129], v[24:25] op_sel_hi:[0,1,1]
	v_pk_fma_f32 v[26:27], v[232:233], v[130:131], v[26:27] op_sel_hi:[0,1,1]
	v_pk_fma_f32 v[28:29], v[232:233], v[132:133], v[28:29] op_sel_hi:[0,1,1]
	v_pk_fma_f32 v[30:31], v[232:233], v[134:135], v[30:31] op_sel_hi:[0,1,1]
	v_pk_fma_f32 v[24:25], v[232:233], v[136:137], v[24:25] op_sel:[1,0,0] op_sel_hi:[1,1,1]
	v_pk_fma_f32 v[26:27], v[232:233], v[138:139], v[26:27] op_sel:[1,0,0] op_sel_hi:[1,1,1]
	v_pk_fma_f32 v[28:29], v[232:233], v[140:141], v[28:29] op_sel:[1,0,0] op_sel_hi:[1,1,1]
	v_pk_fma_f32 v[30:31], v[232:233], v[142:143], v[30:31] op_sel:[1,0,0] op_sel_hi:[1,1,1]
	v_pk_fma_f32 v[24:25], v[234:235], v[144:145], v[24:25] op_sel_hi:[0,1,1]
	v_pk_fma_f32 v[26:27], v[234:235], v[146:147], v[26:27] op_sel_hi:[0,1,1]
	v_pk_fma_f32 v[28:29], v[234:235], v[148:149], v[28:29] op_sel_hi:[0,1,1]
	v_pk_fma_f32 v[30:31], v[234:235], v[150:151], v[30:31] op_sel_hi:[0,1,1]
	v_pk_fma_f32 v[24:25], v[234:235], v[152:153], v[24:25] op_sel:[1,0,0] op_sel_hi:[1,1,1]
	v_pk_fma_f32 v[26:27], v[234:235], v[154:155], v[26:27] op_sel:[1,0,0] op_sel_hi:[1,1,1]
	v_pk_fma_f32 v[28:29], v[234:235], v[156:157], v[28:29] op_sel:[1,0,0] op_sel_hi:[1,1,1]
	v_pk_fma_f32 v[30:31], v[234:235], v[158:159], v[30:31] op_sel:[1,0,0] op_sel_hi:[1,1,1]
	v_pk_fma_f32 v[24:25], v[236:237], v[160:161], v[24:25] op_sel_hi:[0,1,1]
	v_pk_fma_f32 v[26:27], v[236:237], v[162:163], v[26:27] op_sel_hi:[0,1,1]
	v_pk_fma_f32 v[28:29], v[236:237], v[164:165], v[28:29] op_sel_hi:[0,1,1]
	v_pk_fma_f32 v[30:31], v[236:237], v[166:167], v[30:31] op_sel_hi:[0,1,1]
	v_pk_fma_f32 v[24:25], v[236:237], v[168:169], v[24:25] op_sel:[1,0,0] op_sel_hi:[1,1,1]
	v_pk_fma_f32 v[26:27], v[236:237], v[170:171], v[26:27] op_sel:[1,0,0] op_sel_hi:[1,1,1]
	v_pk_fma_f32 v[28:29], v[236:237], v[172:173], v[28:29] op_sel:[1,0,0] op_sel_hi:[1,1,1]
	v_pk_fma_f32 v[30:31], v[236:237], v[174:175], v[30:31] op_sel:[1,0,0] op_sel_hi:[1,1,1]
	v_pk_fma_f32 v[24:25], v[238:239], v[176:177], v[24:25] op_sel_hi:[0,1,1]
	v_pk_fma_f32 v[26:27], v[238:239], v[178:179], v[26:27] op_sel_hi:[0,1,1]
	v_pk_fma_f32 v[28:29], v[238:239], v[180:181], v[28:29] op_sel_hi:[0,1,1]
	v_pk_fma_f32 v[30:31], v[238:239], v[182:183], v[30:31] op_sel_hi:[0,1,1]
	v_pk_fma_f32 v[24:25], v[238:239], v[184:185], v[24:25] op_sel:[1,0,0] op_sel_hi:[1,1,1]
	v_pk_fma_f32 v[26:27], v[238:239], v[186:187], v[26:27] op_sel:[1,0,0] op_sel_hi:[1,1,1]
	v_pk_fma_f32 v[28:29], v[238:239], v[188:189], v[28:29] op_sel:[1,0,0] op_sel_hi:[1,1,1]
	v_pk_fma_f32 v[30:31], v[238:239], v[190:191], v[30:31] op_sel:[1,0,0] op_sel_hi:[1,1,1]
	v_lshlrev_b32_e32 v232, 16, v80
	v_and_b32_e32 v233, s15, v80
	v_lshlrev_b32_e32 v234, 16, v81
	v_and_b32_e32 v235, s15, v81
	v_lshlrev_b32_e32 v236, 16, v82
	v_and_b32_e32 v237, s15, v82
	v_lshlrev_b32_e32 v238, 16, v83
	v_and_b32_e32 v239, s15, v83
	v_pk_fma_f32 v[200:201], v[232:233], v[232:233], v[200:201]
	v_pk_fma_f32 v[200:201], v[234:235], v[234:235], v[200:201]
	v_pk_fma_f32 v[200:201], v[236:237], v[236:237], v[200:201]
	v_pk_fma_f32 v[200:201], v[238:239], v[238:239], v[200:201]
	v_pk_fma_f32 v[32:33], v[232:233], v[128:129], v[32:33] op_sel_hi:[0,1,1]
	v_pk_fma_f32 v[34:35], v[232:233], v[130:131], v[34:35] op_sel_hi:[0,1,1]
	v_pk_fma_f32 v[36:37], v[232:233], v[132:133], v[36:37] op_sel_hi:[0,1,1]
	v_pk_fma_f32 v[38:39], v[232:233], v[134:135], v[38:39] op_sel_hi:[0,1,1]
; #define LAS __attribute__((address_space(3)))
; __global__ void __launch_bounds__(NTHR, 2) fwd_kernel(Args args) {
;     ...
;             for (int i = 0; i < 16; ++i) { const int k = 2 * lane + 128 * i; f32x2 rv[8]; unsigned xw[8];
; #pragma unroll
;                 for (int e = 0; e < 8; ++e) rv[e] = *(const LAS f32x2*)(Rg + e * DM + k);
; #pragma unroll
;                 for (int q = 0; q < 8; ++q) xw[q] = *(const unsigned*)(XB + (size_t)(t0 + q) * DM + k);
; #pragma unroll
;                 for (int q = 0; q < 8; ++q) { const float x0 = bflo(xw[q]), x1 = bfhi(xw[q]); ssq[q] += x0 * x0 + x1 * x1;
; #pragma unroll
;                     for (int e = 0; e < 8; ++e) acc[q][e] += x0 * rv[e].x + x1 * rv[e].y; } }
	v_pk_fma_f32 v[32:33], v[232:233], v[136:137], v[32:33] op_sel:[1,0,0] op_sel_hi:[1,1,1]
	v_pk_fma_f32 v[34:35], v[232:233], v[138:139], v[34:35] op_sel:[1,0,0] op_sel_hi:[1,1,1]
	v_pk_fma_f32 v[36:37], v[232:233], v[140:141], v[36:37] op_sel:[1,0,0] op_sel_hi:[1,1,1]
	v_pk_fma_f32 v[38:39], v[232:233], v[142:143], v[38:39] op_sel:[1,0,0] op_sel_hi:[1,1,1]
	v_pk_fma_f32 v[32:33], v[234:235], v[144:145], v[32:33] op_sel_hi:[0,1,1]
	v_pk_fma_f32 v[34:35], v[234:235], v[146:147], v[34:35] op_sel_hi:[0,1,1]
	v_pk_fma_f32 v[36:37], v[234:235], v[148:149], v[36:37] op_sel_hi:[0,1,1]
	v_pk_fma_f32 v[38:39], v[234:235], v[150:151], v[38:39] op_sel_hi:[0,1,1]
	v_pk_fma_f32 v[32:33], v[234:235], v[152:153], v[32:33] op_sel:[1,0,0] op_sel_hi:[1,1,1]
	v_pk_fma_f32 v[34:35], v[234:235], v[154:155], v[34:35] op_sel:[1,0,0] op_sel_hi:[1,1,1]
	v_pk_fma_f32 v[36:37], v[234:235], v[156:157], v[36:37] op_sel:[1,0,0] op_sel_hi:[1,1,1]
	v_pk_fma_f32 v[38:39], v[234:235], v[158:159], v[38:39] op_sel:[1,0,0] op_sel_hi:[1,1,1]
	v_pk_fma_f32 v[32:33], v[236:237], v[160:161], v[32:33] op_sel_hi:[0,1,1]
	v_pk_fma_f32 v[34:35], v[236:237], v[162:163], v[34:35] op_sel_hi:[0,1,1]
	v_pk_fma_f32 v[36:37], v[236:237], v[164:165], v[36:37] op_sel_hi:[0,1,1]
	v_pk_fma_f32 v[38:39], v[236:237], v[166:167], v[38:39] op_sel_hi:[0,1,1]
	v_pk_fma_f32 v[32:33], v[236:237], v[168:169], v[32:33] op_sel:[1,0,0] op_sel_hi:[1,1,1]
	v_pk_fma_f32 v[34:35], v[236:237], v[170:171], v[34:35] op_sel:[1,0,0] op_sel_hi:[1,1,1]
	v_pk_fma_f32 v[36:37], v[236:237], v[172:173], v[36:37] op_sel:[1,0,0] op_sel_hi:[1,1,1]
	v_pk_fma_f32 v[38:39], v[236:237], v[174:175], v[38:39] op_sel:[1,0,0] op_sel_hi:[1,1,1]
	v_pk_fma_f32 v[32:33], v[238:239], v[176:177], v[32:33] op_sel_hi:[0,1,1]
	v_pk_fma_f32 v[34:35], v[238:239], v[178:179], v[34:35] op_sel_hi:[0,1,1]
	v_pk_fma_f32 v[36:37], v[238:239], v[180:181], v[36:37] op_sel_hi:[0,1,1]
	v_pk_fma_f32 v[38:39], v[238:239], v[182:183], v[38:39] op_sel_hi:[0,1,1]
	v_pk_fma_f32 v[32:33], v[238:239], v[184:185], v[32:33] op_sel:[1,0,0] op_sel_hi:[1,1,1]
	v_pk_fma_f32 v[34:35], v[238:239], v[186:187], v[34:35] op_sel:[1,0,0] op_sel_hi:[1,1,1]
	v_pk_fma_f32 v[36:37], v[238:239], v[188:189], v[36:37] op_sel:[1,0,0] op_sel_hi:[1,1,1]
	v_pk_fma_f32 v[38:39], v[238:239], v[190:191], v[38:39] op_sel:[1,0,0] op_sel_hi:[1,1,1]
	v_lshlrev_b32_e32 v232, 16, v84
	v_and_b32_e32 v233, s15, v84
	v_lshlrev_b32_e32 v234, 16, v85
	v_and_b32_e32 v235, s15, v85
	v_lshlrev_b32_e32 v236, 16, v86
	v_and_b32_e32 v237, s15, v86
	v_lshlrev_b32_e32 v238, 16, v87
	v_and_b32_e32 v239, s15, v87
	v_pk_fma_f32 v[202:203], v[232:233], v[232:233], v[202:203]
	v_pk_fma_f32 v[202:203], v[234:235], v[234:235], v[202:203]
	v_pk_fma_f32 v[202:203], v[236:237], v[236:237], v[202:203]
	v_pk_fma_f32 v[202:203], v[238:239], v[238:239], v[202:203]
	v_pk_fma_f32 v[40:41], v[232:233], v[128:129], v[40:41] op_sel_hi:[0,1,1]
	v_pk_fma_f32 v[42:43], v[232:233], v[130:131], v[42:43] op_sel_hi:[0,1,1]
	v_pk_fma_f32 v[44:45], v[232:233], v[132:133], v[44:45] op_sel_hi:[0,1,1]
	v_pk_fma_f32 v[46:47], v[232:233], v[134:135], v[46:47] op_sel_hi:[0,1,1]
	v_pk_fma_f32 v[40:41], v[232:233], v[136:137], v[40:41] op_sel:[1,0,0] op_sel_hi:[1,1,1]
	v_pk_fma_f32 v[42:43], v[232:233], v[138:139], v[42:43] op_sel:[1,0,0] op_sel_hi:[1,1,1]
	v_pk_fma_f32 v[44:45], v[232:233], v[140:141], v[44:45] op_sel:[1,0,0] op_sel_hi:[1,1,1]
	v_pk_fma_f32 v[46:47], v[232:233], v[142:143], v[46:47] op_sel:[1,0,0] op_sel_hi:[1,1,1]
	v_pk_fma_f32 v[40:41], v[234:235], v[144:145], v[40:41] op_sel_hi:[0,1,1]
	v_pk_fma_f32 v[42:43], v[234:235], v[146:147], v[42:43] op_sel_hi:[0,1,1]
	v_pk_fma_f32 v[44:45], v[234:235], v[148:149], v[44:45] op_sel_hi:[0,1,1]
	v_pk_fma_f32 v[46:47], v[234:235], v[150:151], v[46:47] op_sel_hi:[0,1,1]
	v_pk_fma_f32 v[40:41], v[234:235], v[152:153], v[40:41] op_sel:[1,0,0] op_sel_hi:[1,1,1]
	v_pk_fma_f32 v[42:43], v[234:235], v[154:155], v[42:43] op_sel:[1,0,0] op_sel_hi:[1,1,1]
	v_pk_fma_f32 v[44:45], v[234:235], v[156:157], v[44:45] op_sel:[1,0,0] op_sel_hi:[1,1,1]
	v_pk_fma_f32 v[46:47], v[234:235], v[158:159], v[46:47] op_sel:[1,0,0] op_sel_hi:[1,1,1]
	v_pk_fma_f32 v[40:41], v[236:237], v[160:161], v[40:41] op_sel_hi:[0,1,1]
	v_pk_fma_f32 v[42:43], v[236:237], v[162:163], v[42:43] op_sel_hi:[0,1,1]
	v_pk_fma_f32 v[44:45], v[236:237], v[164:165], v[44:45] op_sel_hi:[0,1,1]
	v_pk_fma_f32 v[46:47], v[236:237], v[166:167], v[46:47] op_sel_hi:[0,1,1]
	v_pk_fma_f32 v[40:41], v[236:237], v[168:169], v[40:41] op_sel:[1,0,0] op_sel_hi:[1,1,1]
	v_pk_fma_f32 v[42:43], v[236:237], v[170:171], v[42:43] op_sel:[1,0,0] op_sel_hi:[1,1,1]
	v_pk_fma_f32 v[44:45], v[236:237], v[172:173], v[44:45] op_sel:[1,0,0] op_sel_hi:[1,1,1]
	v_pk_fma_f32 v[46:47], v[236:237], v[174:175], v[46:47] op_sel:[1,0,0] op_sel_hi:[1,1,1]
	v_pk_fma_f32 v[40:41], v[238:239], v[176:177], v[40:41] op_sel_hi:[0,1,1]
	v_pk_fma_f32 v[42:43], v[238:239], v[178:179], v[42:43] op_sel_hi:[0,1,1]
	v_pk_fma_f32 v[44:45], v[238:239], v[180:181], v[44:45] op_sel_hi:[0,1,1]
	v_pk_fma_f32 v[46:47], v[238:239], v[182:183], v[46:47] op_sel_hi:[0,1,1]
	v_pk_fma_f32 v[40:41], v[238:239], v[184:185], v[40:41] op_sel:[1,0,0] op_sel_hi:[1,1,1]
	v_pk_fma_f32 v[42:43], v[238:239], v[186:187], v[42:43] op_sel:[1,0,0] op_sel_hi:[1,1,1]
	v_pk_fma_f32 v[44:45], v[238:239], v[188:189], v[44:45] op_sel:[1,0,0] op_sel_hi:[1,1,1]
	v_pk_fma_f32 v[46:47], v[238:239], v[190:191], v[46:47] op_sel:[1,0,0] op_sel_hi:[1,1,1]
	v_lshlrev_b32_e32 v232, 16, v88
	v_and_b32_e32 v233, s15, v88
	v_lshlrev_b32_e32 v234, 16, v89
	v_and_b32_e32 v235, s15, v89
	v_lshlrev_b32_e32 v236, 16, v90
; #define LAS __attribute__((address_space(3)))
; __global__ void __launch_bounds__(NTHR, 2) fwd_kernel(Args args) {
;     ...
;             for (int i = 0; i < 16; ++i) { const int k = 2 * lane + 128 * i; f32x2 rv[8]; unsigned xw[8];
; #pragma unroll
;                 for (int e = 0; e < 8; ++e) rv[e] = *(const LAS f32x2*)(Rg + e * DM + k);
; #pragma unroll
;                 for (int q = 0; q < 8; ++q) xw[q] = *(const unsigned*)(XB + (size_t)(t0 + q) * DM + k);
; #pragma unroll
;                 for (int q = 0; q < 8; ++q) { const float x0 = bflo(xw[q]), x1 = bfhi(xw[q]); ssq[q] += x0 * x0 + x1 * x1;
; #pragma unroll
;                     for (int e = 0; e < 8; ++e) acc[q][e] += x0 * rv[e].x + x1 * rv[e].y; } }
	v_and_b32_e32 v237, s15, v90
	v_lshlrev_b32_e32 v238, 16, v91
	v_and_b32_e32 v239, s15, v91
	v_pk_fma_f32 v[204:205], v[232:233], v[232:233], v[204:205]
	v_pk_fma_f32 v[204:205], v[234:235], v[234:235], v[204:205]
	v_pk_fma_f32 v[204:205], v[236:237], v[236:237], v[204:205]
	v_pk_fma_f32 v[204:205], v[238:239], v[238:239], v[204:205]
	v_pk_fma_f32 v[48:49], v[232:233], v[128:129], v[48:49] op_sel_hi:[0,1,1]
	v_pk_fma_f32 v[50:51], v[232:233], v[130:131], v[50:51] op_sel_hi:[0,1,1]
	v_pk_fma_f32 v[52:53], v[232:233], v[132:133], v[52:53] op_sel_hi:[0,1,1]
	v_pk_fma_f32 v[54:55], v[232:233], v[134:135], v[54:55] op_sel_hi:[0,1,1]
	v_pk_fma_f32 v[48:49], v[232:233], v[136:137], v[48:49] op_sel:[1,0,0] op_sel_hi:[1,1,1]
	v_pk_fma_f32 v[50:51], v[232:233], v[138:139], v[50:51] op_sel:[1,0,0] op_sel_hi:[1,1,1]
	v_pk_fma_f32 v[52:53], v[232:233], v[140:141], v[52:53] op_sel:[1,0,0] op_sel_hi:[1,1,1]
	v_pk_fma_f32 v[54:55], v[232:233], v[142:143], v[54:55] op_sel:[1,0,0] op_sel_hi:[1,1,1]
	v_pk_fma_f32 v[48:49], v[234:235], v[144:145], v[48:49] op_sel_hi:[0,1,1]
	v_pk_fma_f32 v[50:51], v[234:235], v[146:147], v[50:51] op_sel_hi:[0,1,1]
	v_pk_fma_f32 v[52:53], v[234:235], v[148:149], v[52:53] op_sel_hi:[0,1,1]
	v_pk_fma_f32 v[54:55], v[234:235], v[150:151], v[54:55] op_sel_hi:[0,1,1]
	v_pk_fma_f32 v[48:49], v[234:235], v[152:153], v[48:49] op_sel:[1,0,0] op_sel_hi:[1,1,1]
	v_pk_fma_f32 v[50:51], v[234:235], v[154:155], v[50:51] op_sel:[1,0,0] op_sel_hi:[1,1,1]
	v_pk_fma_f32 v[52:53], v[234:235], v[156:157], v[52:53] op_sel:[1,0,0] op_sel_hi:[1,1,1]
	v_pk_fma_f32 v[54:55], v[234:235], v[158:159], v[54:55] op_sel:[1,0,0] op_sel_hi:[1,1,1]
	v_pk_fma_f32 v[48:49], v[236:237], v[160:161], v[48:49] op_sel_hi:[0,1,1]
	v_pk_fma_f32 v[50:51], v[236:237], v[162:163], v[50:51] op_sel_hi:[0,1,1]
	v_pk_fma_f32 v[52:53], v[236:237], v[164:165], v[52:53] op_sel_hi:[0,1,1]
	v_pk_fma_f32 v[54:55], v[236:237], v[166:167], v[54:55] op_sel_hi:[0,1,1]
	v_pk_fma_f32 v[48:49], v[236:237], v[168:169], v[48:49] op_sel:[1,0,0] op_sel_hi:[1,1,1]
	v_pk_fma_f32 v[50:51], v[236:237], v[170:171], v[50:51] op_sel:[1,0,0] op_sel_hi:[1,1,1]
	v_pk_fma_f32 v[52:53], v[236:237], v[172:173], v[52:53] op_sel:[1,0,0] op_sel_hi:[1,1,1]
	v_pk_fma_f32 v[54:55], v[236:237], v[174:175], v[54:55] op_sel:[1,0,0] op_sel_hi:[1,1,1]
	v_pk_fma_f32 v[48:49], v[238:239], v[176:177], v[48:49] op_sel_hi:[0,1,1]
	v_pk_fma_f32 v[50:51], v[238:239], v[178:179], v[50:51] op_sel_hi:[0,1,1]
	v_pk_fma_f32 v[52:53], v[238:239], v[180:181], v[52:53] op_sel_hi:[0,1,1]
	v_pk_fma_f32 v[54:55], v[238:239], v[182:183], v[54:55] op_sel_hi:[0,1,1]
	v_pk_fma_f32 v[48:49], v[238:239], v[184:185], v[48:49] op_sel:[1,0,0] op_sel_hi:[1,1,1]
	v_pk_fma_f32 v[50:51], v[238:239], v[186:187], v[50:51] op_sel:[1,0,0] op_sel_hi:[1,1,1]
	v_pk_fma_f32 v[52:53], v[238:239], v[188:189], v[52:53] op_sel:[1,0,0] op_sel_hi:[1,1,1]
	v_pk_fma_f32 v[54:55], v[238:239], v[190:191], v[54:55] op_sel:[1,0,0] op_sel_hi:[1,1,1]
	v_lshlrev_b32_e32 v232, 16, v92
	v_and_b32_e32 v233, s15, v92
	v_lshlrev_b32_e32 v234, 16, v93
	v_and_b32_e32 v235, s15, v93
	v_lshlrev_b32_e32 v236, 16, v94
	v_and_b32_e32 v237, s15, v94
	v_lshlrev_b32_e32 v238, 16, v95
	v_and_b32_e32 v239, s15, v95
	v_pk_fma_f32 v[206:207], v[232:233], v[232:233], v[206:207]
	v_pk_fma_f32 v[206:207], v[234:235], v[234:235], v[206:207]
	v_pk_fma_f32 v[206:207], v[236:237], v[236:237], v[206:207]
	v_pk_fma_f32 v[206:207], v[238:239], v[238:239], v[206:207]
	v_pk_fma_f32 v[56:57], v[232:233], v[128:129], v[56:57] op_sel_hi:[0,1,1]
	v_pk_fma_f32 v[58:59], v[232:233], v[130:131], v[58:59] op_sel_hi:[0,1,1]
	v_pk_fma_f32 v[60:61], v[232:233], v[132:133], v[60:61] op_sel_hi:[0,1,1]
	v_pk_fma_f32 v[62:63], v[232:233], v[134:135], v[62:63] op_sel_hi:[0,1,1]
	v_pk_fma_f32 v[56:57], v[232:233], v[136:137], v[56:57] op_sel:[1,0,0] op_sel_hi:[1,1,1]
	v_pk_fma_f32 v[58:59], v[232:233], v[138:139], v[58:59] op_sel:[1,0,0] op_sel_hi:[1,1,1]
	v_pk_fma_f32 v[60:61], v[232:233], v[140:141], v[60:61] op_sel:[1,0,0] op_sel_hi:[1,1,1]
	v_pk_fma_f32 v[62:63], v[232:233], v[142:143], v[62:63] op_sel:[1,0,0] op_sel_hi:[1,1,1]
	v_pk_fma_f32 v[56:57], v[234:235], v[144:145], v[56:57] op_sel_hi:[0,1,1]
	v_pk_fma_f32 v[58:59], v[234:235], v[146:147], v[58:59] op_sel_hi:[0,1,1]
	v_pk_fma_f32 v[60:61], v[234:235], v[148:149], v[60:61] op_sel_hi:[0,1,1]
	v_pk_fma_f32 v[62:63], v[234:235], v[150:151], v[62:63] op_sel_hi:[0,1,1]
	v_pk_fma_f32 v[56:57], v[234:235], v[152:153], v[56:57] op_sel:[1,0,0] op_sel_hi:[1,1,1]
	v_pk_fma_f32 v[58:59], v[234:235], v[154:155], v[58:59] op_sel:[1,0,0] op_sel_hi:[1,1,1]
	v_pk_fma_f32 v[60:61], v[234:235], v[156:157], v[60:61] op_sel:[1,0,0] op_sel_hi:[1,1,1]
	v_pk_fma_f32 v[62:63], v[234:235], v[158:159], v[62:63] op_sel:[1,0,0] op_sel_hi:[1,1,1]
	v_pk_fma_f32 v[56:57], v[236:237], v[160:161], v[56:57] op_sel_hi:[0,1,1]
	v_pk_fma_f32 v[58:59], v[236:237], v[162:163], v[58:59] op_sel_hi:[0,1,1]
	v_pk_fma_f32 v[60:61], v[236:237], v[164:165], v[60:61] op_sel_hi:[0,1,1]
	v_pk_fma_f32 v[62:63], v[236:237], v[166:167], v[62:63] op_sel_hi:[0,1,1]
	v_pk_fma_f32 v[56:57], v[236:237], v[168:169], v[56:57] op_sel:[1,0,0] op_sel_hi:[1,1,1]
	v_pk_fma_f32 v[58:59], v[236:237], v[170:171], v[58:59] op_sel:[1,0,0] op_sel_hi:[1,1,1]
	v_pk_fma_f32 v[60:61], v[236:237], v[172:173], v[60:61] op_sel:[1,0,0] op_sel_hi:[1,1,1]
	v_pk_fma_f32 v[62:63], v[236:237], v[174:175], v[62:63] op_sel:[1,0,0] op_sel_hi:[1,1,1]
	v_pk_fma_f32 v[56:57], v[238:239], v[176:177], v[56:57] op_sel_hi:[0,1,1]
	v_pk_fma_f32 v[58:59], v[238:239], v[178:179], v[58:59] op_sel_hi:[0,1,1]
	v_pk_fma_f32 v[60:61], v[238:239], v[180:181], v[60:61] op_sel_hi:[0,1,1]
	v_pk_fma_f32 v[62:63], v[238:239], v[182:183], v[62:63] op_sel_hi:[0,1,1]
	v_pk_fma_f32 v[56:57], v[238:239], v[184:185], v[56:57] op_sel:[1,0,0] op_sel_hi:[1,1,1]
	v_pk_fma_f32 v[58:59], v[238:239], v[186:187], v[58:59] op_sel:[1,0,0] op_sel_hi:[1,1,1]
	v_pk_fma_f32 v[60:61], v[238:239], v[188:189], v[60:61] op_sel:[1,0,0] op_sel_hi:[1,1,1]
	v_pk_fma_f32 v[62:63], v[238:239], v[190:191], v[62:63] op_sel:[1,0,0] op_sel_hi:[1,1,1]
	ds_read_b128 v[128:131], v208 offset:49152
	ds_read_b128 v[132:135], v208 offset:50176
	ds_read_b128 v[136:139], v208 offset:51200
	ds_read_b128 v[140:143], v208 offset:52224
	ds_read_b128 v[144:147], v208 offset:53248
	ds_read_b128 v[148:151], v208 offset:54272
	ds_read_b128 v[152:155], v208 offset:55296
	ds_read_b128 v[156:159], v208 offset:56320
	ds_read_b128 v[160:163], v208 offset:57344
	ds_read_b128 v[164:167], v208 offset:58368
	ds_read_b128 v[168:171], v208 offset:59392
	ds_read_b128 v[172:175], v208 offset:60416
	ds_read_b128 v[176:179], v208 offset:61440
	ds_read_b128 v[180:183], v208 offset:62464
	ds_read_b128 v[184:187], v208 offset:63488
	ds_read_b128 v[188:191], v208 offset:64512
	s_waitcnt vmcnt(0)
; #define LAS __attribute__((address_space(3)))
; __global__ void __launch_bounds__(NTHR, 2) fwd_kernel(Args args) {
;     ...
;             for (int i = 0; i < 16; ++i) { const int k = 2 * lane + 128 * i; f32x2 rv[8]; unsigned xw[8];
; #pragma unroll
;                 for (int e = 0; e < 8; ++e) rv[e] = *(const LAS f32x2*)(Rg + e * DM + k);
; #pragma unroll
;                 for (int q = 0; q < 8; ++q) xw[q] = *(const unsigned*)(XB + (size_t)(t0 + q) * DM + k);
; #pragma unroll
;                 for (int q = 0; q < 8; ++q) { const float x0 = bflo(xw[q]), x1 = bfhi(xw[q]); ssq[q] += x0 * x0 + x1 * x1;
; #pragma unroll
;                     for (int e = 0; e < 8; ++e) acc[q][e] += x0 * rv[e].x + x1 * rv[e].y; } }
	s_waitcnt lgkmcnt(0)
	v_lshlrev_b32_e32 v232, 16, v96
	v_and_b32_e32 v233, s15, v96
	v_lshlrev_b32_e32 v234, 16, v97
	v_and_b32_e32 v235, s15, v97
	v_lshlrev_b32_e32 v236, 16, v98
	v_and_b32_e32 v237, s15, v98
	v_lshlrev_b32_e32 v238, 16, v99
	v_and_b32_e32 v239, s15, v99
	v_pk_fma_f32 v[192:193], v[232:233], v[232:233], v[192:193]
	v_pk_fma_f32 v[192:193], v[234:235], v[234:235], v[192:193]
	v_pk_fma_f32 v[192:193], v[236:237], v[236:237], v[192:193]
	v_pk_fma_f32 v[192:193], v[238:239], v[238:239], v[192:193]
	v_pk_fma_f32 v[0:1], v[232:233], v[128:129], v[0:1] op_sel_hi:[0,1,1]
	v_pk_fma_f32 v[2:3], v[232:233], v[130:131], v[2:3] op_sel_hi:[0,1,1]
	v_pk_fma_f32 v[4:5], v[232:233], v[132:133], v[4:5] op_sel_hi:[0,1,1]
	v_pk_fma_f32 v[6:7], v[232:233], v[134:135], v[6:7] op_sel_hi:[0,1,1]
	v_pk_fma_f32 v[0:1], v[232:233], v[136:137], v[0:1] op_sel:[1,0,0] op_sel_hi:[1,1,1]
	v_pk_fma_f32 v[2:3], v[232:233], v[138:139], v[2:3] op_sel:[1,0,0] op_sel_hi:[1,1,1]
	v_pk_fma_f32 v[4:5], v[232:233], v[140:141], v[4:5] op_sel:[1,0,0] op_sel_hi:[1,1,1]
	v_pk_fma_f32 v[6:7], v[232:233], v[142:143], v[6:7] op_sel:[1,0,0] op_sel_hi:[1,1,1]
	v_pk_fma_f32 v[0:1], v[234:235], v[144:145], v[0:1] op_sel_hi:[0,1,1]
	v_pk_fma_f32 v[2:3], v[234:235], v[146:147], v[2:3] op_sel_hi:[0,1,1]
	v_pk_fma_f32 v[4:5], v[234:235], v[148:149], v[4:5] op_sel_hi:[0,1,1]
	v_pk_fma_f32 v[6:7], v[234:235], v[150:151], v[6:7] op_sel_hi:[0,1,1]
	v_pk_fma_f32 v[0:1], v[234:235], v[152:153], v[0:1] op_sel:[1,0,0] op_sel_hi:[1,1,1]
	v_pk_fma_f32 v[2:3], v[234:235], v[154:155], v[2:3] op_sel:[1,0,0] op_sel_hi:[1,1,1]
	v_pk_fma_f32 v[4:5], v[234:235], v[156:157], v[4:5] op_sel:[1,0,0] op_sel_hi:[1,1,1]
	v_pk_fma_f32 v[6:7], v[234:235], v[158:159], v[6:7] op_sel:[1,0,0] op_sel_hi:[1,1,1]
	v_pk_fma_f32 v[0:1], v[236:237], v[160:161], v[0:1] op_sel_hi:[0,1,1]
	v_pk_fma_f32 v[2:3], v[236:237], v[162:163], v[2:3] op_sel_hi:[0,1,1]
	v_pk_fma_f32 v[4:5], v[236:237], v[164:165], v[4:5] op_sel_hi:[0,1,1]
	v_pk_fma_f32 v[6:7], v[236:237], v[166:167], v[6:7] op_sel_hi:[0,1,1]
	v_pk_fma_f32 v[0:1], v[236:237], v[168:169], v[0:1] op_sel:[1,0,0] op_sel_hi:[1,1,1]
	v_pk_fma_f32 v[2:3], v[236:237], v[170:171], v[2:3] op_sel:[1,0,0] op_sel_hi:[1,1,1]
	v_pk_fma_f32 v[4:5], v[236:237], v[172:173], v[4:5] op_sel:[1,0,0] op_sel_hi:[1,1,1]
	v_pk_fma_f32 v[6:7], v[236:237], v[174:175], v[6:7] op_sel:[1,0,0] op_sel_hi:[1,1,1]
	v_pk_fma_f32 v[0:1], v[238:239], v[176:177], v[0:1] op_sel_hi:[0,1,1]
	v_pk_fma_f32 v[2:3], v[238:239], v[178:179], v[2:3] op_sel_hi:[0,1,1]
	v_pk_fma_f32 v[4:5], v[238:239], v[180:181], v[4:5] op_sel_hi:[0,1,1]
	v_pk_fma_f32 v[6:7], v[238:239], v[182:183], v[6:7] op_sel_hi:[0,1,1]
	v_pk_fma_f32 v[0:1], v[238:239], v[184:185], v[0:1] op_sel:[1,0,0] op_sel_hi:[1,1,1]
	v_pk_fma_f32 v[2:3], v[238:239], v[186:187], v[2:3] op_sel:[1,0,0] op_sel_hi:[1,1,1]
	v_pk_fma_f32 v[4:5], v[238:239], v[188:189], v[4:5] op_sel:[1,0,0] op_sel_hi:[1,1,1]
	v_pk_fma_f32 v[6:7], v[238:239], v[190:191], v[6:7] op_sel:[1,0,0] op_sel_hi:[1,1,1]
	v_lshlrev_b32_e32 v232, 16, v100
	v_and_b32_e32 v233, s15, v100
	v_lshlrev_b32_e32 v234, 16, v101
	v_and_b32_e32 v235, s15, v101
	v_lshlrev_b32_e32 v236, 16, v102
	v_and_b32_e32 v237, s15, v102
	v_lshlrev_b32_e32 v238, 16, v103
	v_and_b32_e32 v239, s15, v103
	v_pk_fma_f32 v[194:195], v[232:233], v[232:233], v[194:195]
	v_pk_fma_f32 v[194:195], v[234:235], v[234:235], v[194:195]
	v_pk_fma_f32 v[194:195], v[236:237], v[236:237], v[194:195]
	v_pk_fma_f32 v[194:195], v[238:239], v[238:239], v[194:195]
	v_pk_fma_f32 v[8:9], v[232:233], v[128:129], v[8:9] op_sel_hi:[0,1,1]
	v_pk_fma_f32 v[10:11], v[232:233], v[130:131], v[10:11] op_sel_hi:[0,1,1]
	v_pk_fma_f32 v[12:13], v[232:233], v[132:133], v[12:13] op_sel_hi:[0,1,1]
	v_pk_fma_f32 v[14:15], v[232:233], v[134:135], v[14:15] op_sel_hi:[0,1,1]
	v_pk_fma_f32 v[8:9], v[232:233], v[136:137], v[8:9] op_sel:[1,0,0] op_sel_hi:[1,1,1]
	v_pk_fma_f32 v[10:11], v[232:233], v[138:139], v[10:11] op_sel:[1,0,0] op_sel_hi:[1,1,1]
	v_pk_fma_f32 v[12:13], v[232:233], v[140:141], v[12:13] op_sel:[1,0,0] op_sel_hi:[1,1,1]
	v_pk_fma_f32 v[14:15], v[232:233], v[142:143], v[14:15] op_sel:[1,0,0] op_sel_hi:[1,1,1]
	v_pk_fma_f32 v[8:9], v[234:235], v[144:145], v[8:9] op_sel_hi:[0,1,1]
	v_pk_fma_f32 v[10:11], v[234:235], v[146:147], v[10:11] op_sel_hi:[0,1,1]
	v_pk_fma_f32 v[12:13], v[234:235], v[148:149], v[12:13] op_sel_hi:[0,1,1]
	v_pk_fma_f32 v[14:15], v[234:235], v[150:151], v[14:15] op_sel_hi:[0,1,1]
	v_pk_fma_f32 v[8:9], v[234:235], v[152:153], v[8:9] op_sel:[1,0,0] op_sel_hi:[1,1,1]
	v_pk_fma_f32 v[10:11], v[234:235], v[154:155], v[10:11] op_sel:[1,0,0] op_sel_hi:[1,1,1]
	v_pk_fma_f32 v[12:13], v[234:235], v[156:157], v[12:13] op_sel:[1,0,0] op_sel_hi:[1,1,1]
	v_pk_fma_f32 v[14:15], v[234:235], v[158:159], v[14:15] op_sel:[1,0,0] op_sel_hi:[1,1,1]
	v_pk_fma_f32 v[8:9], v[236:237], v[160:161], v[8:9] op_sel_hi:[0,1,1]
	v_pk_fma_f32 v[10:11], v[236:237], v[162:163], v[10:11] op_sel_hi:[0,1,1]
	v_pk_fma_f32 v[12:13], v[236:237], v[164:165], v[12:13] op_sel_hi:[0,1,1]
	v_pk_fma_f32 v[14:15], v[236:237], v[166:167], v[14:15] op_sel_hi:[0,1,1]
	v_pk_fma_f32 v[8:9], v[236:237], v[168:169], v[8:9] op_sel:[1,0,0] op_sel_hi:[1,1,1]
	v_pk_fma_f32 v[10:11], v[236:237], v[170:171], v[10:11] op_sel:[1,0,0] op_sel_hi:[1,1,1]
	v_pk_fma_f32 v[12:13], v[236:237], v[172:173], v[12:13] op_sel:[1,0,0] op_sel_hi:[1,1,1]
	v_pk_fma_f32 v[14:15], v[236:237], v[174:175], v[14:15] op_sel:[1,0,0] op_sel_hi:[1,1,1]
	v_pk_fma_f32 v[8:9], v[238:239], v[176:177], v[8:9] op_sel_hi:[0,1,1]
	v_pk_fma_f32 v[10:11], v[238:239], v[178:179], v[10:11] op_sel_hi:[0,1,1]
; #define LAS __attribute__((address_space(3)))
; __global__ void __launch_bounds__(NTHR, 2) fwd_kernel(Args args) {
;     ...
;             for (int i = 0; i < 16; ++i) { const int k = 2 * lane + 128 * i; f32x2 rv[8]; unsigned xw[8];
; #pragma unroll
;                 for (int e = 0; e < 8; ++e) rv[e] = *(const LAS f32x2*)(Rg + e * DM + k);
; #pragma unroll
;                 for (int q = 0; q < 8; ++q) xw[q] = *(const unsigned*)(XB + (size_t)(t0 + q) * DM + k);
; #pragma unroll
;                 for (int q = 0; q < 8; ++q) { const float x0 = bflo(xw[q]), x1 = bfhi(xw[q]); ssq[q] += x0 * x0 + x1 * x1;
; #pragma unroll
;                     for (int e = 0; e < 8; ++e) acc[q][e] += x0 * rv[e].x + x1 * rv[e].y; } }
	v_pk_fma_f32 v[12:13], v[238:239], v[180:181], v[12:13] op_sel_hi:[0,1,1]
	v_pk_fma_f32 v[14:15], v[238:239], v[182:183], v[14:15] op_sel_hi:[0,1,1]
	v_pk_fma_f32 v[8:9], v[238:239], v[184:185], v[8:9] op_sel:[1,0,0] op_sel_hi:[1,1,1]
	v_pk_fma_f32 v[10:11], v[238:239], v[186:187], v[10:11] op_sel:[1,0,0] op_sel_hi:[1,1,1]
	v_pk_fma_f32 v[12:13], v[238:239], v[188:189], v[12:13] op_sel:[1,0,0] op_sel_hi:[1,1,1]
	v_pk_fma_f32 v[14:15], v[238:239], v[190:191], v[14:15] op_sel:[1,0,0] op_sel_hi:[1,1,1]
	v_lshlrev_b32_e32 v232, 16, v104
	v_and_b32_e32 v233, s15, v104
	v_lshlrev_b32_e32 v234, 16, v105
	v_and_b32_e32 v235, s15, v105
	v_lshlrev_b32_e32 v236, 16, v106
	v_and_b32_e32 v237, s15, v106
	v_lshlrev_b32_e32 v238, 16, v107
	v_and_b32_e32 v239, s15, v107
	v_pk_fma_f32 v[196:197], v[232:233], v[232:233], v[196:197]
	v_pk_fma_f32 v[196:197], v[234:235], v[234:235], v[196:197]
	v_pk_fma_f32 v[196:197], v[236:237], v[236:237], v[196:197]
	v_pk_fma_f32 v[196:197], v[238:239], v[238:239], v[196:197]
	v_pk_fma_f32 v[16:17], v[232:233], v[128:129], v[16:17] op_sel_hi:[0,1,1]
	v_pk_fma_f32 v[18:19], v[232:233], v[130:131], v[18:19] op_sel_hi:[0,1,1]
	v_pk_fma_f32 v[20:21], v[232:233], v[132:133], v[20:21] op_sel_hi:[0,1,1]
	v_pk_fma_f32 v[22:23], v[232:233], v[134:135], v[22:23] op_sel_hi:[0,1,1]
	v_pk_fma_f32 v[16:17], v[232:233], v[136:137], v[16:17] op_sel:[1,0,0] op_sel_hi:[1,1,1]
	v_pk_fma_f32 v[18:19], v[232:233], v[138:139], v[18:19] op_sel:[1,0,0] op_sel_hi:[1,1,1]
	v_pk_fma_f32 v[20:21], v[232:233], v[140:141], v[20:21] op_sel:[1,0,0] op_sel_hi:[1,1,1]
	v_pk_fma_f32 v[22:23], v[232:233], v[142:143], v[22:23] op_sel:[1,0,0] op_sel_hi:[1,1,1]
	v_pk_fma_f32 v[16:17], v[234:235], v[144:145], v[16:17] op_sel_hi:[0,1,1]
	v_pk_fma_f32 v[18:19], v[234:235], v[146:147], v[18:19] op_sel_hi:[0,1,1]
	v_pk_fma_f32 v[20:21], v[234:235], v[148:149], v[20:21] op_sel_hi:[0,1,1]
	v_pk_fma_f32 v[22:23], v[234:235], v[150:151], v[22:23] op_sel_hi:[0,1,1]
	v_pk_fma_f32 v[16:17], v[234:235], v[152:153], v[16:17] op_sel:[1,0,0] op_sel_hi:[1,1,1]
	v_pk_fma_f32 v[18:19], v[234:235], v[154:155], v[18:19] op_sel:[1,0,0] op_sel_hi:[1,1,1]
	v_pk_fma_f32 v[20:21], v[234:235], v[156:157], v[20:21] op_sel:[1,0,0] op_sel_hi:[1,1,1]
	v_pk_fma_f32 v[22:23], v[234:235], v[158:159], v[22:23] op_sel:[1,0,0] op_sel_hi:[1,1,1]
	v_pk_fma_f32 v[16:17], v[236:237], v[160:161], v[16:17] op_sel_hi:[0,1,1]
	v_pk_fma_f32 v[18:19], v[236:237], v[162:163], v[18:19] op_sel_hi:[0,1,1]
	v_pk_fma_f32 v[20:21], v[236:237], v[164:165], v[20:21] op_sel_hi:[0,1,1]
	v_pk_fma_f32 v[22:23], v[236:237], v[166:167], v[22:23] op_sel_hi:[0,1,1]
	v_pk_fma_f32 v[16:17], v[236:237], v[168:169], v[16:17] op_sel:[1,0,0] op_sel_hi:[1,1,1]
	v_pk_fma_f32 v[18:19], v[236:237], v[170:171], v[18:19] op_sel:[1,0,0] op_sel_hi:[1,1,1]
	v_pk_fma_f32 v[20:21], v[236:237], v[172:173], v[20:21] op_sel:[1,0,0] op_sel_hi:[1,1,1]
	v_pk_fma_f32 v[22:23], v[236:237], v[174:175], v[22:23] op_sel:[1,0,0] op_sel_hi:[1,1,1]
	v_pk_fma_f32 v[16:17], v[238:239], v[176:177], v[16:17] op_sel_hi:[0,1,1]
	v_pk_fma_f32 v[18:19], v[238:239], v[178:179], v[18:19] op_sel_hi:[0,1,1]
	v_pk_fma_f32 v[20:21], v[238:239], v[180:181], v[20:21] op_sel_hi:[0,1,1]
	v_pk_fma_f32 v[22:23], v[238:239], v[182:183], v[22:23] op_sel_hi:[0,1,1]
	v_pk_fma_f32 v[16:17], v[238:239], v[184:185], v[16:17] op_sel:[1,0,0] op_sel_hi:[1,1,1]
	v_pk_fma_f32 v[18:19], v[238:239], v[186:187], v[18:19] op_sel:[1,0,0] op_sel_hi:[1,1,1]
	v_pk_fma_f32 v[20:21], v[238:239], v[188:189], v[20:21] op_sel:[1,0,0] op_sel_hi:[1,1,1]
	v_pk_fma_f32 v[22:23], v[238:239], v[190:191], v[22:23] op_sel:[1,0,0] op_sel_hi:[1,1,1]
	v_lshlrev_b32_e32 v232, 16, v108
	v_and_b32_e32 v233, s15, v108
	v_lshlrev_b32_e32 v234, 16, v109
	v_and_b32_e32 v235, s15, v109
	v_lshlrev_b32_e32 v236, 16, v110
	v_and_b32_e32 v237, s15, v110
	v_lshlrev_b32_e32 v238, 16, v111
	v_and_b32_e32 v239, s15, v111
	v_pk_fma_f32 v[198:199], v[232:233], v[232:233], v[198:199]
	v_pk_fma_f32 v[198:199], v[234:235], v[234:235], v[198:199]
	v_pk_fma_f32 v[198:199], v[236:237], v[236:237], v[198:199]
	v_pk_fma_f32 v[198:199], v[238:239], v[238:239], v[198:199]
	v_pk_fma_f32 v[24:25], v[232:233], v[128:129], v[24:25] op_sel_hi:[0,1,1]
	v_pk_fma_f32 v[26:27], v[232:233], v[130:131], v[26:27] op_sel_hi:[0,1,1]
	v_pk_fma_f32 v[28:29], v[232:233], v[132:133], v[28:29] op_sel_hi:[0,1,1]
	v_pk_fma_f32 v[30:31], v[232:233], v[134:135], v[30:31] op_sel_hi:[0,1,1]
	v_pk_fma_f32 v[24:25], v[232:233], v[136:137], v[24:25] op_sel:[1,0,0] op_sel_hi:[1,1,1]
	v_pk_fma_f32 v[26:27], v[232:233], v[138:139], v[26:27] op_sel:[1,0,0] op_sel_hi:[1,1,1]
	v_pk_fma_f32 v[28:29], v[232:233], v[140:141], v[28:29] op_sel:[1,0,0] op_sel_hi:[1,1,1]
	v_pk_fma_f32 v[30:31], v[232:233], v[142:143], v[30:31] op_sel:[1,0,0] op_sel_hi:[1,1,1]
	v_pk_fma_f32 v[24:25], v[234:235], v[144:145], v[24:25] op_sel_hi:[0,1,1]
	v_pk_fma_f32 v[26:27], v[234:235], v[146:147], v[26:27] op_sel_hi:[0,1,1]
	v_pk_fma_f32 v[28:29], v[234:235], v[148:149], v[28:29] op_sel_hi:[0,1,1]
	v_pk_fma_f32 v[30:31], v[234:235], v[150:151], v[30:31] op_sel_hi:[0,1,1]
	v_pk_fma_f32 v[24:25], v[234:235], v[152:153], v[24:25] op_sel:[1,0,0] op_sel_hi:[1,1,1]
	v_pk_fma_f32 v[26:27], v[234:235], v[154:155], v[26:27] op_sel:[1,0,0] op_sel_hi:[1,1,1]
	v_pk_fma_f32 v[28:29], v[234:235], v[156:157], v[28:29] op_sel:[1,0,0] op_sel_hi:[1,1,1]
	v_pk_fma_f32 v[30:31], v[234:235], v[158:159], v[30:31] op_sel:[1,0,0] op_sel_hi:[1,1,1]
	v_pk_fma_f32 v[24:25], v[236:237], v[160:161], v[24:25] op_sel_hi:[0,1,1]
	v_pk_fma_f32 v[26:27], v[236:237], v[162:163], v[26:27] op_sel_hi:[0,1,1]
; #define LAS __attribute__((address_space(3)))
; __global__ void __launch_bounds__(NTHR, 2) fwd_kernel(Args args) {
;     ...
;             for (int i = 0; i < 16; ++i) { const int k = 2 * lane + 128 * i; f32x2 rv[8]; unsigned xw[8];
; #pragma unroll
;                 for (int e = 0; e < 8; ++e) rv[e] = *(const LAS f32x2*)(Rg + e * DM + k);
; #pragma unroll
;                 for (int q = 0; q < 8; ++q) xw[q] = *(const unsigned*)(XB + (size_t)(t0 + q) * DM + k);
; #pragma unroll
;                 for (int q = 0; q < 8; ++q) { const float x0 = bflo(xw[q]), x1 = bfhi(xw[q]); ssq[q] += x0 * x0 + x1 * x1;
; #pragma unroll
;                     for (int e = 0; e < 8; ++e) acc[q][e] += x0 * rv[e].x + x1 * rv[e].y; } }
	v_pk_fma_f32 v[28:29], v[236:237], v[164:165], v[28:29] op_sel_hi:[0,1,1]
	v_pk_fma_f32 v[30:31], v[236:237], v[166:167], v[30:31] op_sel_hi:[0,1,1]
	v_pk_fma_f32 v[24:25], v[236:237], v[168:169], v[24:25] op_sel:[1,0,0] op_sel_hi:[1,1,1]
	v_pk_fma_f32 v[26:27], v[236:237], v[170:171], v[26:27] op_sel:[1,0,0] op_sel_hi:[1,1,1]
	v_pk_fma_f32 v[28:29], v[236:237], v[172:173], v[28:29] op_sel:[1,0,0] op_sel_hi:[1,1,1]
	v_pk_fma_f32 v[30:31], v[236:237], v[174:175], v[30:31] op_sel:[1,0,0] op_sel_hi:[1,1,1]
	v_pk_fma_f32 v[24:25], v[238:239], v[176:177], v[24:25] op_sel_hi:[0,1,1]
	v_pk_fma_f32 v[26:27], v[238:239], v[178:179], v[26:27] op_sel_hi:[0,1,1]
	v_pk_fma_f32 v[28:29], v[238:239], v[180:181], v[28:29] op_sel_hi:[0,1,1]
	v_pk_fma_f32 v[30:31], v[238:239], v[182:183], v[30:31] op_sel_hi:[0,1,1]
	v_pk_fma_f32 v[24:25], v[238:239], v[184:185], v[24:25] op_sel:[1,0,0] op_sel_hi:[1,1,1]
	v_pk_fma_f32 v[26:27], v[238:239], v[186:187], v[26:27] op_sel:[1,0,0] op_sel_hi:[1,1,1]
	v_pk_fma_f32 v[28:29], v[238:239], v[188:189], v[28:29] op_sel:[1,0,0] op_sel_hi:[1,1,1]
	v_pk_fma_f32 v[30:31], v[238:239], v[190:191], v[30:31] op_sel:[1,0,0] op_sel_hi:[1,1,1]
	v_lshlrev_b32_e32 v232, 16, v112
	v_and_b32_e32 v233, s15, v112
	v_lshlrev_b32_e32 v234, 16, v113
	v_and_b32_e32 v235, s15, v113
	v_lshlrev_b32_e32 v236, 16, v114
	v_and_b32_e32 v237, s15, v114
	v_lshlrev_b32_e32 v238, 16, v115
	v_and_b32_e32 v239, s15, v115
	v_pk_fma_f32 v[200:201], v[232:233], v[232:233], v[200:201]
	v_pk_fma_f32 v[200:201], v[234:235], v[234:235], v[200:201]
	v_pk_fma_f32 v[200:201], v[236:237], v[236:237], v[200:201]
	v_pk_fma_f32 v[200:201], v[238:239], v[238:239], v[200:201]
	v_pk_fma_f32 v[32:33], v[232:233], v[128:129], v[32:33] op_sel_hi:[0,1,1]
	v_pk_fma_f32 v[34:35], v[232:233], v[130:131], v[34:35] op_sel_hi:[0,1,1]
	v_pk_fma_f32 v[36:37], v[232:233], v[132:133], v[36:37] op_sel_hi:[0,1,1]
	v_pk_fma_f32 v[38:39], v[232:233], v[134:135], v[38:39] op_sel_hi:[0,1,1]
	v_pk_fma_f32 v[32:33], v[232:233], v[136:137], v[32:33] op_sel:[1,0,0] op_sel_hi:[1,1,1]
	v_pk_fma_f32 v[34:35], v[232:233], v[138:139], v[34:35] op_sel:[1,0,0] op_sel_hi:[1,1,1]
	v_pk_fma_f32 v[36:37], v[232:233], v[140:141], v[36:37] op_sel:[1,0,0] op_sel_hi:[1,1,1]
	v_pk_fma_f32 v[38:39], v[232:233], v[142:143], v[38:39] op_sel:[1,0,0] op_sel_hi:[1,1,1]
	v_pk_fma_f32 v[32:33], v[234:235], v[144:145], v[32:33] op_sel_hi:[0,1,1]
	v_pk_fma_f32 v[34:35], v[234:235], v[146:147], v[34:35] op_sel_hi:[0,1,1]
	v_pk_fma_f32 v[36:37], v[234:235], v[148:149], v[36:37] op_sel_hi:[0,1,1]
	v_pk_fma_f32 v[38:39], v[234:235], v[150:151], v[38:39] op_sel_hi:[0,1,1]
	v_pk_fma_f32 v[32:33], v[234:235], v[152:153], v[32:33] op_sel:[1,0,0] op_sel_hi:[1,1,1]
	v_pk_fma_f32 v[34:35], v[234:235], v[154:155], v[34:35] op_sel:[1,0,0] op_sel_hi:[1,1,1]
	v_pk_fma_f32 v[36:37], v[234:235], v[156:157], v[36:37] op_sel:[1,0,0] op_sel_hi:[1,1,1]
	v_pk_fma_f32 v[38:39], v[234:235], v[158:159], v[38:39] op_sel:[1,0,0] op_sel_hi:[1,1,1]
	v_pk_fma_f32 v[32:33], v[236:237], v[160:161], v[32:33] op_sel_hi:[0,1,1]
	v_pk_fma_f32 v[34:35], v[236:237], v[162:163], v[34:35] op_sel_hi:[0,1,1]
	v_pk_fma_f32 v[36:37], v[236:237], v[164:165], v[36:37] op_sel_hi:[0,1,1]
	v_pk_fma_f32 v[38:39], v[236:237], v[166:167], v[38:39] op_sel_hi:[0,1,1]
	v_pk_fma_f32 v[32:33], v[236:237], v[168:169], v[32:33] op_sel:[1,0,0] op_sel_hi:[1,1,1]
	v_pk_fma_f32 v[34:35], v[236:237], v[170:171], v[34:35] op_sel:[1,0,0] op_sel_hi:[1,1,1]
	v_pk_fma_f32 v[36:37], v[236:237], v[172:173], v[36:37] op_sel:[1,0,0] op_sel_hi:[1,1,1]
	v_pk_fma_f32 v[38:39], v[236:237], v[174:175], v[38:39] op_sel:[1,0,0] op_sel_hi:[1,1,1]
	v_pk_fma_f32 v[32:33], v[238:239], v[176:177], v[32:33] op_sel_hi:[0,1,1]
	v_pk_fma_f32 v[34:35], v[238:239], v[178:179], v[34:35] op_sel_hi:[0,1,1]
	v_pk_fma_f32 v[36:37], v[238:239], v[180:181], v[36:37] op_sel_hi:[0,1,1]
	v_pk_fma_f32 v[38:39], v[238:239], v[182:183], v[38:39] op_sel_hi:[0,1,1]
	v_pk_fma_f32 v[32:33], v[238:239], v[184:185], v[32:33] op_sel:[1,0,0] op_sel_hi:[1,1,1]
	v_pk_fma_f32 v[34:35], v[238:239], v[186:187], v[34:35] op_sel:[1,0,0] op_sel_hi:[1,1,1]
	v_pk_fma_f32 v[36:37], v[238:239], v[188:189], v[36:37] op_sel:[1,0,0] op_sel_hi:[1,1,1]
	v_pk_fma_f32 v[38:39], v[238:239], v[190:191], v[38:39] op_sel:[1,0,0] op_sel_hi:[1,1,1]
	v_lshlrev_b32_e32 v232, 16, v116
	v_and_b32_e32 v233, s15, v116
	v_lshlrev_b32_e32 v234, 16, v117
	v_and_b32_e32 v235, s15, v117
	v_lshlrev_b32_e32 v236, 16, v118
	v_and_b32_e32 v237, s15, v118
	v_lshlrev_b32_e32 v238, 16, v119
	v_and_b32_e32 v239, s15, v119
	v_pk_fma_f32 v[202:203], v[232:233], v[232:233], v[202:203]
	v_pk_fma_f32 v[202:203], v[234:235], v[234:235], v[202:203]
	v_pk_fma_f32 v[202:203], v[236:237], v[236:237], v[202:203]
	v_pk_fma_f32 v[202:203], v[238:239], v[238:239], v[202:203]
	v_pk_fma_f32 v[40:41], v[232:233], v[128:129], v[40:41] op_sel_hi:[0,1,1]
	v_pk_fma_f32 v[42:43], v[232:233], v[130:131], v[42:43] op_sel_hi:[0,1,1]
	v_pk_fma_f32 v[44:45], v[232:233], v[132:133], v[44:45] op_sel_hi:[0,1,1]
	v_pk_fma_f32 v[46:47], v[232:233], v[134:135], v[46:47] op_sel_hi:[0,1,1]
	v_pk_fma_f32 v[40:41], v[232:233], v[136:137], v[40:41] op_sel:[1,0,0] op_sel_hi:[1,1,1]
	v_pk_fma_f32 v[42:43], v[232:233], v[138:139], v[42:43] op_sel:[1,0,0] op_sel_hi:[1,1,1]
	v_pk_fma_f32 v[44:45], v[232:233], v[140:141], v[44:45] op_sel:[1,0,0] op_sel_hi:[1,1,1]
	v_pk_fma_f32 v[46:47], v[232:233], v[142:143], v[46:47] op_sel:[1,0,0] op_sel_hi:[1,1,1]
	v_pk_fma_f32 v[40:41], v[234:235], v[144:145], v[40:41] op_sel_hi:[0,1,1]
	v_pk_fma_f32 v[42:43], v[234:235], v[146:147], v[42:43] op_sel_hi:[0,1,1]
; #define LAS __attribute__((address_space(3)))
; __global__ void __launch_bounds__(NTHR, 2) fwd_kernel(Args args) {
;     ...
;             for (int i = 0; i < 16; ++i) { const int k = 2 * lane + 128 * i; f32x2 rv[8]; unsigned xw[8];
; #pragma unroll
;                 for (int e = 0; e < 8; ++e) rv[e] = *(const LAS f32x2*)(Rg + e * DM + k);
; #pragma unroll
;                 for (int q = 0; q < 8; ++q) xw[q] = *(const unsigned*)(XB + (size_t)(t0 + q) * DM + k);
; #pragma unroll
;                 for (int q = 0; q < 8; ++q) { const float x0 = bflo(xw[q]), x1 = bfhi(xw[q]); ssq[q] += x0 * x0 + x1 * x1;
; #pragma unroll
;                     for (int e = 0; e < 8; ++e) acc[q][e] += x0 * rv[e].x + x1 * rv[e].y; } }
	v_pk_fma_f32 v[44:45], v[234:235], v[148:149], v[44:45] op_sel_hi:[0,1,1]
	v_pk_fma_f32 v[46:47], v[234:235], v[150:151], v[46:47] op_sel_hi:[0,1,1]
	v_pk_fma_f32 v[40:41], v[234:235], v[152:153], v[40:41] op_sel:[1,0,0] op_sel_hi:[1,1,1]
	v_pk_fma_f32 v[42:43], v[234:235], v[154:155], v[42:43] op_sel:[1,0,0] op_sel_hi:[1,1,1]
	v_pk_fma_f32 v[44:45], v[234:235], v[156:157], v[44:45] op_sel:[1,0,0] op_sel_hi:[1,1,1]
	v_pk_fma_f32 v[46:47], v[234:235], v[158:159], v[46:47] op_sel:[1,0,0] op_sel_hi:[1,1,1]
	v_pk_fma_f32 v[40:41], v[236:237], v[160:161], v[40:41] op_sel_hi:[0,1,1]
	v_pk_fma_f32 v[42:43], v[236:237], v[162:163], v[42:43] op_sel_hi:[0,1,1]
	v_pk_fma_f32 v[44:45], v[236:237], v[164:165], v[44:45] op_sel_hi:[0,1,1]
	v_pk_fma_f32 v[46:47], v[236:237], v[166:167], v[46:47] op_sel_hi:[0,1,1]
	v_pk_fma_f32 v[40:41], v[236:237], v[168:169], v[40:41] op_sel:[1,0,0] op_sel_hi:[1,1,1]
	v_pk_fma_f32 v[42:43], v[236:237], v[170:171], v[42:43] op_sel:[1,0,0] op_sel_hi:[1,1,1]
	v_pk_fma_f32 v[44:45], v[236:237], v[172:173], v[44:45] op_sel:[1,0,0] op_sel_hi:[1,1,1]
	v_pk_fma_f32 v[46:47], v[236:237], v[174:175], v[46:47] op_sel:[1,0,0] op_sel_hi:[1,1,1]
	v_pk_fma_f32 v[40:41], v[238:239], v[176:177], v[40:41] op_sel_hi:[0,1,1]
	v_pk_fma_f32 v[42:43], v[238:239], v[178:179], v[42:43] op_sel_hi:[0,1,1]
	v_pk_fma_f32 v[44:45], v[238:239], v[180:181], v[44:45] op_sel_hi:[0,1,1]
	v_pk_fma_f32 v[46:47], v[238:239], v[182:183], v[46:47] op_sel_hi:[0,1,1]
	v_pk_fma_f32 v[40:41], v[238:239], v[184:185], v[40:41] op_sel:[1,0,0] op_sel_hi:[1,1,1]
	v_pk_fma_f32 v[42:43], v[238:239], v[186:187], v[42:43] op_sel:[1,0,0] op_sel_hi:[1,1,1]
	v_pk_fma_f32 v[44:45], v[238:239], v[188:189], v[44:45] op_sel:[1,0,0] op_sel_hi:[1,1,1]
	v_pk_fma_f32 v[46:47], v[238:239], v[190:191], v[46:47] op_sel:[1,0,0] op_sel_hi:[1,1,1]
	v_lshlrev_b32_e32 v232, 16, v120
	v_and_b32_e32 v233, s15, v120
	v_lshlrev_b32_e32 v234, 16, v121
	v_and_b32_e32 v235, s15, v121
	v_lshlrev_b32_e32 v236, 16, v122
	v_and_b32_e32 v237, s15, v122
	v_lshlrev_b32_e32 v238, 16, v123
	v_and_b32_e32 v239, s15, v123
	v_pk_fma_f32 v[204:205], v[232:233], v[232:233], v[204:205]
	v_pk_fma_f32 v[204:205], v[234:235], v[234:235], v[204:205]
	v_pk_fma_f32 v[204:205], v[236:237], v[236:237], v[204:205]
	v_pk_fma_f32 v[204:205], v[238:239], v[238:239], v[204:205]
	v_pk_fma_f32 v[48:49], v[232:233], v[128:129], v[48:49] op_sel_hi:[0,1,1]
	v_pk_fma_f32 v[50:51], v[232:233], v[130:131], v[50:51] op_sel_hi:[0,1,1]
	v_pk_fma_f32 v[52:53], v[232:233], v[132:133], v[52:53] op_sel_hi:[0,1,1]
	v_pk_fma_f32 v[54:55], v[232:233], v[134:135], v[54:55] op_sel_hi:[0,1,1]
	v_pk_fma_f32 v[48:49], v[232:233], v[136:137], v[48:49] op_sel:[1,0,0] op_sel_hi:[1,1,1]
	v_pk_fma_f32 v[50:51], v[232:233], v[138:139], v[50:51] op_sel:[1,0,0] op_sel_hi:[1,1,1]
	v_pk_fma_f32 v[52:53], v[232:233], v[140:141], v[52:53] op_sel:[1,0,0] op_sel_hi:[1,1,1]
	v_pk_fma_f32 v[54:55], v[232:233], v[142:143], v[54:55] op_sel:[1,0,0] op_sel_hi:[1,1,1]
	v_pk_fma_f32 v[48:49], v[234:235], v[144:145], v[48:49] op_sel_hi:[0,1,1]
	v_pk_fma_f32 v[50:51], v[234:235], v[146:147], v[50:51] op_sel_hi:[0,1,1]
	v_pk_fma_f32 v[52:53], v[234:235], v[148:149], v[52:53] op_sel_hi:[0,1,1]
	v_pk_fma_f32 v[54:55], v[234:235], v[150:151], v[54:55] op_sel_hi:[0,1,1]
	v_pk_fma_f32 v[48:49], v[234:235], v[152:153], v[48:49] op_sel:[1,0,0] op_sel_hi:[1,1,1]
	v_pk_fma_f32 v[50:51], v[234:235], v[154:155], v[50:51] op_sel:[1,0,0] op_sel_hi:[1,1,1]
	v_pk_fma_f32 v[52:53], v[234:235], v[156:157], v[52:53] op_sel:[1,0,0] op_sel_hi:[1,1,1]
	v_pk_fma_f32 v[54:55], v[234:235], v[158:159], v[54:55] op_sel:[1,0,0] op_sel_hi:[1,1,1]
	v_pk_fma_f32 v[48:49], v[236:237], v[160:161], v[48:49] op_sel_hi:[0,1,1]
	v_pk_fma_f32 v[50:51], v[236:237], v[162:163], v[50:51] op_sel_hi:[0,1,1]
	v_pk_fma_f32 v[52:53], v[236:237], v[164:165], v[52:53] op_sel_hi:[0,1,1]
	v_pk_fma_f32 v[54:55], v[236:237], v[166:167], v[54:55] op_sel_hi:[0,1,1]
	v_pk_fma_f32 v[48:49], v[236:237], v[168:169], v[48:49] op_sel:[1,0,0] op_sel_hi:[1,1,1]
	v_pk_fma_f32 v[50:51], v[236:237], v[170:171], v[50:51] op_sel:[1,0,0] op_sel_hi:[1,1,1]
	v_pk_fma_f32 v[52:53], v[236:237], v[172:173], v[52:53] op_sel:[1,0,0] op_sel_hi:[1,1,1]
	v_pk_fma_f32 v[54:55], v[236:237], v[174:175], v[54:55] op_sel:[1,0,0] op_sel_hi:[1,1,1]
	v_pk_fma_f32 v[48:49], v[238:239], v[176:177], v[48:49] op_sel_hi:[0,1,1]
	v_pk_fma_f32 v[50:51], v[238:239], v[178:179], v[50:51] op_sel_hi:[0,1,1]
	v_pk_fma_f32 v[52:53], v[238:239], v[180:181], v[52:53] op_sel_hi:[0,1,1]
	v_pk_fma_f32 v[54:55], v[238:239], v[182:183], v[54:55] op_sel_hi:[0,1,1]
	v_pk_fma_f32 v[48:49], v[238:239], v[184:185], v[48:49] op_sel:[1,0,0] op_sel_hi:[1,1,1]
	v_pk_fma_f32 v[50:51], v[238:239], v[186:187], v[50:51] op_sel:[1,0,0] op_sel_hi:[1,1,1]
	v_pk_fma_f32 v[52:53], v[238:239], v[188:189], v[52:53] op_sel:[1,0,0] op_sel_hi:[1,1,1]
	v_pk_fma_f32 v[54:55], v[238:239], v[190:191], v[54:55] op_sel:[1,0,0] op_sel_hi:[1,1,1]
	v_lshlrev_b32_e32 v232, 16, v124
	v_and_b32_e32 v233, s15, v124
	v_lshlrev_b32_e32 v234, 16, v125
	v_and_b32_e32 v235, s15, v125
	v_lshlrev_b32_e32 v236, 16, v126
	v_and_b32_e32 v237, s15, v126
	v_lshlrev_b32_e32 v238, 16, v127
	v_and_b32_e32 v239, s15, v127
	v_pk_fma_f32 v[206:207], v[232:233], v[232:233], v[206:207]
	v_pk_fma_f32 v[206:207], v[234:235], v[234:235], v[206:207]
	v_pk_fma_f32 v[206:207], v[236:237], v[236:237], v[206:207]
	v_pk_fma_f32 v[206:207], v[238:239], v[238:239], v[206:207]
	v_pk_fma_f32 v[56:57], v[232:233], v[128:129], v[56:57] op_sel_hi:[0,1,1]
	v_pk_fma_f32 v[58:59], v[232:233], v[130:131], v[58:59] op_sel_hi:[0,1,1]
; __device__ __forceinline__ float wave_sum(float v) {
; #pragma unroll
;     for (int o = 1; o < 64; o <<= 1) v += __shfl_xor(v, o);
;     return v;
; __global__ void __launch_bounds__(NTHR, 2) fwd_kernel(Args args) {
;     ...
;                     for (int e = 0; e < 8; ++e) acc[q][e] += x0 * rv[e].x + x1 * rv[e].y; } }
;     ...
;             for (int q = 0; q < 8; ++q) { const float sq = wave_sum(ssq[q]); const float rs = 1.0f / sqrtf(sq * (1.0f / DM) + EPS);
;                 float lg[8];
; #pragma unroll
;                 for (int e = 0; e < 8; ++e) lg[e] = wave_sum(acc[q][e]) * rs;
	v_pk_fma_f32 v[60:61], v[232:233], v[132:133], v[60:61] op_sel_hi:[0,1,1]
	v_pk_fma_f32 v[62:63], v[232:233], v[134:135], v[62:63] op_sel_hi:[0,1,1]
	v_pk_fma_f32 v[56:57], v[232:233], v[136:137], v[56:57] op_sel:[1,0,0] op_sel_hi:[1,1,1]
	v_pk_fma_f32 v[58:59], v[232:233], v[138:139], v[58:59] op_sel:[1,0,0] op_sel_hi:[1,1,1]
	v_pk_fma_f32 v[60:61], v[232:233], v[140:141], v[60:61] op_sel:[1,0,0] op_sel_hi:[1,1,1]
	v_pk_fma_f32 v[62:63], v[232:233], v[142:143], v[62:63] op_sel:[1,0,0] op_sel_hi:[1,1,1]
	v_pk_fma_f32 v[56:57], v[234:235], v[144:145], v[56:57] op_sel_hi:[0,1,1]
	v_pk_fma_f32 v[58:59], v[234:235], v[146:147], v[58:59] op_sel_hi:[0,1,1]
	v_pk_fma_f32 v[60:61], v[234:235], v[148:149], v[60:61] op_sel_hi:[0,1,1]
	v_pk_fma_f32 v[62:63], v[234:235], v[150:151], v[62:63] op_sel_hi:[0,1,1]
	v_pk_fma_f32 v[56:57], v[234:235], v[152:153], v[56:57] op_sel:[1,0,0] op_sel_hi:[1,1,1]
	v_pk_fma_f32 v[58:59], v[234:235], v[154:155], v[58:59] op_sel:[1,0,0] op_sel_hi:[1,1,1]
	v_pk_fma_f32 v[60:61], v[234:235], v[156:157], v[60:61] op_sel:[1,0,0] op_sel_hi:[1,1,1]
	v_pk_fma_f32 v[62:63], v[234:235], v[158:159], v[62:63] op_sel:[1,0,0] op_sel_hi:[1,1,1]
	v_pk_fma_f32 v[56:57], v[236:237], v[160:161], v[56:57] op_sel_hi:[0,1,1]
	v_pk_fma_f32 v[58:59], v[236:237], v[162:163], v[58:59] op_sel_hi:[0,1,1]
	v_pk_fma_f32 v[60:61], v[236:237], v[164:165], v[60:61] op_sel_hi:[0,1,1]
	v_pk_fma_f32 v[62:63], v[236:237], v[166:167], v[62:63] op_sel_hi:[0,1,1]
	v_pk_fma_f32 v[56:57], v[236:237], v[168:169], v[56:57] op_sel:[1,0,0] op_sel_hi:[1,1,1]
	v_pk_fma_f32 v[58:59], v[236:237], v[170:171], v[58:59] op_sel:[1,0,0] op_sel_hi:[1,1,1]
	v_pk_fma_f32 v[60:61], v[236:237], v[172:173], v[60:61] op_sel:[1,0,0] op_sel_hi:[1,1,1]
	v_pk_fma_f32 v[62:63], v[236:237], v[174:175], v[62:63] op_sel:[1,0,0] op_sel_hi:[1,1,1]
	v_pk_fma_f32 v[56:57], v[238:239], v[176:177], v[56:57] op_sel_hi:[0,1,1]
	v_pk_fma_f32 v[58:59], v[238:239], v[178:179], v[58:59] op_sel_hi:[0,1,1]
	v_pk_fma_f32 v[60:61], v[238:239], v[180:181], v[60:61] op_sel_hi:[0,1,1]
	v_pk_fma_f32 v[62:63], v[238:239], v[182:183], v[62:63] op_sel_hi:[0,1,1]
	v_pk_fma_f32 v[56:57], v[238:239], v[184:185], v[56:57] op_sel:[1,0,0] op_sel_hi:[1,1,1]
	v_pk_fma_f32 v[58:59], v[238:239], v[186:187], v[58:59] op_sel:[1,0,0] op_sel_hi:[1,1,1]
	v_pk_fma_f32 v[60:61], v[238:239], v[188:189], v[60:61] op_sel:[1,0,0] op_sel_hi:[1,1,1]
	v_pk_fma_f32 v[62:63], v[238:239], v[190:191], v[62:63] op_sel:[1,0,0] op_sel_hi:[1,1,1]
	v_add_f32_e32 v192, v192, v193
	v_add_f32_e32 v194, v194, v195
	v_add_f32_e32 v196, v196, v197
	v_add_f32_e32 v198, v198, v199
	v_add_f32_e32 v200, v200, v201
	v_add_f32_e32 v202, v202, v203
	v_add_f32_e32 v204, v204, v205
	v_add_f32_e32 v206, v206, v207
	v_add_f32_dpp v0, v0, v0 quad_perm:[1,0,3,2] row_mask:0xf bank_mask:0xf
	v_add_f32_dpp v1, v1, v1 quad_perm:[1,0,3,2] row_mask:0xf bank_mask:0xf
	v_add_f32_dpp v2, v2, v2 quad_perm:[1,0,3,2] row_mask:0xf bank_mask:0xf
	v_add_f32_dpp v3, v3, v3 quad_perm:[1,0,3,2] row_mask:0xf bank_mask:0xf
	v_add_f32_dpp v4, v4, v4 quad_perm:[1,0,3,2] row_mask:0xf bank_mask:0xf
	v_add_f32_dpp v5, v5, v5 quad_perm:[1,0,3,2] row_mask:0xf bank_mask:0xf
	v_add_f32_dpp v6, v6, v6 quad_perm:[1,0,3,2] row_mask:0xf bank_mask:0xf
	v_add_f32_dpp v7, v7, v7 quad_perm:[1,0,3,2] row_mask:0xf bank_mask:0xf
	v_add_f32_dpp v8, v8, v8 quad_perm:[1,0,3,2] row_mask:0xf bank_mask:0xf
	v_add_f32_dpp v9, v9, v9 quad_perm:[1,0,3,2] row_mask:0xf bank_mask:0xf
	v_add_f32_dpp v10, v10, v10 quad_perm:[1,0,3,2] row_mask:0xf bank_mask:0xf
	v_add_f32_dpp v11, v11, v11 quad_perm:[1,0,3,2] row_mask:0xf bank_mask:0xf
	v_add_f32_dpp v12, v12, v12 quad_perm:[1,0,3,2] row_mask:0xf bank_mask:0xf
	v_add_f32_dpp v13, v13, v13 quad_perm:[1,0,3,2] row_mask:0xf bank_mask:0xf
	v_add_f32_dpp v14, v14, v14 quad_perm:[1,0,3,2] row_mask:0xf bank_mask:0xf
	v_add_f32_dpp v15, v15, v15 quad_perm:[1,0,3,2] row_mask:0xf bank_mask:0xf
	v_add_f32_dpp v16, v16, v16 quad_perm:[1,0,3,2] row_mask:0xf bank_mask:0xf
	v_add_f32_dpp v17, v17, v17 quad_perm:[1,0,3,2] row_mask:0xf bank_mask:0xf
	v_add_f32_dpp v18, v18, v18 quad_perm:[1,0,3,2] row_mask:0xf bank_mask:0xf
	v_add_f32_dpp v19, v19, v19 quad_perm:[1,0,3,2] row_mask:0xf bank_mask:0xf
	v_add_f32_dpp v20, v20, v20 quad_perm:[1,0,3,2] row_mask:0xf bank_mask:0xf
	v_add_f32_dpp v21, v21, v21 quad_perm:[1,0,3,2] row_mask:0xf bank_mask:0xf
	v_add_f32_dpp v22, v22, v22 quad_perm:[1,0,3,2] row_mask:0xf bank_mask:0xf
	v_add_f32_dpp v23, v23, v23 quad_perm:[1,0,3,2] row_mask:0xf bank_mask:0xf
	v_add_f32_dpp v24, v24, v24 quad_perm:[1,0,3,2] row_mask:0xf bank_mask:0xf
	v_add_f32_dpp v25, v25, v25 quad_perm:[1,0,3,2] row_mask:0xf bank_mask:0xf
	v_add_f32_dpp v26, v26, v26 quad_perm:[1,0,3,2] row_mask:0xf bank_mask:0xf
	v_add_f32_dpp v27, v27, v27 quad_perm:[1,0,3,2] row_mask:0xf bank_mask:0xf
	v_add_f32_dpp v28, v28, v28 quad_perm:[1,0,3,2] row_mask:0xf bank_mask:0xf
	v_add_f32_dpp v29, v29, v29 quad_perm:[1,0,3,2] row_mask:0xf bank_mask:0xf
	v_add_f32_dpp v30, v30, v30 quad_perm:[1,0,3,2] row_mask:0xf bank_mask:0xf
	v_add_f32_dpp v31, v31, v31 quad_perm:[1,0,3,2] row_mask:0xf bank_mask:0xf
	v_add_f32_dpp v32, v32, v32 quad_perm:[1,0,3,2] row_mask:0xf bank_mask:0xf
	v_add_f32_dpp v33, v33, v33 quad_perm:[1,0,3,2] row_mask:0xf bank_mask:0xf
	v_add_f32_dpp v34, v34, v34 quad_perm:[1,0,3,2] row_mask:0xf bank_mask:0xf
	v_add_f32_dpp v35, v35, v35 quad_perm:[1,0,3,2] row_mask:0xf bank_mask:0xf
	v_add_f32_dpp v36, v36, v36 quad_perm:[1,0,3,2] row_mask:0xf bank_mask:0xf
	v_add_f32_dpp v37, v37, v37 quad_perm:[1,0,3,2] row_mask:0xf bank_mask:0xf
; __device__ __forceinline__ float wave_sum(float v) {
; #pragma unroll
;     for (int o = 1; o < 64; o <<= 1) v += __shfl_xor(v, o);
;     return v;
; __global__ void __launch_bounds__(NTHR, 2) fwd_kernel(Args args) {
;     ...
;             for (int q = 0; q < 8; ++q) { const float sq = wave_sum(ssq[q]); const float rs = 1.0f / sqrtf(sq * (1.0f / DM) + EPS);
;                 float lg[8];
; #pragma unroll
;                 for (int e = 0; e < 8; ++e) lg[e] = wave_sum(acc[q][e]) * rs;
	v_add_f32_dpp v38, v38, v38 quad_perm:[1,0,3,2] row_mask:0xf bank_mask:0xf
	v_add_f32_dpp v39, v39, v39 quad_perm:[1,0,3,2] row_mask:0xf bank_mask:0xf
	v_add_f32_dpp v40, v40, v40 quad_perm:[1,0,3,2] row_mask:0xf bank_mask:0xf
	v_add_f32_dpp v41, v41, v41 quad_perm:[1,0,3,2] row_mask:0xf bank_mask:0xf
	v_add_f32_dpp v42, v42, v42 quad_perm:[1,0,3,2] row_mask:0xf bank_mask:0xf
	v_add_f32_dpp v43, v43, v43 quad_perm:[1,0,3,2] row_mask:0xf bank_mask:0xf
	v_add_f32_dpp v44, v44, v44 quad_perm:[1,0,3,2] row_mask:0xf bank_mask:0xf
	v_add_f32_dpp v45, v45, v45 quad_perm:[1,0,3,2] row_mask:0xf bank_mask:0xf
	v_add_f32_dpp v46, v46, v46 quad_perm:[1,0,3,2] row_mask:0xf bank_mask:0xf
	v_add_f32_dpp v47, v47, v47 quad_perm:[1,0,3,2] row_mask:0xf bank_mask:0xf
	v_add_f32_dpp v48, v48, v48 quad_perm:[1,0,3,2] row_mask:0xf bank_mask:0xf
	v_add_f32_dpp v49, v49, v49 quad_perm:[1,0,3,2] row_mask:0xf bank_mask:0xf
	v_add_f32_dpp v50, v50, v50 quad_perm:[1,0,3,2] row_mask:0xf bank_mask:0xf
	v_add_f32_dpp v51, v51, v51 quad_perm:[1,0,3,2] row_mask:0xf bank_mask:0xf
	v_add_f32_dpp v52, v52, v52 quad_perm:[1,0,3,2] row_mask:0xf bank_mask:0xf
	v_add_f32_dpp v53, v53, v53 quad_perm:[1,0,3,2] row_mask:0xf bank_mask:0xf
	v_add_f32_dpp v54, v54, v54 quad_perm:[1,0,3,2] row_mask:0xf bank_mask:0xf
	v_add_f32_dpp v55, v55, v55 quad_perm:[1,0,3,2] row_mask:0xf bank_mask:0xf
	v_add_f32_dpp v56, v56, v56 quad_perm:[1,0,3,2] row_mask:0xf bank_mask:0xf
	v_add_f32_dpp v57, v57, v57 quad_perm:[1,0,3,2] row_mask:0xf bank_mask:0xf
	v_add_f32_dpp v58, v58, v58 quad_perm:[1,0,3,2] row_mask:0xf bank_mask:0xf
	v_add_f32_dpp v59, v59, v59 quad_perm:[1,0,3,2] row_mask:0xf bank_mask:0xf
	v_add_f32_dpp v60, v60, v60 quad_perm:[1,0,3,2] row_mask:0xf bank_mask:0xf
	v_add_f32_dpp v61, v61, v61 quad_perm:[1,0,3,2] row_mask:0xf bank_mask:0xf
	v_add_f32_dpp v62, v62, v62 quad_perm:[1,0,3,2] row_mask:0xf bank_mask:0xf
	v_add_f32_dpp v63, v63, v63 quad_perm:[1,0,3,2] row_mask:0xf bank_mask:0xf
	v_add_f32_dpp v192, v192, v192 quad_perm:[1,0,3,2] row_mask:0xf bank_mask:0xf
	v_add_f32_dpp v194, v194, v194 quad_perm:[1,0,3,2] row_mask:0xf bank_mask:0xf
	v_add_f32_dpp v196, v196, v196 quad_perm:[1,0,3,2] row_mask:0xf bank_mask:0xf
	v_add_f32_dpp v198, v198, v198 quad_perm:[1,0,3,2] row_mask:0xf bank_mask:0xf
	v_add_f32_dpp v200, v200, v200 quad_perm:[1,0,3,2] row_mask:0xf bank_mask:0xf
	v_add_f32_dpp v202, v202, v202 quad_perm:[1,0,3,2] row_mask:0xf bank_mask:0xf
	v_add_f32_dpp v204, v204, v204 quad_perm:[1,0,3,2] row_mask:0xf bank_mask:0xf
	v_add_f32_dpp v206, v206, v206 quad_perm:[1,0,3,2] row_mask:0xf bank_mask:0xf
	v_add_f32_dpp v0, v0, v0 quad_perm:[2,3,0,1] row_mask:0xf bank_mask:0xf
	v_add_f32_dpp v1, v1, v1 quad_perm:[2,3,0,1] row_mask:0xf bank_mask:0xf
	v_add_f32_dpp v2, v2, v2 quad_perm:[2,3,0,1] row_mask:0xf bank_mask:0xf
	v_add_f32_dpp v3, v3, v3 quad_perm:[2,3,0,1] row_mask:0xf bank_mask:0xf
	v_add_f32_dpp v4, v4, v4 quad_perm:[2,3,0,1] row_mask:0xf bank_mask:0xf
	v_add_f32_dpp v5, v5, v5 quad_perm:[2,3,0,1] row_mask:0xf bank_mask:0xf
	v_add_f32_dpp v6, v6, v6 quad_perm:[2,3,0,1] row_mask:0xf bank_mask:0xf
	v_add_f32_dpp v7, v7, v7 quad_perm:[2,3,0,1] row_mask:0xf bank_mask:0xf
	v_add_f32_dpp v8, v8, v8 quad_perm:[2,3,0,1] row_mask:0xf bank_mask:0xf
	v_add_f32_dpp v9, v9, v9 quad_perm:[2,3,0,1] row_mask:0xf bank_mask:0xf
	v_add_f32_dpp v10, v10, v10 quad_perm:[2,3,0,1] row_mask:0xf bank_mask:0xf
	v_add_f32_dpp v11, v11, v11 quad_perm:[2,3,0,1] row_mask:0xf bank_mask:0xf
	v_add_f32_dpp v12, v12, v12 quad_perm:[2,3,0,1] row_mask:0xf bank_mask:0xf
	v_add_f32_dpp v13, v13, v13 quad_perm:[2,3,0,1] row_mask:0xf bank_mask:0xf
	v_add_f32_dpp v14, v14, v14 quad_perm:[2,3,0,1] row_mask:0xf bank_mask:0xf
	v_add_f32_dpp v15, v15, v15 quad_perm:[2,3,0,1] row_mask:0xf bank_mask:0xf
	v_add_f32_dpp v16, v16, v16 quad_perm:[2,3,0,1] row_mask:0xf bank_mask:0xf
	v_add_f32_dpp v17, v17, v17 quad_perm:[2,3,0,1] row_mask:0xf bank_mask:0xf
	v_add_f32_dpp v18, v18, v18 quad_perm:[2,3,0,1] row_mask:0xf bank_mask:0xf
	v_add_f32_dpp v19, v19, v19 quad_perm:[2,3,0,1] row_mask:0xf bank_mask:0xf
	v_add_f32_dpp v20, v20, v20 quad_perm:[2,3,0,1] row_mask:0xf bank_mask:0xf
	v_add_f32_dpp v21, v21, v21 quad_perm:[2,3,0,1] row_mask:0xf bank_mask:0xf
	v_add_f32_dpp v22, v22, v22 quad_perm:[2,3,0,1] row_mask:0xf bank_mask:0xf
	v_add_f32_dpp v23, v23, v23 quad_perm:[2,3,0,1] row_mask:0xf bank_mask:0xf
	v_add_f32_dpp v24, v24, v24 quad_perm:[2,3,0,1] row_mask:0xf bank_mask:0xf
	v_add_f32_dpp v25, v25, v25 quad_perm:[2,3,0,1] row_mask:0xf bank_mask:0xf
	v_add_f32_dpp v26, v26, v26 quad_perm:[2,3,0,1] row_mask:0xf bank_mask:0xf
	v_add_f32_dpp v27, v27, v27 quad_perm:[2,3,0,1] row_mask:0xf bank_mask:0xf
	v_add_f32_dpp v28, v28, v28 quad_perm:[2,3,0,1] row_mask:0xf bank_mask:0xf
	v_add_f32_dpp v29, v29, v29 quad_perm:[2,3,0,1] row_mask:0xf bank_mask:0xf
	v_add_f32_dpp v30, v30, v30 quad_perm:[2,3,0,1] row_mask:0xf bank_mask:0xf
	v_add_f32_dpp v31, v31, v31 quad_perm:[2,3,0,1] row_mask:0xf bank_mask:0xf
	v_add_f32_dpp v32, v32, v32 quad_perm:[2,3,0,1] row_mask:0xf bank_mask:0xf
	v_add_f32_dpp v33, v33, v33 quad_perm:[2,3,0,1] row_mask:0xf bank_mask:0xf
	v_add_f32_dpp v34, v34, v34 quad_perm:[2,3,0,1] row_mask:0xf bank_mask:0xf
	v_add_f32_dpp v35, v35, v35 quad_perm:[2,3,0,1] row_mask:0xf bank_mask:0xf
	v_add_f32_dpp v36, v36, v36 quad_perm:[2,3,0,1] row_mask:0xf bank_mask:0xf
	v_add_f32_dpp v37, v37, v37 quad_perm:[2,3,0,1] row_mask:0xf bank_mask:0xf
	v_add_f32_dpp v38, v38, v38 quad_perm:[2,3,0,1] row_mask:0xf bank_mask:0xf
	v_add_f32_dpp v39, v39, v39 quad_perm:[2,3,0,1] row_mask:0xf bank_mask:0xf
; __device__ __forceinline__ float wave_sum(float v) {
; #pragma unroll
;     for (int o = 1; o < 64; o <<= 1) v += __shfl_xor(v, o);
;     return v;
; __global__ void __launch_bounds__(NTHR, 2) fwd_kernel(Args args) {
;     ...
;             for (int q = 0; q < 8; ++q) { const float sq = wave_sum(ssq[q]); const float rs = 1.0f / sqrtf(sq * (1.0f / DM) + EPS);
;                 float lg[8];
; #pragma unroll
;                 for (int e = 0; e < 8; ++e) lg[e] = wave_sum(acc[q][e]) * rs;
	v_add_f32_dpp v40, v40, v40 quad_perm:[2,3,0,1] row_mask:0xf bank_mask:0xf
	v_add_f32_dpp v41, v41, v41 quad_perm:[2,3,0,1] row_mask:0xf bank_mask:0xf
	v_add_f32_dpp v42, v42, v42 quad_perm:[2,3,0,1] row_mask:0xf bank_mask:0xf
	v_add_f32_dpp v43, v43, v43 quad_perm:[2,3,0,1] row_mask:0xf bank_mask:0xf
	v_add_f32_dpp v44, v44, v44 quad_perm:[2,3,0,1] row_mask:0xf bank_mask:0xf
	v_add_f32_dpp v45, v45, v45 quad_perm:[2,3,0,1] row_mask:0xf bank_mask:0xf
	v_add_f32_dpp v46, v46, v46 quad_perm:[2,3,0,1] row_mask:0xf bank_mask:0xf
	v_add_f32_dpp v47, v47, v47 quad_perm:[2,3,0,1] row_mask:0xf bank_mask:0xf
	v_add_f32_dpp v48, v48, v48 quad_perm:[2,3,0,1] row_mask:0xf bank_mask:0xf
	v_add_f32_dpp v49, v49, v49 quad_perm:[2,3,0,1] row_mask:0xf bank_mask:0xf
	v_add_f32_dpp v50, v50, v50 quad_perm:[2,3,0,1] row_mask:0xf bank_mask:0xf
	v_add_f32_dpp v51, v51, v51 quad_perm:[2,3,0,1] row_mask:0xf bank_mask:0xf
	v_add_f32_dpp v52, v52, v52 quad_perm:[2,3,0,1] row_mask:0xf bank_mask:0xf
	v_add_f32_dpp v53, v53, v53 quad_perm:[2,3,0,1] row_mask:0xf bank_mask:0xf
	v_add_f32_dpp v54, v54, v54 quad_perm:[2,3,0,1] row_mask:0xf bank_mask:0xf
	v_add_f32_dpp v55, v55, v55 quad_perm:[2,3,0,1] row_mask:0xf bank_mask:0xf
	v_add_f32_dpp v56, v56, v56 quad_perm:[2,3,0,1] row_mask:0xf bank_mask:0xf
	v_add_f32_dpp v57, v57, v57 quad_perm:[2,3,0,1] row_mask:0xf bank_mask:0xf
	v_add_f32_dpp v58, v58, v58 quad_perm:[2,3,0,1] row_mask:0xf bank_mask:0xf
	v_add_f32_dpp v59, v59, v59 quad_perm:[2,3,0,1] row_mask:0xf bank_mask:0xf
	v_add_f32_dpp v60, v60, v60 quad_perm:[2,3,0,1] row_mask:0xf bank_mask:0xf
	v_add_f32_dpp v61, v61, v61 quad_perm:[2,3,0,1] row_mask:0xf bank_mask:0xf
	v_add_f32_dpp v62, v62, v62 quad_perm:[2,3,0,1] row_mask:0xf bank_mask:0xf
	v_add_f32_dpp v63, v63, v63 quad_perm:[2,3,0,1] row_mask:0xf bank_mask:0xf
	v_add_f32_dpp v192, v192, v192 quad_perm:[2,3,0,1] row_mask:0xf bank_mask:0xf
	v_add_f32_dpp v194, v194, v194 quad_perm:[2,3,0,1] row_mask:0xf bank_mask:0xf
	v_add_f32_dpp v196, v196, v196 quad_perm:[2,3,0,1] row_mask:0xf bank_mask:0xf
	v_add_f32_dpp v198, v198, v198 quad_perm:[2,3,0,1] row_mask:0xf bank_mask:0xf
	v_add_f32_dpp v200, v200, v200 quad_perm:[2,3,0,1] row_mask:0xf bank_mask:0xf
	v_add_f32_dpp v202, v202, v202 quad_perm:[2,3,0,1] row_mask:0xf bank_mask:0xf
	v_add_f32_dpp v204, v204, v204 quad_perm:[2,3,0,1] row_mask:0xf bank_mask:0xf
	v_add_f32_dpp v206, v206, v206 quad_perm:[2,3,0,1] row_mask:0xf bank_mask:0xf
	v_add_f32_dpp v0, v0, v0 row_half_mirror row_mask:0xf bank_mask:0xf
	v_add_f32_dpp v1, v1, v1 row_half_mirror row_mask:0xf bank_mask:0xf
	v_add_f32_dpp v2, v2, v2 row_half_mirror row_mask:0xf bank_mask:0xf
	v_add_f32_dpp v3, v3, v3 row_half_mirror row_mask:0xf bank_mask:0xf
	v_add_f32_dpp v4, v4, v4 row_half_mirror row_mask:0xf bank_mask:0xf
	v_add_f32_dpp v5, v5, v5 row_half_mirror row_mask:0xf bank_mask:0xf
	v_add_f32_dpp v6, v6, v6 row_half_mirror row_mask:0xf bank_mask:0xf
	v_add_f32_dpp v7, v7, v7 row_half_mirror row_mask:0xf bank_mask:0xf
	v_add_f32_dpp v8, v8, v8 row_half_mirror row_mask:0xf bank_mask:0xf
	v_add_f32_dpp v9, v9, v9 row_half_mirror row_mask:0xf bank_mask:0xf
	v_add_f32_dpp v10, v10, v10 row_half_mirror row_mask:0xf bank_mask:0xf
	v_add_f32_dpp v11, v11, v11 row_half_mirror row_mask:0xf bank_mask:0xf
	v_add_f32_dpp v12, v12, v12 row_half_mirror row_mask:0xf bank_mask:0xf
	v_add_f32_dpp v13, v13, v13 row_half_mirror row_mask:0xf bank_mask:0xf
	v_add_f32_dpp v14, v14, v14 row_half_mirror row_mask:0xf bank_mask:0xf
	v_add_f32_dpp v15, v15, v15 row_half_mirror row_mask:0xf bank_mask:0xf
	v_add_f32_dpp v16, v16, v16 row_half_mirror row_mask:0xf bank_mask:0xf
	v_add_f32_dpp v17, v17, v17 row_half_mirror row_mask:0xf bank_mask:0xf
	v_add_f32_dpp v18, v18, v18 row_half_mirror row_mask:0xf bank_mask:0xf
	v_add_f32_dpp v19, v19, v19 row_half_mirror row_mask:0xf bank_mask:0xf
	v_add_f32_dpp v20, v20, v20 row_half_mirror row_mask:0xf bank_mask:0xf
	v_add_f32_dpp v21, v21, v21 row_half_mirror row_mask:0xf bank_mask:0xf
	v_add_f32_dpp v22, v22, v22 row_half_mirror row_mask:0xf bank_mask:0xf
	v_add_f32_dpp v23, v23, v23 row_half_mirror row_mask:0xf bank_mask:0xf
	v_add_f32_dpp v24, v24, v24 row_half_mirror row_mask:0xf bank_mask:0xf
	v_add_f32_dpp v25, v25, v25 row_half_mirror row_mask:0xf bank_mask:0xf
	v_add_f32_dpp v26, v26, v26 row_half_mirror row_mask:0xf bank_mask:0xf
	v_add_f32_dpp v27, v27, v27 row_half_mirror row_mask:0xf bank_mask:0xf
	v_add_f32_dpp v28, v28, v28 row_half_mirror row_mask:0xf bank_mask:0xf
	v_add_f32_dpp v29, v29, v29 row_half_mirror row_mask:0xf bank_mask:0xf
	v_add_f32_dpp v30, v30, v30 row_half_mirror row_mask:0xf bank_mask:0xf
	v_add_f32_dpp v31, v31, v31 row_half_mirror row_mask:0xf bank_mask:0xf
	v_add_f32_dpp v32, v32, v32 row_half_mirror row_mask:0xf bank_mask:0xf
	v_add_f32_dpp v33, v33, v33 row_half_mirror row_mask:0xf bank_mask:0xf
	v_add_f32_dpp v34, v34, v34 row_half_mirror row_mask:0xf bank_mask:0xf
	v_add_f32_dpp v35, v35, v35 row_half_mirror row_mask:0xf bank_mask:0xf
	v_add_f32_dpp v36, v36, v36 row_half_mirror row_mask:0xf bank_mask:0xf
	v_add_f32_dpp v37, v37, v37 row_half_mirror row_mask:0xf bank_mask:0xf
	v_add_f32_dpp v38, v38, v38 row_half_mirror row_mask:0xf bank_mask:0xf
	v_add_f32_dpp v39, v39, v39 row_half_mirror row_mask:0xf bank_mask:0xf
	v_add_f32_dpp v40, v40, v40 row_half_mirror row_mask:0xf bank_mask:0xf
	v_add_f32_dpp v41, v41, v41 row_half_mirror row_mask:0xf bank_mask:0xf
	v_add_f32_dpp v42, v42, v42 row_half_mirror row_mask:0xf bank_mask:0xf
	v_add_f32_dpp v43, v43, v43 row_half_mirror row_mask:0xf bank_mask:0xf
	v_add_f32_dpp v44, v44, v44 row_half_mirror row_mask:0xf bank_mask:0xf
; __device__ __forceinline__ float wave_sum(float v) {
; #pragma unroll
;     for (int o = 1; o < 64; o <<= 1) v += __shfl_xor(v, o);
;     return v;
; __global__ void __launch_bounds__(NTHR, 2) fwd_kernel(Args args) {
;     ...
;             for (int q = 0; q < 8; ++q) { const float sq = wave_sum(ssq[q]); const float rs = 1.0f / sqrtf(sq * (1.0f / DM) + EPS);
;                 float lg[8];
; #pragma unroll
;                 for (int e = 0; e < 8; ++e) lg[e] = wave_sum(acc[q][e]) * rs;
	v_add_f32_dpp v45, v45, v45 row_half_mirror row_mask:0xf bank_mask:0xf
	v_add_f32_dpp v46, v46, v46 row_half_mirror row_mask:0xf bank_mask:0xf
	v_add_f32_dpp v47, v47, v47 row_half_mirror row_mask:0xf bank_mask:0xf
	v_add_f32_dpp v48, v48, v48 row_half_mirror row_mask:0xf bank_mask:0xf
	v_add_f32_dpp v49, v49, v49 row_half_mirror row_mask:0xf bank_mask:0xf
	v_add_f32_dpp v50, v50, v50 row_half_mirror row_mask:0xf bank_mask:0xf
	v_add_f32_dpp v51, v51, v51 row_half_mirror row_mask:0xf bank_mask:0xf
	v_add_f32_dpp v52, v52, v52 row_half_mirror row_mask:0xf bank_mask:0xf
	v_add_f32_dpp v53, v53, v53 row_half_mirror row_mask:0xf bank_mask:0xf
	v_add_f32_dpp v54, v54, v54 row_half_mirror row_mask:0xf bank_mask:0xf
	v_add_f32_dpp v55, v55, v55 row_half_mirror row_mask:0xf bank_mask:0xf
	v_add_f32_dpp v56, v56, v56 row_half_mirror row_mask:0xf bank_mask:0xf
	v_add_f32_dpp v57, v57, v57 row_half_mirror row_mask:0xf bank_mask:0xf
	v_add_f32_dpp v58, v58, v58 row_half_mirror row_mask:0xf bank_mask:0xf
	v_add_f32_dpp v59, v59, v59 row_half_mirror row_mask:0xf bank_mask:0xf
	v_add_f32_dpp v60, v60, v60 row_half_mirror row_mask:0xf bank_mask:0xf
	v_add_f32_dpp v61, v61, v61 row_half_mirror row_mask:0xf bank_mask:0xf
	v_add_f32_dpp v62, v62, v62 row_half_mirror row_mask:0xf bank_mask:0xf
	v_add_f32_dpp v63, v63, v63 row_half_mirror row_mask:0xf bank_mask:0xf
	v_add_f32_dpp v192, v192, v192 row_half_mirror row_mask:0xf bank_mask:0xf
	v_add_f32_dpp v194, v194, v194 row_half_mirror row_mask:0xf bank_mask:0xf
	v_add_f32_dpp v196, v196, v196 row_half_mirror row_mask:0xf bank_mask:0xf
	v_add_f32_dpp v198, v198, v198 row_half_mirror row_mask:0xf bank_mask:0xf
	v_add_f32_dpp v200, v200, v200 row_half_mirror row_mask:0xf bank_mask:0xf
	v_add_f32_dpp v202, v202, v202 row_half_mirror row_mask:0xf bank_mask:0xf
	v_add_f32_dpp v204, v204, v204 row_half_mirror row_mask:0xf bank_mask:0xf
	v_add_f32_dpp v206, v206, v206 row_half_mirror row_mask:0xf bank_mask:0xf
	v_add_f32_dpp v0, v0, v0 row_mirror row_mask:0xf bank_mask:0xf
	v_add_f32_dpp v1, v1, v1 row_mirror row_mask:0xf bank_mask:0xf
	v_add_f32_dpp v2, v2, v2 row_mirror row_mask:0xf bank_mask:0xf
	v_add_f32_dpp v3, v3, v3 row_mirror row_mask:0xf bank_mask:0xf
	v_add_f32_dpp v4, v4, v4 row_mirror row_mask:0xf bank_mask:0xf
	v_add_f32_dpp v5, v5, v5 row_mirror row_mask:0xf bank_mask:0xf
	v_add_f32_dpp v6, v6, v6 row_mirror row_mask:0xf bank_mask:0xf
	v_add_f32_dpp v7, v7, v7 row_mirror row_mask:0xf bank_mask:0xf
	v_add_f32_dpp v8, v8, v8 row_mirror row_mask:0xf bank_mask:0xf
	v_add_f32_dpp v9, v9, v9 row_mirror row_mask:0xf bank_mask:0xf
	v_add_f32_dpp v10, v10, v10 row_mirror row_mask:0xf bank_mask:0xf
	v_add_f32_dpp v11, v11, v11 row_mirror row_mask:0xf bank_mask:0xf
	v_add_f32_dpp v12, v12, v12 row_mirror row_mask:0xf bank_mask:0xf
	v_add_f32_dpp v13, v13, v13 row_mirror row_mask:0xf bank_mask:0xf
	v_add_f32_dpp v14, v14, v14 row_mirror row_mask:0xf bank_mask:0xf
	v_add_f32_dpp v15, v15, v15 row_mirror row_mask:0xf bank_mask:0xf
	v_add_f32_dpp v16, v16, v16 row_mirror row_mask:0xf bank_mask:0xf
	v_add_f32_dpp v17, v17, v17 row_mirror row_mask:0xf bank_mask:0xf
	v_add_f32_dpp v18, v18, v18 row_mirror row_mask:0xf bank_mask:0xf
	v_add_f32_dpp v19, v19, v19 row_mirror row_mask:0xf bank_mask:0xf
	v_add_f32_dpp v20, v20, v20 row_mirror row_mask:0xf bank_mask:0xf
	v_add_f32_dpp v21, v21, v21 row_mirror row_mask:0xf bank_mask:0xf
	v_add_f32_dpp v22, v22, v22 row_mirror row_mask:0xf bank_mask:0xf
	v_add_f32_dpp v23, v23, v23 row_mirror row_mask:0xf bank_mask:0xf
	v_add_f32_dpp v24, v24, v24 row_mirror row_mask:0xf bank_mask:0xf
	v_add_f32_dpp v25, v25, v25 row_mirror row_mask:0xf bank_mask:0xf
	v_add_f32_dpp v26, v26, v26 row_mirror row_mask:0xf bank_mask:0xf
	v_add_f32_dpp v27, v27, v27 row_mirror row_mask:0xf bank_mask:0xf
	v_add_f32_dpp v28, v28, v28 row_mirror row_mask:0xf bank_mask:0xf
	v_add_f32_dpp v29, v29, v29 row_mirror row_mask:0xf bank_mask:0xf
	v_add_f32_dpp v30, v30, v30 row_mirror row_mask:0xf bank_mask:0xf
	v_add_f32_dpp v31, v31, v31 row_mirror row_mask:0xf bank_mask:0xf
	v_add_f32_dpp v32, v32, v32 row_mirror row_mask:0xf bank_mask:0xf
	v_add_f32_dpp v33, v33, v33 row_mirror row_mask:0xf bank_mask:0xf
	v_add_f32_dpp v34, v34, v34 row_mirror row_mask:0xf bank_mask:0xf
	v_add_f32_dpp v35, v35, v35 row_mirror row_mask:0xf bank_mask:0xf
	v_add_f32_dpp v36, v36, v36 row_mirror row_mask:0xf bank_mask:0xf
	v_add_f32_dpp v37, v37, v37 row_mirror row_mask:0xf bank_mask:0xf
	v_add_f32_dpp v38, v38, v38 row_mirror row_mask:0xf bank_mask:0xf
	v_add_f32_dpp v39, v39, v39 row_mirror row_mask:0xf bank_mask:0xf
	v_add_f32_dpp v40, v40, v40 row_mirror row_mask:0xf bank_mask:0xf
	v_add_f32_dpp v41, v41, v41 row_mirror row_mask:0xf bank_mask:0xf
	v_add_f32_dpp v42, v42, v42 row_mirror row_mask:0xf bank_mask:0xf
	v_add_f32_dpp v43, v43, v43 row_mirror row_mask:0xf bank_mask:0xf
	v_add_f32_dpp v44, v44, v44 row_mirror row_mask:0xf bank_mask:0xf
	v_add_f32_dpp v45, v45, v45 row_mirror row_mask:0xf bank_mask:0xf
	v_add_f32_dpp v46, v46, v46 row_mirror row_mask:0xf bank_mask:0xf
	v_add_f32_dpp v47, v47, v47 row_mirror row_mask:0xf bank_mask:0xf
	v_add_f32_dpp v48, v48, v48 row_mirror row_mask:0xf bank_mask:0xf
	v_add_f32_dpp v49, v49, v49 row_mirror row_mask:0xf bank_mask:0xf
	v_add_f32_dpp v50, v50, v50 row_mirror row_mask:0xf bank_mask:0xf
	v_add_f32_dpp v51, v51, v51 row_mirror row_mask:0xf bank_mask:0xf
	v_add_f32_dpp v52, v52, v52 row_mirror row_mask:0xf bank_mask:0xf
	v_add_f32_dpp v53, v53, v53 row_mirror row_mask:0xf bank_mask:0xf
	v_add_f32_dpp v54, v54, v54 row_mirror row_mask:0xf bank_mask:0xf
; __device__ __forceinline__ float wave_sum(float v) {
; #pragma unroll
;     for (int o = 1; o < 64; o <<= 1) v += __shfl_xor(v, o);
;     return v;
; __global__ void __launch_bounds__(NTHR, 2) fwd_kernel(Args args) {
;     ...
;             for (int q = 0; q < 8; ++q) { const float sq = wave_sum(ssq[q]); const float rs = 1.0f / sqrtf(sq * (1.0f / DM) + EPS);
;                 float lg[8];
; #pragma unroll
;                 for (int e = 0; e < 8; ++e) lg[e] = wave_sum(acc[q][e]) * rs;
	v_add_f32_dpp v55, v55, v55 row_mirror row_mask:0xf bank_mask:0xf
	v_add_f32_dpp v56, v56, v56 row_mirror row_mask:0xf bank_mask:0xf
	v_add_f32_dpp v57, v57, v57 row_mirror row_mask:0xf bank_mask:0xf
	v_add_f32_dpp v58, v58, v58 row_mirror row_mask:0xf bank_mask:0xf
	v_add_f32_dpp v59, v59, v59 row_mirror row_mask:0xf bank_mask:0xf
	v_add_f32_dpp v60, v60, v60 row_mirror row_mask:0xf bank_mask:0xf
	v_add_f32_dpp v61, v61, v61 row_mirror row_mask:0xf bank_mask:0xf
	v_add_f32_dpp v62, v62, v62 row_mirror row_mask:0xf bank_mask:0xf
	v_add_f32_dpp v63, v63, v63 row_mirror row_mask:0xf bank_mask:0xf
	v_add_f32_dpp v192, v192, v192 row_mirror row_mask:0xf bank_mask:0xf
	v_add_f32_dpp v194, v194, v194 row_mirror row_mask:0xf bank_mask:0xf
	v_add_f32_dpp v196, v196, v196 row_mirror row_mask:0xf bank_mask:0xf
	v_add_f32_dpp v198, v198, v198 row_mirror row_mask:0xf bank_mask:0xf
	v_add_f32_dpp v200, v200, v200 row_mirror row_mask:0xf bank_mask:0xf
	v_add_f32_dpp v202, v202, v202 row_mirror row_mask:0xf bank_mask:0xf
	v_add_f32_dpp v204, v204, v204 row_mirror row_mask:0xf bank_mask:0xf
	v_add_f32_dpp v206, v206, v206 row_mirror row_mask:0xf bank_mask:0xf
	v_add_f32_dpp v0, v0, v0 row_bcast:15 row_mask:0xa bank_mask:0xf
	v_add_f32_dpp v1, v1, v1 row_bcast:15 row_mask:0xa bank_mask:0xf
	v_add_f32_dpp v2, v2, v2 row_bcast:15 row_mask:0xa bank_mask:0xf
	v_add_f32_dpp v3, v3, v3 row_bcast:15 row_mask:0xa bank_mask:0xf
	v_add_f32_dpp v4, v4, v4 row_bcast:15 row_mask:0xa bank_mask:0xf
	v_add_f32_dpp v5, v5, v5 row_bcast:15 row_mask:0xa bank_mask:0xf
	v_add_f32_dpp v6, v6, v6 row_bcast:15 row_mask:0xa bank_mask:0xf
	v_add_f32_dpp v7, v7, v7 row_bcast:15 row_mask:0xa bank_mask:0xf
	v_add_f32_dpp v8, v8, v8 row_bcast:15 row_mask:0xa bank_mask:0xf
	v_add_f32_dpp v9, v9, v9 row_bcast:15 row_mask:0xa bank_mask:0xf
	v_add_f32_dpp v10, v10, v10 row_bcast:15 row_mask:0xa bank_mask:0xf
	v_add_f32_dpp v11, v11, v11 row_bcast:15 row_mask:0xa bank_mask:0xf
	v_add_f32_dpp v12, v12, v12 row_bcast:15 row_mask:0xa bank_mask:0xf
	v_add_f32_dpp v13, v13, v13 row_bcast:15 row_mask:0xa bank_mask:0xf
	v_add_f32_dpp v14, v14, v14 row_bcast:15 row_mask:0xa bank_mask:0xf
	v_add_f32_dpp v15, v15, v15 row_bcast:15 row_mask:0xa bank_mask:0xf
	v_add_f32_dpp v16, v16, v16 row_bcast:15 row_mask:0xa bank_mask:0xf
	v_add_f32_dpp v17, v17, v17 row_bcast:15 row_mask:0xa bank_mask:0xf
	v_add_f32_dpp v18, v18, v18 row_bcast:15 row_mask:0xa bank_mask:0xf
	v_add_f32_dpp v19, v19, v19 row_bcast:15 row_mask:0xa bank_mask:0xf
	v_add_f32_dpp v20, v20, v20 row_bcast:15 row_mask:0xa bank_mask:0xf
	v_add_f32_dpp v21, v21, v21 row_bcast:15 row_mask:0xa bank_mask:0xf
	v_add_f32_dpp v22, v22, v22 row_bcast:15 row_mask:0xa bank_mask:0xf
	v_add_f32_dpp v23, v23, v23 row_bcast:15 row_mask:0xa bank_mask:0xf
	v_add_f32_dpp v24, v24, v24 row_bcast:15 row_mask:0xa bank_mask:0xf
	v_add_f32_dpp v25, v25, v25 row_bcast:15 row_mask:0xa bank_mask:0xf
	v_add_f32_dpp v26, v26, v26 row_bcast:15 row_mask:0xa bank_mask:0xf
	v_add_f32_dpp v27, v27, v27 row_bcast:15 row_mask:0xa bank_mask:0xf
	v_add_f32_dpp v28, v28, v28 row_bcast:15 row_mask:0xa bank_mask:0xf
	v_add_f32_dpp v29, v29, v29 row_bcast:15 row_mask:0xa bank_mask:0xf
	v_add_f32_dpp v30, v30, v30 row_bcast:15 row_mask:0xa bank_mask:0xf
	v_add_f32_dpp v31, v31, v31 row_bcast:15 row_mask:0xa bank_mask:0xf
	v_add_f32_dpp v32, v32, v32 row_bcast:15 row_mask:0xa bank_mask:0xf
	v_add_f32_dpp v33, v33, v33 row_bcast:15 row_mask:0xa bank_mask:0xf
	v_add_f32_dpp v34, v34, v34 row_bcast:15 row_mask:0xa bank_mask:0xf
	v_add_f32_dpp v35, v35, v35 row_bcast:15 row_mask:0xa bank_mask:0xf
	v_add_f32_dpp v36, v36, v36 row_bcast:15 row_mask:0xa bank_mask:0xf
	v_add_f32_dpp v37, v37, v37 row_bcast:15 row_mask:0xa bank_mask:0xf
	v_add_f32_dpp v38, v38, v38 row_bcast:15 row_mask:0xa bank_mask:0xf
	v_add_f32_dpp v39, v39, v39 row_bcast:15 row_mask:0xa bank_mask:0xf
	v_add_f32_dpp v40, v40, v40 row_bcast:15 row_mask:0xa bank_mask:0xf
	v_add_f32_dpp v41, v41, v41 row_bcast:15 row_mask:0xa bank_mask:0xf
	v_add_f32_dpp v42, v42, v42 row_bcast:15 row_mask:0xa bank_mask:0xf
	v_add_f32_dpp v43, v43, v43 row_bcast:15 row_mask:0xa bank_mask:0xf
	v_add_f32_dpp v44, v44, v44 row_bcast:15 row_mask:0xa bank_mask:0xf
	v_add_f32_dpp v45, v45, v45 row_bcast:15 row_mask:0xa bank_mask:0xf
	v_add_f32_dpp v46, v46, v46 row_bcast:15 row_mask:0xa bank_mask:0xf
	v_add_f32_dpp v47, v47, v47 row_bcast:15 row_mask:0xa bank_mask:0xf
	v_add_f32_dpp v48, v48, v48 row_bcast:15 row_mask:0xa bank_mask:0xf
	v_add_f32_dpp v49, v49, v49 row_bcast:15 row_mask:0xa bank_mask:0xf
	v_add_f32_dpp v50, v50, v50 row_bcast:15 row_mask:0xa bank_mask:0xf
	v_add_f32_dpp v51, v51, v51 row_bcast:15 row_mask:0xa bank_mask:0xf
	v_add_f32_dpp v52, v52, v52 row_bcast:15 row_mask:0xa bank_mask:0xf
	v_add_f32_dpp v53, v53, v53 row_bcast:15 row_mask:0xa bank_mask:0xf
	v_add_f32_dpp v54, v54, v54 row_bcast:15 row_mask:0xa bank_mask:0xf
	v_add_f32_dpp v55, v55, v55 row_bcast:15 row_mask:0xa bank_mask:0xf
	v_add_f32_dpp v56, v56, v56 row_bcast:15 row_mask:0xa bank_mask:0xf
	v_add_f32_dpp v57, v57, v57 row_bcast:15 row_mask:0xa bank_mask:0xf
	v_add_f32_dpp v58, v58, v58 row_bcast:15 row_mask:0xa bank_mask:0xf
	v_add_f32_dpp v59, v59, v59 row_bcast:15 row_mask:0xa bank_mask:0xf
	v_add_f32_dpp v60, v60, v60 row_bcast:15 row_mask:0xa bank_mask:0xf
	v_add_f32_dpp v61, v61, v61 row_bcast:15 row_mask:0xa bank_mask:0xf
	v_add_f32_dpp v62, v62, v62 row_bcast:15 row_mask:0xa bank_mask:0xf
	v_add_f32_dpp v63, v63, v63 row_bcast:15 row_mask:0xa bank_mask:0xf
	v_add_f32_dpp v192, v192, v192 row_bcast:15 row_mask:0xa bank_mask:0xf
; __global__ void __launch_bounds__(NTHR, 2) fwd_kernel(Args args) {
;     ...
;             for (int q = 0; q < 8; ++q) { const float sq = wave_sum(ssq[q]); const float rs = 1.0f / sqrtf(sq * (1.0f / DM) + EPS);
;                 float lg[8];
; #pragma unroll
;                 for (int e = 0; e < 8; ++e) lg[e] = wave_sum(acc[q][e]) * rs;
	v_add_f32_dpp v194, v194, v194 row_bcast:15 row_mask:0xa bank_mask:0xf
	v_add_f32_dpp v196, v196, v196 row_bcast:15 row_mask:0xa bank_mask:0xf
	v_add_f32_dpp v198, v198, v198 row_bcast:15 row_mask:0xa bank_mask:0xf
	v_add_f32_dpp v200, v200, v200 row_bcast:15 row_mask:0xa bank_mask:0xf
	v_add_f32_dpp v202, v202, v202 row_bcast:15 row_mask:0xa bank_mask:0xf
	v_add_f32_dpp v204, v204, v204 row_bcast:15 row_mask:0xa bank_mask:0xf
	v_add_f32_dpp v206, v206, v206 row_bcast:15 row_mask:0xa bank_mask:0xf
	v_add_f32_dpp v0, v0, v0 row_bcast:31 row_mask:0xc bank_mask:0xf
	v_add_f32_dpp v1, v1, v1 row_bcast:31 row_mask:0xc bank_mask:0xf
	v_add_f32_dpp v2, v2, v2 row_bcast:31 row_mask:0xc bank_mask:0xf
	v_add_f32_dpp v3, v3, v3 row_bcast:31 row_mask:0xc bank_mask:0xf
	v_add_f32_dpp v4, v4, v4 row_bcast:31 row_mask:0xc bank_mask:0xf
	v_add_f32_dpp v5, v5, v5 row_bcast:31 row_mask:0xc bank_mask:0xf
	v_add_f32_dpp v6, v6, v6 row_bcast:31 row_mask:0xc bank_mask:0xf
	v_add_f32_dpp v7, v7, v7 row_bcast:31 row_mask:0xc bank_mask:0xf
	v_add_f32_dpp v8, v8, v8 row_bcast:31 row_mask:0xc bank_mask:0xf
	v_add_f32_dpp v9, v9, v9 row_bcast:31 row_mask:0xc bank_mask:0xf
	v_add_f32_dpp v10, v10, v10 row_bcast:31 row_mask:0xc bank_mask:0xf
	v_add_f32_dpp v11, v11, v11 row_bcast:31 row_mask:0xc bank_mask:0xf
	v_add_f32_dpp v12, v12, v12 row_bcast:31 row_mask:0xc bank_mask:0xf
	v_add_f32_dpp v13, v13, v13 row_bcast:31 row_mask:0xc bank_mask:0xf
	v_add_f32_dpp v14, v14, v14 row_bcast:31 row_mask:0xc bank_mask:0xf
	v_add_f32_dpp v15, v15, v15 row_bcast:31 row_mask:0xc bank_mask:0xf
	v_add_f32_dpp v16, v16, v16 row_bcast:31 row_mask:0xc bank_mask:0xf
	v_add_f32_dpp v17, v17, v17 row_bcast:31 row_mask:0xc bank_mask:0xf
	v_add_f32_dpp v18, v18, v18 row_bcast:31 row_mask:0xc bank_mask:0xf
	v_add_f32_dpp v19, v19, v19 row_bcast:31 row_mask:0xc bank_mask:0xf
	v_add_f32_dpp v20, v20, v20 row_bcast:31 row_mask:0xc bank_mask:0xf
	v_add_f32_dpp v21, v21, v21 row_bcast:31 row_mask:0xc bank_mask:0xf
	v_add_f32_dpp v22, v22, v22 row_bcast:31 row_mask:0xc bank_mask:0xf
	v_add_f32_dpp v23, v23, v23 row_bcast:31 row_mask:0xc bank_mask:0xf
	v_add_f32_dpp v24, v24, v24 row_bcast:31 row_mask:0xc bank_mask:0xf
	v_add_f32_dpp v25, v25, v25 row_bcast:31 row_mask:0xc bank_mask:0xf
	v_add_f32_dpp v26, v26, v26 row_bcast:31 row_mask:0xc bank_mask:0xf
	v_add_f32_dpp v27, v27, v27 row_bcast:31 row_mask:0xc bank_mask:0xf
	v_add_f32_dpp v28, v28, v28 row_bcast:31 row_mask:0xc bank_mask:0xf
	v_add_f32_dpp v29, v29, v29 row_bcast:31 row_mask:0xc bank_mask:0xf
	v_add_f32_dpp v30, v30, v30 row_bcast:31 row_mask:0xc bank_mask:0xf
	v_add_f32_dpp v31, v31, v31 row_bcast:31 row_mask:0xc bank_mask:0xf
	v_add_f32_dpp v32, v32, v32 row_bcast:31 row_mask:0xc bank_mask:0xf
	v_add_f32_dpp v33, v33, v33 row_bcast:31 row_mask:0xc bank_mask:0xf
	v_add_f32_dpp v34, v34, v34 row_bcast:31 row_mask:0xc bank_mask:0xf
	v_add_f32_dpp v35, v35, v35 row_bcast:31 row_mask:0xc bank_mask:0xf
	v_add_f32_dpp v36, v36, v36 row_bcast:31 row_mask:0xc bank_mask:0xf
	v_add_f32_dpp v37, v37, v37 row_bcast:31 row_mask:0xc bank_mask:0xf
	v_add_f32_dpp v38, v38, v38 row_bcast:31 row_mask:0xc bank_mask:0xf
	v_add_f32_dpp v39, v39, v39 row_bcast:31 row_mask:0xc bank_mask:0xf
	v_add_f32_dpp v40, v40, v40 row_bcast:31 row_mask:0xc bank_mask:0xf
	v_add_f32_dpp v41, v41, v41 row_bcast:31 row_mask:0xc bank_mask:0xf
	v_add_f32_dpp v42, v42, v42 row_bcast:31 row_mask:0xc bank_mask:0xf
	v_add_f32_dpp v43, v43, v43 row_bcast:31 row_mask:0xc bank_mask:0xf
	v_add_f32_dpp v44, v44, v44 row_bcast:31 row_mask:0xc bank_mask:0xf
	v_add_f32_dpp v45, v45, v45 row_bcast:31 row_mask:0xc bank_mask:0xf
	v_add_f32_dpp v46, v46, v46 row_bcast:31 row_mask:0xc bank_mask:0xf
	v_add_f32_dpp v47, v47, v47 row_bcast:31 row_mask:0xc bank_mask:0xf
	v_add_f32_dpp v48, v48, v48 row_bcast:31 row_mask:0xc bank_mask:0xf
	v_add_f32_dpp v49, v49, v49 row_bcast:31 row_mask:0xc bank_mask:0xf
	v_add_f32_dpp v50, v50, v50 row_bcast:31 row_mask:0xc bank_mask:0xf
	v_add_f32_dpp v51, v51, v51 row_bcast:31 row_mask:0xc bank_mask:0xf
	v_add_f32_dpp v52, v52, v52 row_bcast:31 row_mask:0xc bank_mask:0xf
	v_add_f32_dpp v53, v53, v53 row_bcast:31 row_mask:0xc bank_mask:0xf
	v_add_f32_dpp v54, v54, v54 row_bcast:31 row_mask:0xc bank_mask:0xf
	v_add_f32_dpp v55, v55, v55 row_bcast:31 row_mask:0xc bank_mask:0xf
	v_add_f32_dpp v56, v56, v56 row_bcast:31 row_mask:0xc bank_mask:0xf
	v_add_f32_dpp v57, v57, v57 row_bcast:31 row_mask:0xc bank_mask:0xf
	v_add_f32_dpp v58, v58, v58 row_bcast:31 row_mask:0xc bank_mask:0xf
	v_add_f32_dpp v59, v59, v59 row_bcast:31 row_mask:0xc bank_mask:0xf
	v_add_f32_dpp v60, v60, v60 row_bcast:31 row_mask:0xc bank_mask:0xf
	v_add_f32_dpp v61, v61, v61 row_bcast:31 row_mask:0xc bank_mask:0xf
	v_add_f32_dpp v62, v62, v62 row_bcast:31 row_mask:0xc bank_mask:0xf
	v_add_f32_dpp v63, v63, v63 row_bcast:31 row_mask:0xc bank_mask:0xf
	v_add_f32_dpp v192, v192, v192 row_bcast:31 row_mask:0xc bank_mask:0xf
	v_add_f32_dpp v194, v194, v194 row_bcast:31 row_mask:0xc bank_mask:0xf
	v_add_f32_dpp v196, v196, v196 row_bcast:31 row_mask:0xc bank_mask:0xf
	v_add_f32_dpp v198, v198, v198 row_bcast:31 row_mask:0xc bank_mask:0xf
	v_add_f32_dpp v200, v200, v200 row_bcast:31 row_mask:0xc bank_mask:0xf
	v_add_f32_dpp v202, v202, v202 row_bcast:31 row_mask:0xc bank_mask:0xf
	v_add_f32_dpp v204, v204, v204 row_bcast:31 row_mask:0xc bank_mask:0xf
	v_add_f32_dpp v206, v206, v206 row_bcast:31 row_mask:0xc bank_mask:0xf
	v_fmamk_f32 v232, v192, 0x3a000000, v222
	v_mul_f32_e32 v233, 0x4f800000, v232
	v_cmp_gt_f32_e32 vcc, s63, v232
	s_nop 1
	v_cndmask_b32_e32 v232, v232, v233, vcc
; __global__ void __launch_bounds__(NTHR, 2) fwd_kernel(Args args) {
;     ...
;             for (int q = 0; q < 8; ++q) { const float sq = wave_sum(ssq[q]); const float rs = 1.0f / sqrtf(sq * (1.0f / DM) + EPS);
;                 float lg[8];
; #pragma unroll
;                 for (int e = 0; e < 8; ++e) lg[e] = wave_sum(acc[q][e]) * rs;
;                 int i0 = 0; float v0 = lg[0];
; #pragma unroll
;                 for (int e = 1; e < 8; ++e) if (lg[e] > v0) { v0 = lg[e]; i0 = e; }
;                 int i1 = -1; float v1 = -__builtin_inff();
; #pragma unroll
;                 for (int e = 0; e < 8; ++e) if (e != i0 && lg[e] > v1) { v1 = lg[e]; i1 = e; }
;                 if (lane == 0) { const int t = t0 + q; const float w0 = 1.0f / (1.0f + expf(v1 - v0));
;                     tok_e[t] = i0 | (i1 << 8); tok_w[2 * t] = w0; tok_w[2 * t + 1] = 1.0f - w0; rstd3[t] = rs;
	v_sqrt_f32_e32 v233, v232
	s_nop 0
	v_add_u32_e32 v234, -1, v233
	v_add_u32_e32 v235, 1, v233
	v_fma_f32 v236, -v234, v233, v232
	v_fma_f32 v237, -v235, v233, v232
	v_cmp_ge_f32_e64 s[68:69], 0, v236
	s_nop 1
	v_cndmask_b32_e64 v233, v233, v234, s[68:69]
	v_cmp_lt_f32_e64 s[68:69], 0, v237
	s_nop 1
	v_cndmask_b32_e64 v233, v233, v235, s[68:69]
	v_mul_f32_e32 v234, 0x37800000, v233
	v_cndmask_b32_e32 v233, v233, v234, vcc
	v_cmp_class_f32_e32 vcc, v232, v223
	s_nop 1
	v_cndmask_b32_e32 v232, v233, v232, vcc
	v_div_scale_f32 v233, s[68:69], v232, v232, 1.0
	v_rcp_f32_e32 v234, v233
	s_nop 0
	v_fma_f32 v235, -v233, v234, 1.0
	v_fmac_f32_e32 v234, v235, v234
	v_div_scale_f32 v235, vcc, 1.0, v232, 1.0
	v_mul_f32_e32 v236, v235, v234
	v_fma_f32 v237, -v233, v236, v235
	v_fmac_f32_e32 v236, v237, v234
	v_fma_f32 v233, -v233, v236, v235
	s_nop 0
	v_div_fmas_f32 v233, v233, v234, v236
	v_div_fixup_f32 v112, v233, v232, 1.0
	v_mul_f32_e32 v0, v112, v0
	v_mul_f32_e32 v1, v112, v1
	v_mul_f32_e32 v2, v112, v2
	v_mul_f32_e32 v3, v112, v3
	v_mul_f32_e32 v4, v112, v4
	v_mul_f32_e32 v5, v112, v5
	v_mul_f32_e32 v6, v112, v6
	v_mul_f32_e32 v7, v112, v7
	v_mov_b32_e32 v238, v0
	v_mov_b32_e32 v64, 0
	v_cmp_gt_f32_e32 vcc, v1, v238
	s_nop 1
	v_cndmask_b32_e32 v238, v238, v1, vcc
	v_cndmask_b32_e64 v64, v64, 1, vcc
	v_cmp_gt_f32_e32 vcc, v2, v238
	s_nop 1
	v_cndmask_b32_e32 v238, v238, v2, vcc
	v_cndmask_b32_e64 v64, v64, 2, vcc
	v_cmp_gt_f32_e32 vcc, v3, v238
	s_nop 1
	v_cndmask_b32_e32 v238, v238, v3, vcc
	v_cndmask_b32_e64 v64, v64, 3, vcc
	v_cmp_gt_f32_e32 vcc, v4, v238
	s_nop 1
	v_cndmask_b32_e32 v238, v238, v4, vcc
	v_cndmask_b32_e64 v64, v64, 4, vcc
	v_cmp_gt_f32_e32 vcc, v5, v238
	s_nop 1
	v_cndmask_b32_e32 v238, v238, v5, vcc
	v_cndmask_b32_e64 v64, v64, 5, vcc
	v_cmp_gt_f32_e32 vcc, v6, v238
	s_nop 1
	v_cndmask_b32_e32 v238, v238, v6, vcc
	v_cndmask_b32_e64 v64, v64, 6, vcc
	v_cmp_gt_f32_e32 vcc, v7, v238
	s_nop 1
	v_cndmask_b32_e32 v238, v238, v7, vcc
	v_cndmask_b32_e64 v64, v64, 7, vcc
	v_mov_b32_e32 v239, v224
	v_mov_b32_e32 v65, -1
	v_cmp_ne_u32_e64 s[68:69], 0, v64
	v_cmp_gt_f32_e32 vcc, v0, v239
	s_and_b64 vcc, vcc, s[68:69]
	v_cndmask_b32_e32 v239, v239, v0, vcc
	v_cndmask_b32_e64 v65, v65, 0, vcc
	v_cmp_ne_u32_e64 s[68:69], 1, v64
	v_cmp_gt_f32_e32 vcc, v1, v239
	s_and_b64 vcc, vcc, s[68:69]
	v_cndmask_b32_e32 v239, v239, v1, vcc
	v_cndmask_b32_e64 v65, v65, 1, vcc
	v_cmp_ne_u32_e64 s[68:69], 2, v64
	v_cmp_gt_f32_e32 vcc, v2, v239
	s_and_b64 vcc, vcc, s[68:69]
	v_cndmask_b32_e32 v239, v239, v2, vcc
	v_cndmask_b32_e64 v65, v65, 2, vcc
	v_cmp_ne_u32_e64 s[68:69], 3, v64
	v_cmp_gt_f32_e32 vcc, v3, v239
	s_and_b64 vcc, vcc, s[68:69]
	v_cndmask_b32_e32 v239, v239, v3, vcc
	v_cndmask_b32_e64 v65, v65, 3, vcc
	v_cmp_ne_u32_e64 s[68:69], 4, v64
	v_cmp_gt_f32_e32 vcc, v4, v239
	s_and_b64 vcc, vcc, s[68:69]
	v_cndmask_b32_e32 v239, v239, v4, vcc
	v_cndmask_b32_e64 v65, v65, 4, vcc
	v_cmp_ne_u32_e64 s[68:69], 5, v64
	v_cmp_gt_f32_e32 vcc, v5, v239
	s_and_b64 vcc, vcc, s[68:69]
	v_cndmask_b32_e32 v239, v239, v5, vcc
	v_cndmask_b32_e64 v65, v65, 5, vcc
	v_cmp_ne_u32_e64 s[68:69], 6, v64
	v_cmp_gt_f32_e32 vcc, v6, v239
	s_and_b64 vcc, vcc, s[68:69]
	v_cndmask_b32_e32 v239, v239, v6, vcc
	v_cndmask_b32_e64 v65, v65, 6, vcc
	v_cmp_ne_u32_e64 s[68:69], 7, v64
	v_cmp_gt_f32_e32 vcc, v7, v239
	s_and_b64 vcc, vcc, s[68:69]
	v_cndmask_b32_e32 v239, v239, v7, vcc
	v_cndmask_b32_e64 v65, v65, 7, vcc
	v_sub_f32_e32 v232, v239, v238
	v_mul_f32_e32 v233, 0x3fb8aa3b, v232
	v_fma_f32 v234, v232, s65, -v233
	v_rndne_f32_e32 v235, v233
	v_fmac_f32_e32 v234, 0x32a5705f, v232
	v_sub_f32_e32 v233, v233, v235
	v_add_f32_e32 v233, v233, v234
	v_exp_f32_e32 v233, v233
	v_cvt_i32_f32_e32 v234, v235
	v_cmp_ngt_f32_e32 vcc, s66, v232
	v_ldexp_f32 v233, v233, v234
	s_nop 0
	v_cndmask_b32_e32 v233, 0, v233, vcc
	v_cmp_nlt_f32_e32 vcc, s67, v232
	s_nop 1
	v_cndmask_b32_e32 v232, v225, v233, vcc
	v_add_f32_e32 v232, 1.0, v232
	v_div_scale_f32 v233, s[68:69], v232, v232, 1.0
	v_rcp_f32_e32 v234, v233
	s_nop 0
	v_fma_f32 v235, -v233, v234, 1.0
	v_fmac_f32_e32 v234, v235, v234
	v_div_scale_f32 v235, vcc, 1.0, v232, 1.0
	v_mul_f32_e32 v236, v235, v234
	v_fma_f32 v237, -v233, v236, v235
	v_fmac_f32_e32 v236, v237, v234
	v_fma_f32 v233, -v233, v236, v235
	s_nop 0
	v_div_fmas_f32 v233, v233, v234, v236
	v_div_fixup_f32 v66, v233, v232, 1.0
	v_sub_f32_e32 v67, 1.0, v66
	v_lshl_add_u32 v68, v65, 8, v64
	v_fmamk_f32 v232, v194, 0x3a000000, v222
	v_mul_f32_e32 v233, 0x4f800000, v232
	v_cmp_gt_f32_e32 vcc, s63, v232
	s_nop 1
	v_cndmask_b32_e32 v232, v232, v233, vcc
	v_sqrt_f32_e32 v233, v232
	s_nop 0
	v_add_u32_e32 v234, -1, v233
	v_add_u32_e32 v235, 1, v233
	v_fma_f32 v236, -v234, v233, v232
	v_fma_f32 v237, -v235, v233, v232
	v_cmp_ge_f32_e64 s[68:69], 0, v236
	s_nop 1
	v_cndmask_b32_e64 v233, v233, v234, s[68:69]
	v_cmp_lt_f32_e64 s[68:69], 0, v237
	s_nop 1
	v_cndmask_b32_e64 v233, v233, v235, s[68:69]
	v_mul_f32_e32 v234, 0x37800000, v233
	v_cndmask_b32_e32 v233, v233, v234, vcc
	v_cmp_class_f32_e32 vcc, v232, v223
	s_nop 1
	v_cndmask_b32_e32 v232, v233, v232, vcc
	v_div_scale_f32 v233, s[68:69], v232, v232, 1.0
	v_rcp_f32_e32 v234, v233
	s_nop 0
	v_fma_f32 v235, -v233, v234, 1.0
	v_fmac_f32_e32 v234, v235, v234
	v_div_scale_f32 v235, vcc, 1.0, v232, 1.0
	v_mul_f32_e32 v236, v235, v234
	v_fma_f32 v237, -v233, v236, v235
	v_fmac_f32_e32 v236, v237, v234
	v_fma_f32 v233, -v233, v236, v235
	s_nop 0
	v_div_fmas_f32 v233, v233, v234, v236
	v_div_fixup_f32 v113, v233, v232, 1.0
	v_mul_f32_e32 v8, v113, v8
	v_mul_f32_e32 v9, v113, v9
	v_mul_f32_e32 v10, v113, v10
	v_mul_f32_e32 v11, v113, v11
; __global__ void __launch_bounds__(NTHR, 2) fwd_kernel(Args args) {
;     ...
;             for (int q = 0; q < 8; ++q) { const float sq = wave_sum(ssq[q]); const float rs = 1.0f / sqrtf(sq * (1.0f / DM) + EPS);
;                 float lg[8];
; #pragma unroll
;                 for (int e = 0; e < 8; ++e) lg[e] = wave_sum(acc[q][e]) * rs;
;                 int i0 = 0; float v0 = lg[0];
; #pragma unroll
;                 for (int e = 1; e < 8; ++e) if (lg[e] > v0) { v0 = lg[e]; i0 = e; }
;                 int i1 = -1; float v1 = -__builtin_inff();
; #pragma unroll
;                 for (int e = 0; e < 8; ++e) if (e != i0 && lg[e] > v1) { v1 = lg[e]; i1 = e; }
;                 if (lane == 0) { const int t = t0 + q; const float w0 = 1.0f / (1.0f + expf(v1 - v0));
;                     tok_e[t] = i0 | (i1 << 8); tok_w[2 * t] = w0; tok_w[2 * t + 1] = 1.0f - w0; rstd3[t] = rs;
	v_mul_f32_e32 v12, v113, v12
	v_mul_f32_e32 v13, v113, v13
	v_mul_f32_e32 v14, v113, v14
	v_mul_f32_e32 v15, v113, v15
	v_mov_b32_e32 v238, v8
	v_mov_b32_e32 v70, 0
	v_cmp_gt_f32_e32 vcc, v9, v238
	s_nop 1
	v_cndmask_b32_e32 v238, v238, v9, vcc
	v_cndmask_b32_e64 v70, v70, 1, vcc
	v_cmp_gt_f32_e32 vcc, v10, v238
	s_nop 1
	v_cndmask_b32_e32 v238, v238, v10, vcc
	v_cndmask_b32_e64 v70, v70, 2, vcc
	v_cmp_gt_f32_e32 vcc, v11, v238
	s_nop 1
	v_cndmask_b32_e32 v238, v238, v11, vcc
	v_cndmask_b32_e64 v70, v70, 3, vcc
	v_cmp_gt_f32_e32 vcc, v12, v238
	s_nop 1
	v_cndmask_b32_e32 v238, v238, v12, vcc
	v_cndmask_b32_e64 v70, v70, 4, vcc
	v_cmp_gt_f32_e32 vcc, v13, v238
	s_nop 1
	v_cndmask_b32_e32 v238, v238, v13, vcc
	v_cndmask_b32_e64 v70, v70, 5, vcc
	v_cmp_gt_f32_e32 vcc, v14, v238
	s_nop 1
	v_cndmask_b32_e32 v238, v238, v14, vcc
	v_cndmask_b32_e64 v70, v70, 6, vcc
	v_cmp_gt_f32_e32 vcc, v15, v238
	s_nop 1
	v_cndmask_b32_e32 v238, v238, v15, vcc
	v_cndmask_b32_e64 v70, v70, 7, vcc
	v_mov_b32_e32 v239, v224
	v_mov_b32_e32 v71, -1
	v_cmp_ne_u32_e64 s[68:69], 0, v70
	v_cmp_gt_f32_e32 vcc, v8, v239
	s_and_b64 vcc, vcc, s[68:69]
	v_cndmask_b32_e32 v239, v239, v8, vcc
	v_cndmask_b32_e64 v71, v71, 0, vcc
	v_cmp_ne_u32_e64 s[68:69], 1, v70
	v_cmp_gt_f32_e32 vcc, v9, v239
	s_and_b64 vcc, vcc, s[68:69]
	v_cndmask_b32_e32 v239, v239, v9, vcc
	v_cndmask_b32_e64 v71, v71, 1, vcc
	v_cmp_ne_u32_e64 s[68:69], 2, v70
	v_cmp_gt_f32_e32 vcc, v10, v239
	s_and_b64 vcc, vcc, s[68:69]
	v_cndmask_b32_e32 v239, v239, v10, vcc
	v_cndmask_b32_e64 v71, v71, 2, vcc
	v_cmp_ne_u32_e64 s[68:69], 3, v70
	v_cmp_gt_f32_e32 vcc, v11, v239
	s_and_b64 vcc, vcc, s[68:69]
	v_cndmask_b32_e32 v239, v239, v11, vcc
	v_cndmask_b32_e64 v71, v71, 3, vcc
	v_cmp_ne_u32_e64 s[68:69], 4, v70
	v_cmp_gt_f32_e32 vcc, v12, v239
	s_and_b64 vcc, vcc, s[68:69]
	v_cndmask_b32_e32 v239, v239, v12, vcc
	v_cndmask_b32_e64 v71, v71, 4, vcc
	v_cmp_ne_u32_e64 s[68:69], 5, v70
	v_cmp_gt_f32_e32 vcc, v13, v239
	s_and_b64 vcc, vcc, s[68:69]
	v_cndmask_b32_e32 v239, v239, v13, vcc
	v_cndmask_b32_e64 v71, v71, 5, vcc
	v_cmp_ne_u32_e64 s[68:69], 6, v70
	v_cmp_gt_f32_e32 vcc, v14, v239
	s_and_b64 vcc, vcc, s[68:69]
	v_cndmask_b32_e32 v239, v239, v14, vcc
	v_cndmask_b32_e64 v71, v71, 6, vcc
	v_cmp_ne_u32_e64 s[68:69], 7, v70
	v_cmp_gt_f32_e32 vcc, v15, v239
	s_and_b64 vcc, vcc, s[68:69]
	v_cndmask_b32_e32 v239, v239, v15, vcc
	v_cndmask_b32_e64 v71, v71, 7, vcc
	v_sub_f32_e32 v232, v239, v238
	v_mul_f32_e32 v233, 0x3fb8aa3b, v232
	v_fma_f32 v234, v232, s65, -v233
	v_rndne_f32_e32 v235, v233
	v_fmac_f32_e32 v234, 0x32a5705f, v232
	v_sub_f32_e32 v233, v233, v235
	v_add_f32_e32 v233, v233, v234
	v_exp_f32_e32 v233, v233
	v_cvt_i32_f32_e32 v234, v235
	v_cmp_ngt_f32_e32 vcc, s66, v232
	v_ldexp_f32 v233, v233, v234
	s_nop 0
	v_cndmask_b32_e32 v233, 0, v233, vcc
	v_cmp_nlt_f32_e32 vcc, s67, v232
	s_nop 1
	v_cndmask_b32_e32 v232, v225, v233, vcc
	v_add_f32_e32 v232, 1.0, v232
	v_div_scale_f32 v233, s[68:69], v232, v232, 1.0
	v_rcp_f32_e32 v234, v233
	s_nop 0
	v_fma_f32 v235, -v233, v234, 1.0
	v_fmac_f32_e32 v234, v235, v234
	v_div_scale_f32 v235, vcc, 1.0, v232, 1.0
	v_mul_f32_e32 v236, v235, v234
	v_fma_f32 v237, -v233, v236, v235
	v_fmac_f32_e32 v236, v237, v234
	v_fma_f32 v233, -v233, v236, v235
	s_nop 0
	v_div_fmas_f32 v233, v233, v234, v236
	v_div_fixup_f32 v72, v233, v232, 1.0
	v_sub_f32_e32 v73, 1.0, v72
	v_lshl_add_u32 v74, v71, 8, v70
	v_fmamk_f32 v232, v196, 0x3a000000, v222
	v_mul_f32_e32 v233, 0x4f800000, v232
	v_cmp_gt_f32_e32 vcc, s63, v232
	s_nop 1
	v_cndmask_b32_e32 v232, v232, v233, vcc
	v_sqrt_f32_e32 v233, v232
	s_nop 0
	v_add_u32_e32 v234, -1, v233
	v_add_u32_e32 v235, 1, v233
	v_fma_f32 v236, -v234, v233, v232
	v_fma_f32 v237, -v235, v233, v232
	v_cmp_ge_f32_e64 s[68:69], 0, v236
	s_nop 1
	v_cndmask_b32_e64 v233, v233, v234, s[68:69]
	v_cmp_lt_f32_e64 s[68:69], 0, v237
	s_nop 1
	v_cndmask_b32_e64 v233, v233, v235, s[68:69]
	v_mul_f32_e32 v234, 0x37800000, v233
	v_cndmask_b32_e32 v233, v233, v234, vcc
	v_cmp_class_f32_e32 vcc, v232, v223
	s_nop 1
	v_cndmask_b32_e32 v232, v233, v232, vcc
	v_div_scale_f32 v233, s[68:69], v232, v232, 1.0
	v_rcp_f32_e32 v234, v233
	s_nop 0
	v_fma_f32 v235, -v233, v234, 1.0
	v_fmac_f32_e32 v234, v235, v234
	v_div_scale_f32 v235, vcc, 1.0, v232, 1.0
	v_mul_f32_e32 v236, v235, v234
	v_fma_f32 v237, -v233, v236, v235
	v_fmac_f32_e32 v236, v237, v234
	v_fma_f32 v233, -v233, v236, v235
	s_nop 0
	v_div_fmas_f32 v233, v233, v234, v236
	v_div_fixup_f32 v114, v233, v232, 1.0
	v_mul_f32_e32 v16, v114, v16
	v_mul_f32_e32 v17, v114, v17
	v_mul_f32_e32 v18, v114, v18
	v_mul_f32_e32 v19, v114, v19
	v_mul_f32_e32 v20, v114, v20
	v_mul_f32_e32 v21, v114, v21
	v_mul_f32_e32 v22, v114, v22
	v_mul_f32_e32 v23, v114, v23
	v_mov_b32_e32 v238, v16
	v_mov_b32_e32 v76, 0
	v_cmp_gt_f32_e32 vcc, v17, v238
	s_nop 1
	v_cndmask_b32_e32 v238, v238, v17, vcc
	v_cndmask_b32_e64 v76, v76, 1, vcc
	v_cmp_gt_f32_e32 vcc, v18, v238
	s_nop 1
	v_cndmask_b32_e32 v238, v238, v18, vcc
	v_cndmask_b32_e64 v76, v76, 2, vcc
	v_cmp_gt_f32_e32 vcc, v19, v238
	s_nop 1
	v_cndmask_b32_e32 v238, v238, v19, vcc
	v_cndmask_b32_e64 v76, v76, 3, vcc
	v_cmp_gt_f32_e32 vcc, v20, v238
	s_nop 1
	v_cndmask_b32_e32 v238, v238, v20, vcc
	v_cndmask_b32_e64 v76, v76, 4, vcc
	v_cmp_gt_f32_e32 vcc, v21, v238
	s_nop 1
	v_cndmask_b32_e32 v238, v238, v21, vcc
	v_cndmask_b32_e64 v76, v76, 5, vcc
	v_cmp_gt_f32_e32 vcc, v22, v238
	s_nop 1
	v_cndmask_b32_e32 v238, v238, v22, vcc
	v_cndmask_b32_e64 v76, v76, 6, vcc
	v_cmp_gt_f32_e32 vcc, v23, v238
	s_nop 1
	v_cndmask_b32_e32 v238, v238, v23, vcc
	v_cndmask_b32_e64 v76, v76, 7, vcc
	v_mov_b32_e32 v239, v224
; __global__ void __launch_bounds__(NTHR, 2) fwd_kernel(Args args) {
;     ...
;             for (int q = 0; q < 8; ++q) { const float sq = wave_sum(ssq[q]); const float rs = 1.0f / sqrtf(sq * (1.0f / DM) + EPS);
;                 float lg[8];
; #pragma unroll
;                 for (int e = 0; e < 8; ++e) lg[e] = wave_sum(acc[q][e]) * rs;
;                 int i0 = 0; float v0 = lg[0];
; #pragma unroll
;                 for (int e = 1; e < 8; ++e) if (lg[e] > v0) { v0 = lg[e]; i0 = e; }
;                 int i1 = -1; float v1 = -__builtin_inff();
; #pragma unroll
;                 for (int e = 0; e < 8; ++e) if (e != i0 && lg[e] > v1) { v1 = lg[e]; i1 = e; }
;                 if (lane == 0) { const int t = t0 + q; const float w0 = 1.0f / (1.0f + expf(v1 - v0));
;                     tok_e[t] = i0 | (i1 << 8); tok_w[2 * t] = w0; tok_w[2 * t + 1] = 1.0f - w0; rstd3[t] = rs;
	v_mov_b32_e32 v77, -1
	v_cmp_ne_u32_e64 s[68:69], 0, v76
	v_cmp_gt_f32_e32 vcc, v16, v239
	s_and_b64 vcc, vcc, s[68:69]
	v_cndmask_b32_e32 v239, v239, v16, vcc
	v_cndmask_b32_e64 v77, v77, 0, vcc
	v_cmp_ne_u32_e64 s[68:69], 1, v76
	v_cmp_gt_f32_e32 vcc, v17, v239
	s_and_b64 vcc, vcc, s[68:69]
	v_cndmask_b32_e32 v239, v239, v17, vcc
	v_cndmask_b32_e64 v77, v77, 1, vcc
	v_cmp_ne_u32_e64 s[68:69], 2, v76
	v_cmp_gt_f32_e32 vcc, v18, v239
	s_and_b64 vcc, vcc, s[68:69]
	v_cndmask_b32_e32 v239, v239, v18, vcc
	v_cndmask_b32_e64 v77, v77, 2, vcc
	v_cmp_ne_u32_e64 s[68:69], 3, v76
	v_cmp_gt_f32_e32 vcc, v19, v239
	s_and_b64 vcc, vcc, s[68:69]
	v_cndmask_b32_e32 v239, v239, v19, vcc
	v_cndmask_b32_e64 v77, v77, 3, vcc
	v_cmp_ne_u32_e64 s[68:69], 4, v76
	v_cmp_gt_f32_e32 vcc, v20, v239
	s_and_b64 vcc, vcc, s[68:69]
	v_cndmask_b32_e32 v239, v239, v20, vcc
	v_cndmask_b32_e64 v77, v77, 4, vcc
	v_cmp_ne_u32_e64 s[68:69], 5, v76
	v_cmp_gt_f32_e32 vcc, v21, v239
	s_and_b64 vcc, vcc, s[68:69]
	v_cndmask_b32_e32 v239, v239, v21, vcc
	v_cndmask_b32_e64 v77, v77, 5, vcc
	v_cmp_ne_u32_e64 s[68:69], 6, v76
	v_cmp_gt_f32_e32 vcc, v22, v239
	s_and_b64 vcc, vcc, s[68:69]
	v_cndmask_b32_e32 v239, v239, v22, vcc
	v_cndmask_b32_e64 v77, v77, 6, vcc
	v_cmp_ne_u32_e64 s[68:69], 7, v76
	v_cmp_gt_f32_e32 vcc, v23, v239
	s_and_b64 vcc, vcc, s[68:69]
	v_cndmask_b32_e32 v239, v239, v23, vcc
	v_cndmask_b32_e64 v77, v77, 7, vcc
	v_sub_f32_e32 v232, v239, v238
	v_mul_f32_e32 v233, 0x3fb8aa3b, v232
	v_fma_f32 v234, v232, s65, -v233
	v_rndne_f32_e32 v235, v233
	v_fmac_f32_e32 v234, 0x32a5705f, v232
	v_sub_f32_e32 v233, v233, v235
	v_add_f32_e32 v233, v233, v234
	v_exp_f32_e32 v233, v233
	v_cvt_i32_f32_e32 v234, v235
	v_cmp_ngt_f32_e32 vcc, s66, v232
	v_ldexp_f32 v233, v233, v234
	s_nop 0
	v_cndmask_b32_e32 v233, 0, v233, vcc
	v_cmp_nlt_f32_e32 vcc, s67, v232
	s_nop 1
	v_cndmask_b32_e32 v232, v225, v233, vcc
	v_add_f32_e32 v232, 1.0, v232
	v_div_scale_f32 v233, s[68:69], v232, v232, 1.0
	v_rcp_f32_e32 v234, v233
	s_nop 0
	v_fma_f32 v235, -v233, v234, 1.0
	v_fmac_f32_e32 v234, v235, v234
	v_div_scale_f32 v235, vcc, 1.0, v232, 1.0
	v_mul_f32_e32 v236, v235, v234
	v_fma_f32 v237, -v233, v236, v235
	v_fmac_f32_e32 v236, v237, v234
	v_fma_f32 v233, -v233, v236, v235
	s_nop 0
	v_div_fmas_f32 v233, v233, v234, v236
	v_div_fixup_f32 v78, v233, v232, 1.0
	v_sub_f32_e32 v79, 1.0, v78
	v_lshl_add_u32 v80, v77, 8, v76
	v_fmamk_f32 v232, v198, 0x3a000000, v222
	v_mul_f32_e32 v233, 0x4f800000, v232
	v_cmp_gt_f32_e32 vcc, s63, v232
	s_nop 1
	v_cndmask_b32_e32 v232, v232, v233, vcc
	v_sqrt_f32_e32 v233, v232
	s_nop 0
	v_add_u32_e32 v234, -1, v233
	v_add_u32_e32 v235, 1, v233
	v_fma_f32 v236, -v234, v233, v232
	v_fma_f32 v237, -v235, v233, v232
	v_cmp_ge_f32_e64 s[68:69], 0, v236
	s_nop 1
	v_cndmask_b32_e64 v233, v233, v234, s[68:69]
	v_cmp_lt_f32_e64 s[68:69], 0, v237
	s_nop 1
	v_cndmask_b32_e64 v233, v233, v235, s[68:69]
	v_mul_f32_e32 v234, 0x37800000, v233
	v_cndmask_b32_e32 v233, v233, v234, vcc
	v_cmp_class_f32_e32 vcc, v232, v223
	s_nop 1
	v_cndmask_b32_e32 v232, v233, v232, vcc
	v_div_scale_f32 v233, s[68:69], v232, v232, 1.0
	v_rcp_f32_e32 v234, v233
	s_nop 0
	v_fma_f32 v235, -v233, v234, 1.0
	v_fmac_f32_e32 v234, v235, v234
	v_div_scale_f32 v235, vcc, 1.0, v232, 1.0
	v_mul_f32_e32 v236, v235, v234
	v_fma_f32 v237, -v233, v236, v235
	v_fmac_f32_e32 v236, v237, v234
	v_fma_f32 v233, -v233, v236, v235
	s_nop 0
	v_div_fmas_f32 v233, v233, v234, v236
	v_div_fixup_f32 v115, v233, v232, 1.0
	v_mul_f32_e32 v24, v115, v24
	v_mul_f32_e32 v25, v115, v25
	v_mul_f32_e32 v26, v115, v26
	v_mul_f32_e32 v27, v115, v27
	v_mul_f32_e32 v28, v115, v28
	v_mul_f32_e32 v29, v115, v29
	v_mul_f32_e32 v30, v115, v30
	v_mul_f32_e32 v31, v115, v31
	v_mov_b32_e32 v238, v24
	v_mov_b32_e32 v82, 0
	v_cmp_gt_f32_e32 vcc, v25, v238
	s_nop 1
	v_cndmask_b32_e32 v238, v238, v25, vcc
	v_cndmask_b32_e64 v82, v82, 1, vcc
	v_cmp_gt_f32_e32 vcc, v26, v238
	s_nop 1
	v_cndmask_b32_e32 v238, v238, v26, vcc
	v_cndmask_b32_e64 v82, v82, 2, vcc
	v_cmp_gt_f32_e32 vcc, v27, v238
	s_nop 1
	v_cndmask_b32_e32 v238, v238, v27, vcc
	v_cndmask_b32_e64 v82, v82, 3, vcc
	v_cmp_gt_f32_e32 vcc, v28, v238
	s_nop 1
	v_cndmask_b32_e32 v238, v238, v28, vcc
	v_cndmask_b32_e64 v82, v82, 4, vcc
	v_cmp_gt_f32_e32 vcc, v29, v238
	s_nop 1
	v_cndmask_b32_e32 v238, v238, v29, vcc
	v_cndmask_b32_e64 v82, v82, 5, vcc
	v_cmp_gt_f32_e32 vcc, v30, v238
	s_nop 1
	v_cndmask_b32_e32 v238, v238, v30, vcc
	v_cndmask_b32_e64 v82, v82, 6, vcc
	v_cmp_gt_f32_e32 vcc, v31, v238
	s_nop 1
	v_cndmask_b32_e32 v238, v238, v31, vcc
	v_cndmask_b32_e64 v82, v82, 7, vcc
	v_mov_b32_e32 v239, v224
	v_mov_b32_e32 v83, -1
	v_cmp_ne_u32_e64 s[68:69], 0, v82
	v_cmp_gt_f32_e32 vcc, v24, v239
	s_and_b64 vcc, vcc, s[68:69]
	v_cndmask_b32_e32 v239, v239, v24, vcc
	v_cndmask_b32_e64 v83, v83, 0, vcc
	v_cmp_ne_u32_e64 s[68:69], 1, v82
	v_cmp_gt_f32_e32 vcc, v25, v239
	s_and_b64 vcc, vcc, s[68:69]
	v_cndmask_b32_e32 v239, v239, v25, vcc
	v_cndmask_b32_e64 v83, v83, 1, vcc
	v_cmp_ne_u32_e64 s[68:69], 2, v82
	v_cmp_gt_f32_e32 vcc, v26, v239
	s_and_b64 vcc, vcc, s[68:69]
	v_cndmask_b32_e32 v239, v239, v26, vcc
	v_cndmask_b32_e64 v83, v83, 2, vcc
	v_cmp_ne_u32_e64 s[68:69], 3, v82
	v_cmp_gt_f32_e32 vcc, v27, v239
	s_and_b64 vcc, vcc, s[68:69]
	v_cndmask_b32_e32 v239, v239, v27, vcc
	v_cndmask_b32_e64 v83, v83, 3, vcc
	v_cmp_ne_u32_e64 s[68:69], 4, v82
	v_cmp_gt_f32_e32 vcc, v28, v239
	s_and_b64 vcc, vcc, s[68:69]
	v_cndmask_b32_e32 v239, v239, v28, vcc
	v_cndmask_b32_e64 v83, v83, 4, vcc
	v_cmp_ne_u32_e64 s[68:69], 5, v82
	v_cmp_gt_f32_e32 vcc, v29, v239
	s_and_b64 vcc, vcc, s[68:69]
; __global__ void __launch_bounds__(NTHR, 2) fwd_kernel(Args args) {
;     ...
;             for (int q = 0; q < 8; ++q) { const float sq = wave_sum(ssq[q]); const float rs = 1.0f / sqrtf(sq * (1.0f / DM) + EPS);
;                 float lg[8];
; #pragma unroll
;                 for (int e = 0; e < 8; ++e) lg[e] = wave_sum(acc[q][e]) * rs;
;                 int i0 = 0; float v0 = lg[0];
; #pragma unroll
;                 for (int e = 1; e < 8; ++e) if (lg[e] > v0) { v0 = lg[e]; i0 = e; }
;                 int i1 = -1; float v1 = -__builtin_inff();
; #pragma unroll
;                 for (int e = 0; e < 8; ++e) if (e != i0 && lg[e] > v1) { v1 = lg[e]; i1 = e; }
;                 if (lane == 0) { const int t = t0 + q; const float w0 = 1.0f / (1.0f + expf(v1 - v0));
;                     tok_e[t] = i0 | (i1 << 8); tok_w[2 * t] = w0; tok_w[2 * t + 1] = 1.0f - w0; rstd3[t] = rs;
	v_cndmask_b32_e32 v239, v239, v29, vcc
	v_cndmask_b32_e64 v83, v83, 5, vcc
	v_cmp_ne_u32_e64 s[68:69], 6, v82
	v_cmp_gt_f32_e32 vcc, v30, v239
	s_and_b64 vcc, vcc, s[68:69]
	v_cndmask_b32_e32 v239, v239, v30, vcc
	v_cndmask_b32_e64 v83, v83, 6, vcc
	v_cmp_ne_u32_e64 s[68:69], 7, v82
	v_cmp_gt_f32_e32 vcc, v31, v239
	s_and_b64 vcc, vcc, s[68:69]
	v_cndmask_b32_e32 v239, v239, v31, vcc
	v_cndmask_b32_e64 v83, v83, 7, vcc
	v_sub_f32_e32 v232, v239, v238
	v_mul_f32_e32 v233, 0x3fb8aa3b, v232
	v_fma_f32 v234, v232, s65, -v233
	v_rndne_f32_e32 v235, v233
	v_fmac_f32_e32 v234, 0x32a5705f, v232
	v_sub_f32_e32 v233, v233, v235
	v_add_f32_e32 v233, v233, v234
	v_exp_f32_e32 v233, v233
	v_cvt_i32_f32_e32 v234, v235
	v_cmp_ngt_f32_e32 vcc, s66, v232
	v_ldexp_f32 v233, v233, v234
	s_nop 0
	v_cndmask_b32_e32 v233, 0, v233, vcc
	v_cmp_nlt_f32_e32 vcc, s67, v232
	s_nop 1
	v_cndmask_b32_e32 v232, v225, v233, vcc
	v_add_f32_e32 v232, 1.0, v232
	v_div_scale_f32 v233, s[68:69], v232, v232, 1.0
	v_rcp_f32_e32 v234, v233
	s_nop 0
	v_fma_f32 v235, -v233, v234, 1.0
	v_fmac_f32_e32 v234, v235, v234
	v_div_scale_f32 v235, vcc, 1.0, v232, 1.0
	v_mul_f32_e32 v236, v235, v234
	v_fma_f32 v237, -v233, v236, v235
	v_fmac_f32_e32 v236, v237, v234
	v_fma_f32 v233, -v233, v236, v235
	s_nop 0
	v_div_fmas_f32 v233, v233, v234, v236
	v_div_fixup_f32 v84, v233, v232, 1.0
	v_sub_f32_e32 v85, 1.0, v84
	v_lshl_add_u32 v86, v83, 8, v82
	v_fmamk_f32 v232, v200, 0x3a000000, v222
	v_mul_f32_e32 v233, 0x4f800000, v232
	v_cmp_gt_f32_e32 vcc, s63, v232
	s_nop 1
	v_cndmask_b32_e32 v232, v232, v233, vcc
	v_sqrt_f32_e32 v233, v232
	s_nop 0
	v_add_u32_e32 v234, -1, v233
	v_add_u32_e32 v235, 1, v233
	v_fma_f32 v236, -v234, v233, v232
	v_fma_f32 v237, -v235, v233, v232
	v_cmp_ge_f32_e64 s[68:69], 0, v236
	s_nop 1
	v_cndmask_b32_e64 v233, v233, v234, s[68:69]
	v_cmp_lt_f32_e64 s[68:69], 0, v237
	s_nop 1
	v_cndmask_b32_e64 v233, v233, v235, s[68:69]
	v_mul_f32_e32 v234, 0x37800000, v233
	v_cndmask_b32_e32 v233, v233, v234, vcc
	v_cmp_class_f32_e32 vcc, v232, v223
	s_nop 1
	v_cndmask_b32_e32 v232, v233, v232, vcc
	v_div_scale_f32 v233, s[68:69], v232, v232, 1.0
	v_rcp_f32_e32 v234, v233
	s_nop 0
	v_fma_f32 v235, -v233, v234, 1.0
	v_fmac_f32_e32 v234, v235, v234
	v_div_scale_f32 v235, vcc, 1.0, v232, 1.0
	v_mul_f32_e32 v236, v235, v234
	v_fma_f32 v237, -v233, v236, v235
	v_fmac_f32_e32 v236, v237, v234
	v_fma_f32 v233, -v233, v236, v235
	s_nop 0
	v_div_fmas_f32 v233, v233, v234, v236
	v_div_fixup_f32 v116, v233, v232, 1.0
	v_mul_f32_e32 v32, v116, v32
	v_mul_f32_e32 v33, v116, v33
	v_mul_f32_e32 v34, v116, v34
	v_mul_f32_e32 v35, v116, v35
	v_mul_f32_e32 v36, v116, v36
	v_mul_f32_e32 v37, v116, v37
	v_mul_f32_e32 v38, v116, v38
	v_mul_f32_e32 v39, v116, v39
	v_mov_b32_e32 v238, v32
	v_mov_b32_e32 v88, 0
	v_cmp_gt_f32_e32 vcc, v33, v238
	s_nop 1
	v_cndmask_b32_e32 v238, v238, v33, vcc
	v_cndmask_b32_e64 v88, v88, 1, vcc
	v_cmp_gt_f32_e32 vcc, v34, v238
	s_nop 1
	v_cndmask_b32_e32 v238, v238, v34, vcc
	v_cndmask_b32_e64 v88, v88, 2, vcc
	v_cmp_gt_f32_e32 vcc, v35, v238
	s_nop 1
	v_cndmask_b32_e32 v238, v238, v35, vcc
	v_cndmask_b32_e64 v88, v88, 3, vcc
	v_cmp_gt_f32_e32 vcc, v36, v238
	s_nop 1
	v_cndmask_b32_e32 v238, v238, v36, vcc
	v_cndmask_b32_e64 v88, v88, 4, vcc
	v_cmp_gt_f32_e32 vcc, v37, v238
	s_nop 1
	v_cndmask_b32_e32 v238, v238, v37, vcc
	v_cndmask_b32_e64 v88, v88, 5, vcc
	v_cmp_gt_f32_e32 vcc, v38, v238
	s_nop 1
	v_cndmask_b32_e32 v238, v238, v38, vcc
	v_cndmask_b32_e64 v88, v88, 6, vcc
	v_cmp_gt_f32_e32 vcc, v39, v238
	s_nop 1
	v_cndmask_b32_e32 v238, v238, v39, vcc
	v_cndmask_b32_e64 v88, v88, 7, vcc
	v_mov_b32_e32 v239, v224
	v_mov_b32_e32 v89, -1
	v_cmp_ne_u32_e64 s[68:69], 0, v88
	v_cmp_gt_f32_e32 vcc, v32, v239
	s_and_b64 vcc, vcc, s[68:69]
	v_cndmask_b32_e32 v239, v239, v32, vcc
	v_cndmask_b32_e64 v89, v89, 0, vcc
	v_cmp_ne_u32_e64 s[68:69], 1, v88
	v_cmp_gt_f32_e32 vcc, v33, v239
	s_and_b64 vcc, vcc, s[68:69]
	v_cndmask_b32_e32 v239, v239, v33, vcc
	v_cndmask_b32_e64 v89, v89, 1, vcc
	v_cmp_ne_u32_e64 s[68:69], 2, v88
	v_cmp_gt_f32_e32 vcc, v34, v239
	s_and_b64 vcc, vcc, s[68:69]
	v_cndmask_b32_e32 v239, v239, v34, vcc
	v_cndmask_b32_e64 v89, v89, 2, vcc
	v_cmp_ne_u32_e64 s[68:69], 3, v88
	v_cmp_gt_f32_e32 vcc, v35, v239
	s_and_b64 vcc, vcc, s[68:69]
	v_cndmask_b32_e32 v239, v239, v35, vcc
	v_cndmask_b32_e64 v89, v89, 3, vcc
	v_cmp_ne_u32_e64 s[68:69], 4, v88
	v_cmp_gt_f32_e32 vcc, v36, v239
	s_and_b64 vcc, vcc, s[68:69]
	v_cndmask_b32_e32 v239, v239, v36, vcc
	v_cndmask_b32_e64 v89, v89, 4, vcc
	v_cmp_ne_u32_e64 s[68:69], 5, v88
	v_cmp_gt_f32_e32 vcc, v37, v239
	s_and_b64 vcc, vcc, s[68:69]
	v_cndmask_b32_e32 v239, v239, v37, vcc
	v_cndmask_b32_e64 v89, v89, 5, vcc
	v_cmp_ne_u32_e64 s[68:69], 6, v88
	v_cmp_gt_f32_e32 vcc, v38, v239
	s_and_b64 vcc, vcc, s[68:69]
	v_cndmask_b32_e32 v239, v239, v38, vcc
	v_cndmask_b32_e64 v89, v89, 6, vcc
	v_cmp_ne_u32_e64 s[68:69], 7, v88
	v_cmp_gt_f32_e32 vcc, v39, v239
	s_and_b64 vcc, vcc, s[68:69]
	v_cndmask_b32_e32 v239, v239, v39, vcc
	v_cndmask_b32_e64 v89, v89, 7, vcc
	v_sub_f32_e32 v232, v239, v238
	v_mul_f32_e32 v233, 0x3fb8aa3b, v232
	v_fma_f32 v234, v232, s65, -v233
	v_rndne_f32_e32 v235, v233
	v_fmac_f32_e32 v234, 0x32a5705f, v232
	v_sub_f32_e32 v233, v233, v235
	v_add_f32_e32 v233, v233, v234
	v_exp_f32_e32 v233, v233
	v_cvt_i32_f32_e32 v234, v235
	v_cmp_ngt_f32_e32 vcc, s66, v232
	v_ldexp_f32 v233, v233, v234
	s_nop 0
	v_cndmask_b32_e32 v233, 0, v233, vcc
	v_cmp_nlt_f32_e32 vcc, s67, v232
	s_nop 1
	v_cndmask_b32_e32 v232, v225, v233, vcc
	v_add_f32_e32 v232, 1.0, v232
	v_div_scale_f32 v233, s[68:69], v232, v232, 1.0
; __global__ void __launch_bounds__(NTHR, 2) fwd_kernel(Args args) {
;     ...
;             for (int q = 0; q < 8; ++q) { const float sq = wave_sum(ssq[q]); const float rs = 1.0f / sqrtf(sq * (1.0f / DM) + EPS);
;                 float lg[8];
; #pragma unroll
;                 for (int e = 0; e < 8; ++e) lg[e] = wave_sum(acc[q][e]) * rs;
;                 int i0 = 0; float v0 = lg[0];
; #pragma unroll
;                 for (int e = 1; e < 8; ++e) if (lg[e] > v0) { v0 = lg[e]; i0 = e; }
;                 int i1 = -1; float v1 = -__builtin_inff();
; #pragma unroll
;                 for (int e = 0; e < 8; ++e) if (e != i0 && lg[e] > v1) { v1 = lg[e]; i1 = e; }
;                 if (lane == 0) { const int t = t0 + q; const float w0 = 1.0f / (1.0f + expf(v1 - v0));
;                     tok_e[t] = i0 | (i1 << 8); tok_w[2 * t] = w0; tok_w[2 * t + 1] = 1.0f - w0; rstd3[t] = rs;
	v_rcp_f32_e32 v234, v233
	s_nop 0
	v_fma_f32 v235, -v233, v234, 1.0
	v_fmac_f32_e32 v234, v235, v234
	v_div_scale_f32 v235, vcc, 1.0, v232, 1.0
	v_mul_f32_e32 v236, v235, v234
	v_fma_f32 v237, -v233, v236, v235
	v_fmac_f32_e32 v236, v237, v234
	v_fma_f32 v233, -v233, v236, v235
	s_nop 0
	v_div_fmas_f32 v233, v233, v234, v236
	v_div_fixup_f32 v90, v233, v232, 1.0
	v_sub_f32_e32 v91, 1.0, v90
	v_lshl_add_u32 v92, v89, 8, v88
	v_fmamk_f32 v232, v202, 0x3a000000, v222
	v_mul_f32_e32 v233, 0x4f800000, v232
	v_cmp_gt_f32_e32 vcc, s63, v232
	s_nop 1
	v_cndmask_b32_e32 v232, v232, v233, vcc
	v_sqrt_f32_e32 v233, v232
	s_nop 0
	v_add_u32_e32 v234, -1, v233
	v_add_u32_e32 v235, 1, v233
	v_fma_f32 v236, -v234, v233, v232
	v_fma_f32 v237, -v235, v233, v232
	v_cmp_ge_f32_e64 s[68:69], 0, v236
	s_nop 1
	v_cndmask_b32_e64 v233, v233, v234, s[68:69]
	v_cmp_lt_f32_e64 s[68:69], 0, v237
	s_nop 1
	v_cndmask_b32_e64 v233, v233, v235, s[68:69]
	v_mul_f32_e32 v234, 0x37800000, v233
	v_cndmask_b32_e32 v233, v233, v234, vcc
	v_cmp_class_f32_e32 vcc, v232, v223
	s_nop 1
	v_cndmask_b32_e32 v232, v233, v232, vcc
	v_div_scale_f32 v233, s[68:69], v232, v232, 1.0
	v_rcp_f32_e32 v234, v233
	s_nop 0
	v_fma_f32 v235, -v233, v234, 1.0
	v_fmac_f32_e32 v234, v235, v234
	v_div_scale_f32 v235, vcc, 1.0, v232, 1.0
	v_mul_f32_e32 v236, v235, v234
	v_fma_f32 v237, -v233, v236, v235
	v_fmac_f32_e32 v236, v237, v234
	v_fma_f32 v233, -v233, v236, v235
	s_nop 0
	v_div_fmas_f32 v233, v233, v234, v236
	v_div_fixup_f32 v117, v233, v232, 1.0
	v_mul_f32_e32 v40, v117, v40
	v_mul_f32_e32 v41, v117, v41
	v_mul_f32_e32 v42, v117, v42
	v_mul_f32_e32 v43, v117, v43
	v_mul_f32_e32 v44, v117, v44
	v_mul_f32_e32 v45, v117, v45
	v_mul_f32_e32 v46, v117, v46
	v_mul_f32_e32 v47, v117, v47
	v_mov_b32_e32 v238, v40
	v_mov_b32_e32 v94, 0
	v_cmp_gt_f32_e32 vcc, v41, v238
	s_nop 1
	v_cndmask_b32_e32 v238, v238, v41, vcc
	v_cndmask_b32_e64 v94, v94, 1, vcc
	v_cmp_gt_f32_e32 vcc, v42, v238
	s_nop 1
	v_cndmask_b32_e32 v238, v238, v42, vcc
	v_cndmask_b32_e64 v94, v94, 2, vcc
	v_cmp_gt_f32_e32 vcc, v43, v238
	s_nop 1
	v_cndmask_b32_e32 v238, v238, v43, vcc
	v_cndmask_b32_e64 v94, v94, 3, vcc
	v_cmp_gt_f32_e32 vcc, v44, v238
	s_nop 1
	v_cndmask_b32_e32 v238, v238, v44, vcc
	v_cndmask_b32_e64 v94, v94, 4, vcc
	v_cmp_gt_f32_e32 vcc, v45, v238
	s_nop 1
	v_cndmask_b32_e32 v238, v238, v45, vcc
	v_cndmask_b32_e64 v94, v94, 5, vcc
	v_cmp_gt_f32_e32 vcc, v46, v238
	s_nop 1
	v_cndmask_b32_e32 v238, v238, v46, vcc
	v_cndmask_b32_e64 v94, v94, 6, vcc
	v_cmp_gt_f32_e32 vcc, v47, v238
	s_nop 1
	v_cndmask_b32_e32 v238, v238, v47, vcc
	v_cndmask_b32_e64 v94, v94, 7, vcc
	v_mov_b32_e32 v239, v224
	v_mov_b32_e32 v95, -1
	v_cmp_ne_u32_e64 s[68:69], 0, v94
	v_cmp_gt_f32_e32 vcc, v40, v239
	s_and_b64 vcc, vcc, s[68:69]
	v_cndmask_b32_e32 v239, v239, v40, vcc
	v_cndmask_b32_e64 v95, v95, 0, vcc
	v_cmp_ne_u32_e64 s[68:69], 1, v94
	v_cmp_gt_f32_e32 vcc, v41, v239
	s_and_b64 vcc, vcc, s[68:69]
	v_cndmask_b32_e32 v239, v239, v41, vcc
	v_cndmask_b32_e64 v95, v95, 1, vcc
	v_cmp_ne_u32_e64 s[68:69], 2, v94
	v_cmp_gt_f32_e32 vcc, v42, v239
	s_and_b64 vcc, vcc, s[68:69]
	v_cndmask_b32_e32 v239, v239, v42, vcc
	v_cndmask_b32_e64 v95, v95, 2, vcc
	v_cmp_ne_u32_e64 s[68:69], 3, v94
	v_cmp_gt_f32_e32 vcc, v43, v239
	s_and_b64 vcc, vcc, s[68:69]
	v_cndmask_b32_e32 v239, v239, v43, vcc
	v_cndmask_b32_e64 v95, v95, 3, vcc
	v_cmp_ne_u32_e64 s[68:69], 4, v94
	v_cmp_gt_f32_e32 vcc, v44, v239
	s_and_b64 vcc, vcc, s[68:69]
	v_cndmask_b32_e32 v239, v239, v44, vcc
	v_cndmask_b32_e64 v95, v95, 4, vcc
	v_cmp_ne_u32_e64 s[68:69], 5, v94
	v_cmp_gt_f32_e32 vcc, v45, v239
	s_and_b64 vcc, vcc, s[68:69]
	v_cndmask_b32_e32 v239, v239, v45, vcc
	v_cndmask_b32_e64 v95, v95, 5, vcc
	v_cmp_ne_u32_e64 s[68:69], 6, v94
	v_cmp_gt_f32_e32 vcc, v46, v239
	s_and_b64 vcc, vcc, s[68:69]
	v_cndmask_b32_e32 v239, v239, v46, vcc
	v_cndmask_b32_e64 v95, v95, 6, vcc
	v_cmp_ne_u32_e64 s[68:69], 7, v94
	v_cmp_gt_f32_e32 vcc, v47, v239
	s_and_b64 vcc, vcc, s[68:69]
	v_cndmask_b32_e32 v239, v239, v47, vcc
	v_cndmask_b32_e64 v95, v95, 7, vcc
	v_sub_f32_e32 v232, v239, v238
	v_mul_f32_e32 v233, 0x3fb8aa3b, v232
	v_fma_f32 v234, v232, s65, -v233
	v_rndne_f32_e32 v235, v233
	v_fmac_f32_e32 v234, 0x32a5705f, v232
	v_sub_f32_e32 v233, v233, v235
	v_add_f32_e32 v233, v233, v234
	v_exp_f32_e32 v233, v233
	v_cvt_i32_f32_e32 v234, v235
	v_cmp_ngt_f32_e32 vcc, s66, v232
	v_ldexp_f32 v233, v233, v234
	s_nop 0
	v_cndmask_b32_e32 v233, 0, v233, vcc
	v_cmp_nlt_f32_e32 vcc, s67, v232
	s_nop 1
	v_cndmask_b32_e32 v232, v225, v233, vcc
	v_add_f32_e32 v232, 1.0, v232
	v_div_scale_f32 v233, s[68:69], v232, v232, 1.0
	v_rcp_f32_e32 v234, v233
	s_nop 0
	v_fma_f32 v235, -v233, v234, 1.0
	v_fmac_f32_e32 v234, v235, v234
	v_div_scale_f32 v235, vcc, 1.0, v232, 1.0
	v_mul_f32_e32 v236, v235, v234
	v_fma_f32 v237, -v233, v236, v235
	v_fmac_f32_e32 v236, v237, v234
	v_fma_f32 v233, -v233, v236, v235
	s_nop 0
	v_div_fmas_f32 v233, v233, v234, v236
	v_div_fixup_f32 v96, v233, v232, 1.0
	v_sub_f32_e32 v97, 1.0, v96
	v_lshl_add_u32 v98, v95, 8, v94
	v_fmamk_f32 v232, v204, 0x3a000000, v222
	v_mul_f32_e32 v233, 0x4f800000, v232
	v_cmp_gt_f32_e32 vcc, s63, v232
	s_nop 1
	v_cndmask_b32_e32 v232, v232, v233, vcc
	v_sqrt_f32_e32 v233, v232
	s_nop 0
	v_add_u32_e32 v234, -1, v233
	v_add_u32_e32 v235, 1, v233
	v_fma_f32 v236, -v234, v233, v232
	v_fma_f32 v237, -v235, v233, v232
	v_cmp_ge_f32_e64 s[68:69], 0, v236
	s_nop 1
	v_cndmask_b32_e64 v233, v233, v234, s[68:69]
	v_cmp_lt_f32_e64 s[68:69], 0, v237
	s_nop 1
	v_cndmask_b32_e64 v233, v233, v235, s[68:69]
	v_mul_f32_e32 v234, 0x37800000, v233
	v_cndmask_b32_e32 v233, v233, v234, vcc
; __global__ void __launch_bounds__(NTHR, 2) fwd_kernel(Args args) {
;     ...
;             for (int q = 0; q < 8; ++q) { const float sq = wave_sum(ssq[q]); const float rs = 1.0f / sqrtf(sq * (1.0f / DM) + EPS);
;                 float lg[8];
; #pragma unroll
;                 for (int e = 0; e < 8; ++e) lg[e] = wave_sum(acc[q][e]) * rs;
;                 int i0 = 0; float v0 = lg[0];
; #pragma unroll
;                 for (int e = 1; e < 8; ++e) if (lg[e] > v0) { v0 = lg[e]; i0 = e; }
;                 int i1 = -1; float v1 = -__builtin_inff();
; #pragma unroll
;                 for (int e = 0; e < 8; ++e) if (e != i0 && lg[e] > v1) { v1 = lg[e]; i1 = e; }
;                 if (lane == 0) { const int t = t0 + q; const float w0 = 1.0f / (1.0f + expf(v1 - v0));
;                     tok_e[t] = i0 | (i1 << 8); tok_w[2 * t] = w0; tok_w[2 * t + 1] = 1.0f - w0; rstd3[t] = rs;
	v_cmp_class_f32_e32 vcc, v232, v223
	s_nop 1
	v_cndmask_b32_e32 v232, v233, v232, vcc
	v_div_scale_f32 v233, s[68:69], v232, v232, 1.0
	v_rcp_f32_e32 v234, v233
	s_nop 0
	v_fma_f32 v235, -v233, v234, 1.0
	v_fmac_f32_e32 v234, v235, v234
	v_div_scale_f32 v235, vcc, 1.0, v232, 1.0
	v_mul_f32_e32 v236, v235, v234
	v_fma_f32 v237, -v233, v236, v235
	v_fmac_f32_e32 v236, v237, v234
	v_fma_f32 v233, -v233, v236, v235
	s_nop 0
	v_div_fmas_f32 v233, v233, v234, v236
	v_div_fixup_f32 v118, v233, v232, 1.0
	v_mul_f32_e32 v48, v118, v48
	v_mul_f32_e32 v49, v118, v49
	v_mul_f32_e32 v50, v118, v50
	v_mul_f32_e32 v51, v118, v51
	v_mul_f32_e32 v52, v118, v52
	v_mul_f32_e32 v53, v118, v53
	v_mul_f32_e32 v54, v118, v54
	v_mul_f32_e32 v55, v118, v55
	v_mov_b32_e32 v238, v48
	v_mov_b32_e32 v100, 0
	v_cmp_gt_f32_e32 vcc, v49, v238
	s_nop 1
	v_cndmask_b32_e32 v238, v238, v49, vcc
	v_cndmask_b32_e64 v100, v100, 1, vcc
	v_cmp_gt_f32_e32 vcc, v50, v238
	s_nop 1
	v_cndmask_b32_e32 v238, v238, v50, vcc
	v_cndmask_b32_e64 v100, v100, 2, vcc
	v_cmp_gt_f32_e32 vcc, v51, v238
	s_nop 1
	v_cndmask_b32_e32 v238, v238, v51, vcc
	v_cndmask_b32_e64 v100, v100, 3, vcc
	v_cmp_gt_f32_e32 vcc, v52, v238
	s_nop 1
	v_cndmask_b32_e32 v238, v238, v52, vcc
	v_cndmask_b32_e64 v100, v100, 4, vcc
	v_cmp_gt_f32_e32 vcc, v53, v238
	s_nop 1
	v_cndmask_b32_e32 v238, v238, v53, vcc
	v_cndmask_b32_e64 v100, v100, 5, vcc
	v_cmp_gt_f32_e32 vcc, v54, v238
	s_nop 1
	v_cndmask_b32_e32 v238, v238, v54, vcc
	v_cndmask_b32_e64 v100, v100, 6, vcc
	v_cmp_gt_f32_e32 vcc, v55, v238
	s_nop 1
	v_cndmask_b32_e32 v238, v238, v55, vcc
	v_cndmask_b32_e64 v100, v100, 7, vcc
	v_mov_b32_e32 v239, v224
	v_mov_b32_e32 v101, -1
	v_cmp_ne_u32_e64 s[68:69], 0, v100
	v_cmp_gt_f32_e32 vcc, v48, v239
	s_and_b64 vcc, vcc, s[68:69]
	v_cndmask_b32_e32 v239, v239, v48, vcc
	v_cndmask_b32_e64 v101, v101, 0, vcc
	v_cmp_ne_u32_e64 s[68:69], 1, v100
	v_cmp_gt_f32_e32 vcc, v49, v239
	s_and_b64 vcc, vcc, s[68:69]
	v_cndmask_b32_e32 v239, v239, v49, vcc
	v_cndmask_b32_e64 v101, v101, 1, vcc
	v_cmp_ne_u32_e64 s[68:69], 2, v100
	v_cmp_gt_f32_e32 vcc, v50, v239
	s_and_b64 vcc, vcc, s[68:69]
	v_cndmask_b32_e32 v239, v239, v50, vcc
	v_cndmask_b32_e64 v101, v101, 2, vcc
	v_cmp_ne_u32_e64 s[68:69], 3, v100
	v_cmp_gt_f32_e32 vcc, v51, v239
	s_and_b64 vcc, vcc, s[68:69]
	v_cndmask_b32_e32 v239, v239, v51, vcc
	v_cndmask_b32_e64 v101, v101, 3, vcc
	v_cmp_ne_u32_e64 s[68:69], 4, v100
	v_cmp_gt_f32_e32 vcc, v52, v239
	s_and_b64 vcc, vcc, s[68:69]
	v_cndmask_b32_e32 v239, v239, v52, vcc
	v_cndmask_b32_e64 v101, v101, 4, vcc
	v_cmp_ne_u32_e64 s[68:69], 5, v100
	v_cmp_gt_f32_e32 vcc, v53, v239
	s_and_b64 vcc, vcc, s[68:69]
	v_cndmask_b32_e32 v239, v239, v53, vcc
	v_cndmask_b32_e64 v101, v101, 5, vcc
	v_cmp_ne_u32_e64 s[68:69], 6, v100
	v_cmp_gt_f32_e32 vcc, v54, v239
	s_and_b64 vcc, vcc, s[68:69]
	v_cndmask_b32_e32 v239, v239, v54, vcc
	v_cndmask_b32_e64 v101, v101, 6, vcc
	v_cmp_ne_u32_e64 s[68:69], 7, v100
	v_cmp_gt_f32_e32 vcc, v55, v239
	s_and_b64 vcc, vcc, s[68:69]
	v_cndmask_b32_e32 v239, v239, v55, vcc
	v_cndmask_b32_e64 v101, v101, 7, vcc
	v_sub_f32_e32 v232, v239, v238
	v_mul_f32_e32 v233, 0x3fb8aa3b, v232
	v_fma_f32 v234, v232, s65, -v233
	v_rndne_f32_e32 v235, v233
	v_fmac_f32_e32 v234, 0x32a5705f, v232
	v_sub_f32_e32 v233, v233, v235
	v_add_f32_e32 v233, v233, v234
	v_exp_f32_e32 v233, v233
	v_cvt_i32_f32_e32 v234, v235
	v_cmp_ngt_f32_e32 vcc, s66, v232
	v_ldexp_f32 v233, v233, v234
	s_nop 0
	v_cndmask_b32_e32 v233, 0, v233, vcc
	v_cmp_nlt_f32_e32 vcc, s67, v232
	s_nop 1
	v_cndmask_b32_e32 v232, v225, v233, vcc
	v_add_f32_e32 v232, 1.0, v232
	v_div_scale_f32 v233, s[68:69], v232, v232, 1.0
	v_rcp_f32_e32 v234, v233
	s_nop 0
	v_fma_f32 v235, -v233, v234, 1.0
	v_fmac_f32_e32 v234, v235, v234
	v_div_scale_f32 v235, vcc, 1.0, v232, 1.0
	v_mul_f32_e32 v236, v235, v234
	v_fma_f32 v237, -v233, v236, v235
	v_fmac_f32_e32 v236, v237, v234
	v_fma_f32 v233, -v233, v236, v235
	s_nop 0
	v_div_fmas_f32 v233, v233, v234, v236
	v_div_fixup_f32 v102, v233, v232, 1.0
	v_sub_f32_e32 v103, 1.0, v102
	v_lshl_add_u32 v104, v101, 8, v100
	v_fmamk_f32 v232, v206, 0x3a000000, v222
	v_mul_f32_e32 v233, 0x4f800000, v232
	v_cmp_gt_f32_e32 vcc, s63, v232
	s_nop 1
	v_cndmask_b32_e32 v232, v232, v233, vcc
	v_sqrt_f32_e32 v233, v232
	s_nop 0
	v_add_u32_e32 v234, -1, v233
	v_add_u32_e32 v235, 1, v233
	v_fma_f32 v236, -v234, v233, v232
	v_fma_f32 v237, -v235, v233, v232
	v_cmp_ge_f32_e64 s[68:69], 0, v236
	s_nop 1
	v_cndmask_b32_e64 v233, v233, v234, s[68:69]
	v_cmp_lt_f32_e64 s[68:69], 0, v237
	s_nop 1
	v_cndmask_b32_e64 v233, v233, v235, s[68:69]
	v_mul_f32_e32 v234, 0x37800000, v233
	v_cndmask_b32_e32 v233, v233, v234, vcc
	v_cmp_class_f32_e32 vcc, v232, v223
	s_nop 1
	v_cndmask_b32_e32 v232, v233, v232, vcc
	v_div_scale_f32 v233, s[68:69], v232, v232, 1.0
	v_rcp_f32_e32 v234, v233
	s_nop 0
	v_fma_f32 v235, -v233, v234, 1.0
	v_fmac_f32_e32 v234, v235, v234
	v_div_scale_f32 v235, vcc, 1.0, v232, 1.0
	v_mul_f32_e32 v236, v235, v234
	v_fma_f32 v237, -v233, v236, v235
	v_fmac_f32_e32 v236, v237, v234
	v_fma_f32 v233, -v233, v236, v235
	s_nop 0
	v_div_fmas_f32 v233, v233, v234, v236
	v_div_fixup_f32 v119, v233, v232, 1.0
	v_mul_f32_e32 v56, v119, v56
	v_mul_f32_e32 v57, v119, v57
	v_mul_f32_e32 v58, v119, v58
	v_mul_f32_e32 v59, v119, v59
	v_mul_f32_e32 v60, v119, v60
	v_mul_f32_e32 v61, v119, v61
	v_mul_f32_e32 v62, v119, v62
	v_mul_f32_e32 v63, v119, v63
	v_mov_b32_e32 v238, v56
	v_mov_b32_e32 v106, 0
	v_cmp_gt_f32_e32 vcc, v57, v238
	s_nop 1
	v_cndmask_b32_e32 v238, v238, v57, vcc
	v_cndmask_b32_e64 v106, v106, 1, vcc
	v_cmp_gt_f32_e32 vcc, v58, v238
	s_nop 1
; __global__ void __launch_bounds__(NTHR, 2) fwd_kernel(Args args) {
;     ...
;             for (int q = 0; q < 8; ++q) { const float sq = wave_sum(ssq[q]); const float rs = 1.0f / sqrtf(sq * (1.0f / DM) + EPS);
;                 float lg[8];
; #pragma unroll
;                 for (int e = 0; e < 8; ++e) lg[e] = wave_sum(acc[q][e]) * rs;
;                 int i0 = 0; float v0 = lg[0];
; #pragma unroll
;                 for (int e = 1; e < 8; ++e) if (lg[e] > v0) { v0 = lg[e]; i0 = e; }
;                 int i1 = -1; float v1 = -__builtin_inff();
; #pragma unroll
;                 for (int e = 0; e < 8; ++e) if (e != i0 && lg[e] > v1) { v1 = lg[e]; i1 = e; }
;                 if (lane == 0) { const int t = t0 + q; const float w0 = 1.0f / (1.0f + expf(v1 - v0));
;                     tok_e[t] = i0 | (i1 << 8); tok_w[2 * t] = w0; tok_w[2 * t + 1] = 1.0f - w0; rstd3[t] = rs;
;                     atomicAdd((int*)&lcnt[i0], 1); atomicAdd((int*)&lcnt[i1], 1); } }
;             __syncthreads();
;             if (tid < 8) cnt_chunk[c * 8 + tid] = lcnt[tid];
;             __syncthreads();
	v_cndmask_b32_e32 v238, v238, v58, vcc
	v_cndmask_b32_e64 v106, v106, 2, vcc
	v_cmp_gt_f32_e32 vcc, v59, v238
	s_nop 1
	v_cndmask_b32_e32 v238, v238, v59, vcc
	v_cndmask_b32_e64 v106, v106, 3, vcc
	v_cmp_gt_f32_e32 vcc, v60, v238
	s_nop 1
	v_cndmask_b32_e32 v238, v238, v60, vcc
	v_cndmask_b32_e64 v106, v106, 4, vcc
	v_cmp_gt_f32_e32 vcc, v61, v238
	s_nop 1
	v_cndmask_b32_e32 v238, v238, v61, vcc
	v_cndmask_b32_e64 v106, v106, 5, vcc
	v_cmp_gt_f32_e32 vcc, v62, v238
	s_nop 1
	v_cndmask_b32_e32 v238, v238, v62, vcc
	v_cndmask_b32_e64 v106, v106, 6, vcc
	v_cmp_gt_f32_e32 vcc, v63, v238
	s_nop 1
	v_cndmask_b32_e32 v238, v238, v63, vcc
	v_cndmask_b32_e64 v106, v106, 7, vcc
	v_mov_b32_e32 v239, v224
	v_mov_b32_e32 v107, -1
	v_cmp_ne_u32_e64 s[68:69], 0, v106
	v_cmp_gt_f32_e32 vcc, v56, v239
	s_and_b64 vcc, vcc, s[68:69]
	v_cndmask_b32_e32 v239, v239, v56, vcc
	v_cndmask_b32_e64 v107, v107, 0, vcc
	v_cmp_ne_u32_e64 s[68:69], 1, v106
	v_cmp_gt_f32_e32 vcc, v57, v239
	s_and_b64 vcc, vcc, s[68:69]
	v_cndmask_b32_e32 v239, v239, v57, vcc
	v_cndmask_b32_e64 v107, v107, 1, vcc
	v_cmp_ne_u32_e64 s[68:69], 2, v106
	v_cmp_gt_f32_e32 vcc, v58, v239
	s_and_b64 vcc, vcc, s[68:69]
	v_cndmask_b32_e32 v239, v239, v58, vcc
	v_cndmask_b32_e64 v107, v107, 2, vcc
	v_cmp_ne_u32_e64 s[68:69], 3, v106
	v_cmp_gt_f32_e32 vcc, v59, v239
	s_and_b64 vcc, vcc, s[68:69]
	v_cndmask_b32_e32 v239, v239, v59, vcc
	v_cndmask_b32_e64 v107, v107, 3, vcc
	v_cmp_ne_u32_e64 s[68:69], 4, v106
	v_cmp_gt_f32_e32 vcc, v60, v239
	s_and_b64 vcc, vcc, s[68:69]
	v_cndmask_b32_e32 v239, v239, v60, vcc
	v_cndmask_b32_e64 v107, v107, 4, vcc
	v_cmp_ne_u32_e64 s[68:69], 5, v106
	v_cmp_gt_f32_e32 vcc, v61, v239
	s_and_b64 vcc, vcc, s[68:69]
	v_cndmask_b32_e32 v239, v239, v61, vcc
	v_cndmask_b32_e64 v107, v107, 5, vcc
	v_cmp_ne_u32_e64 s[68:69], 6, v106
	v_cmp_gt_f32_e32 vcc, v62, v239
	s_and_b64 vcc, vcc, s[68:69]
	v_cndmask_b32_e32 v239, v239, v62, vcc
	v_cndmask_b32_e64 v107, v107, 6, vcc
	v_cmp_ne_u32_e64 s[68:69], 7, v106
	v_cmp_gt_f32_e32 vcc, v63, v239
	s_and_b64 vcc, vcc, s[68:69]
	v_cndmask_b32_e32 v239, v239, v63, vcc
	v_cndmask_b32_e64 v107, v107, 7, vcc
	v_sub_f32_e32 v232, v239, v238
	v_mul_f32_e32 v233, 0x3fb8aa3b, v232
	v_fma_f32 v234, v232, s65, -v233
	v_rndne_f32_e32 v235, v233
	v_fmac_f32_e32 v234, 0x32a5705f, v232
	v_sub_f32_e32 v233, v233, v235
	v_add_f32_e32 v233, v233, v234
	v_exp_f32_e32 v233, v233
	v_cvt_i32_f32_e32 v234, v235
	v_cmp_ngt_f32_e32 vcc, s66, v232
	v_ldexp_f32 v233, v233, v234
	s_nop 0
	v_cndmask_b32_e32 v233, 0, v233, vcc
	v_cmp_nlt_f32_e32 vcc, s67, v232
	s_nop 1
	v_cndmask_b32_e32 v232, v225, v233, vcc
	v_add_f32_e32 v232, 1.0, v232
	v_div_scale_f32 v233, s[68:69], v232, v232, 1.0
	v_rcp_f32_e32 v234, v233
	s_nop 0
	v_fma_f32 v235, -v233, v234, 1.0
	v_fmac_f32_e32 v234, v235, v234
	v_div_scale_f32 v235, vcc, 1.0, v232, 1.0
	v_mul_f32_e32 v236, v235, v234
	v_fma_f32 v237, -v233, v236, v235
	v_fmac_f32_e32 v236, v237, v234
	v_fma_f32 v233, -v233, v236, v235
	s_nop 0
	v_div_fmas_f32 v233, v233, v234, v236
	v_div_fixup_f32 v108, v233, v232, 1.0
	v_sub_f32_e32 v109, 1.0, v108
	v_lshl_add_u32 v110, v107, 8, v106
	s_lshl_b32 s14, s13, 2
	s_add_u32 s56, s8, s14
	s_addc_u32 s57, s9, 0
	s_lshl_b32 s14, s13, 3
	s_add_u32 s58, s8, s14
	s_addc_u32 s59, s9, 0
	v_cmp_eq_u32_e32 vcc, 63, v210
	s_and_saveexec_b64 s[2:3], vcc
	global_store_dword v226, v68, s[56:57] offset:0
	global_store_dwordx2 v227, v[66:67], s[58:59] offset:0
	global_store_dword v228, v112, s[56:57] offset:0
	v_lshl_add_u32 v232, v64, 2, s20
	v_lshl_add_u32 v233, v65, 2, s20
	ds_add_u32 v232, v221
	ds_add_u32 v233, v221
	global_store_dword v226, v74, s[56:57] offset:4
	global_store_dwordx2 v227, v[72:73], s[58:59] offset:8
	global_store_dword v228, v113, s[56:57] offset:4
	v_lshl_add_u32 v232, v70, 2, s20
	v_lshl_add_u32 v233, v71, 2, s20
	ds_add_u32 v232, v221
	ds_add_u32 v233, v221
	global_store_dword v226, v80, s[56:57] offset:8
	global_store_dwordx2 v227, v[78:79], s[58:59] offset:16
	global_store_dword v228, v114, s[56:57] offset:8
	v_lshl_add_u32 v232, v76, 2, s20
	v_lshl_add_u32 v233, v77, 2, s20
	ds_add_u32 v232, v221
	ds_add_u32 v233, v221
	global_store_dword v226, v86, s[56:57] offset:12
	global_store_dwordx2 v227, v[84:85], s[58:59] offset:24
	global_store_dword v228, v115, s[56:57] offset:12
	v_lshl_add_u32 v232, v82, 2, s20
	v_lshl_add_u32 v233, v83, 2, s20
	ds_add_u32 v232, v221
	ds_add_u32 v233, v221
	global_store_dword v226, v92, s[56:57] offset:16
	global_store_dwordx2 v227, v[90:91], s[58:59] offset:32
	global_store_dword v228, v116, s[56:57] offset:16
	v_lshl_add_u32 v232, v88, 2, s20
	v_lshl_add_u32 v233, v89, 2, s20
	ds_add_u32 v232, v221
	ds_add_u32 v233, v221
	global_store_dword v226, v98, s[56:57] offset:20
	global_store_dwordx2 v227, v[96:97], s[58:59] offset:40
	global_store_dword v228, v117, s[56:57] offset:20
	v_lshl_add_u32 v232, v94, 2, s20
	v_lshl_add_u32 v233, v95, 2, s20
	ds_add_u32 v232, v221
	ds_add_u32 v233, v221
	global_store_dword v226, v104, s[56:57] offset:24
	global_store_dwordx2 v227, v[102:103], s[58:59] offset:48
	global_store_dword v228, v118, s[56:57] offset:24
	v_lshl_add_u32 v232, v100, 2, s20
	v_lshl_add_u32 v233, v101, 2, s20
	ds_add_u32 v232, v221
	ds_add_u32 v233, v221
	global_store_dword v226, v110, s[56:57] offset:28
	global_store_dwordx2 v227, v[108:109], s[58:59] offset:56
	global_store_dword v228, v119, s[56:57] offset:28
	v_lshl_add_u32 v232, v106, 2, s20
	v_lshl_add_u32 v233, v107, 2, s20
	ds_add_u32 v232, v221
	ds_add_u32 v233, v221
	s_mov_b64 exec, s[2:3]
	s_waitcnt lgkmcnt(0)
	s_barrier
	v_cmp_gt_u32_e32 vcc, 8, v211
	s_and_saveexec_b64 s[2:3], vcc
	ds_read_b32 v232, v229
	s_lshl_b32 s14, s12, 5
	v_lshl_add_u32 v233, v211, 2, s14
	v_add_u32_e32 v233, 0x392000, v233
	s_waitcnt lgkmcnt(0)
	global_store_dword v233, v232, s[8:9]
	s_mov_b64 exec, s[2:3]
	s_add_i32 s12, s12, s92
	s_cmpk_lt_i32 s12, 0x100
	s_barrier
	s_cbranch_scc1 .Lr14_chunk

; #define PG8_ACC_INIT(unit) do { if constexpr (Epi::ACC_INIT) { E.init(acc, unit, wr, wc, fr, fq); } else { \
;         _Pragma("unroll") for (int a = 0; a < 2; ++a) _Pragma("unroll") for (int b = 0; b < 2; ++b) _Pragma("unroll") for (int m = 0; m < 4; ++m) _Pragma("unroll") for (int n = 0; n < 2; ++n) acc[a][b][m][n] = (f32x4){0.f, 0.f, 0.f, 0.f}; } } while (0)
; template <class Epi, class Sched, class Prob>
; __device__ __forceinline__ void gemm_phase(LAS unsigned char* lds, LAS unsigned char* lds_epi, const Prob g, const Sched& S, const Epi& E, int wid) {
;     ...
;         const bool has_next = S.next(ui + 1, nxt);
;         const char* nA = has_next ? g.a_base(nxt) : cA; const char* nB = has_next ? g.b_base(nxt) : cB;
;     ...
;         PG8_ACC_INIT(nxt);
;         cur = nxt; cA = nA; cB = nB; ++ui;
.LBB0_2090:
	s_ashr_i32 s11, s10, 31
	s_lshl_b64 s[30:31], s[10:11], 19
	s_add_u32 s30, s51, s30
	s_addc_u32 s31, s52, s31
	s_and_b64 s[40:41], s[40:41], exec
	s_cselect_b32 s11, s31, s37
	s_cselect_b32 s29, s30, s36
	s_add_u32 s36, s36, 0x80
	v_mov_b32_e32 v32, 0
	s_addc_u32 s37, s37, 0
	v_lshl_add_u64 v[182:183], v[0:1], 0, s[22:23]
	s_mov_b32 s69, -2
	v_mov_b32_e32 v33, 0
	v_mov_b64_e32 v[34:35], 0
	v_mov_b64_e32 v[36:37], 0
	v_mov_b64_e32 v[38:39], 0
	v_mov_b64_e32 v[48:49], 0
	v_mov_b64_e32 v[50:51], 0
	v_mov_b64_e32 v[52:53], 0
	v_mov_b64_e32 v[54:55], 0
	v_mov_b64_e32 v[64:65], 0
	v_mov_b64_e32 v[66:67], 0
	v_mov_b64_e32 v[68:69], 0
	v_mov_b64_e32 v[70:71], 0
	v_mov_b64_e32 v[80:81], 0
	v_mov_b64_e32 v[82:83], 0
	v_mov_b64_e32 v[84:85], 0
	v_mov_b64_e32 v[86:87], 0
	v_mov_b64_e32 v[40:41], 0
	v_mov_b64_e32 v[42:43], 0
	v_mov_b64_e32 v[44:45], 0
	v_mov_b64_e32 v[46:47], 0
	v_mov_b64_e32 v[56:57], 0
	v_mov_b64_e32 v[58:59], 0
	v_mov_b64_e32 v[60:61], 0
	v_mov_b64_e32 v[62:63], 0
	v_mov_b64_e32 v[72:73], 0
	v_mov_b64_e32 v[74:75], 0
	v_mov_b64_e32 v[76:77], 0
	v_mov_b64_e32 v[78:79], 0
	v_mov_b64_e32 v[88:89], 0
	v_mov_b64_e32 v[90:91], 0
	v_mov_b64_e32 v[92:93], 0
	v_mov_b64_e32 v[94:95], 0
	v_mov_b64_e32 v[96:97], 0
	v_mov_b64_e32 v[98:99], 0
	v_mov_b64_e32 v[100:101], 0
	v_mov_b64_e32 v[102:103], 0
	v_mov_b64_e32 v[112:113], 0
	v_mov_b64_e32 v[114:115], 0
	v_mov_b64_e32 v[116:117], 0
	v_mov_b64_e32 v[118:119], 0
	v_mov_b64_e32 v[128:129], 0
	v_mov_b64_e32 v[130:131], 0
	v_mov_b64_e32 v[132:133], 0
	v_mov_b64_e32 v[134:135], 0
	v_mov_b64_e32 v[144:145], 0
	v_mov_b64_e32 v[146:147], 0
	v_mov_b64_e32 v[148:149], 0
	v_mov_b64_e32 v[150:151], 0
	v_mov_b64_e32 v[104:105], 0
	v_mov_b64_e32 v[106:107], 0
	v_mov_b64_e32 v[108:109], 0
	v_mov_b64_e32 v[110:111], 0
	v_mov_b64_e32 v[120:121], 0
	v_mov_b64_e32 v[122:123], 0
	v_mov_b64_e32 v[124:125], 0
	v_mov_b64_e32 v[126:127], 0
	v_mov_b64_e32 v[136:137], 0
	v_mov_b64_e32 v[138:139], 0
	v_mov_b64_e32 v[140:141], 0
	v_mov_b64_e32 v[142:143], 0
	v_mov_b64_e32 v[152:153], 0
	v_mov_b64_e32 v[154:155], 0
	v_mov_b64_e32 v[156:157], 0
	v_mov_b64_e32 v[158:159], 0

; #define PG8_ACC_INIT(unit) do { if constexpr (Epi::ACC_INIT) { E.init(acc, unit, wr, wc, fr, fq); } else { \
;         _Pragma("unroll") for (int a = 0; a < 2; ++a) _Pragma("unroll") for (int b = 0; b < 2; ++b) _Pragma("unroll") for (int m = 0; m < 4; ++m) _Pragma("unroll") for (int n = 0; n < 2; ++n) acc[a][b][m][n] = (f32x4){0.f, 0.f, 0.f, 0.f}; } } while (0)
; template <class Epi, class Sched, class Prob>
; __device__ __forceinline__ void gemm_phase(LAS unsigned char* lds, LAS unsigned char* lds_epi, const Prob g, const Sched& S, const Epi& E, int wid) {
;     ...
;         const bool has_next = S.next(ui + 1, nxt);
;         const char* nA = has_next ? g.a_base(nxt) : cA; const char* nB = has_next ? g.b_base(nxt) : cB;
;     ...
;         PG8_ACC_INIT(nxt);
;         cur = nxt; cA = nA; cB = nB; ++ui;
.LBB0_2172:
	s_add_u32 s36, s36, 0x80
	v_mov_b32_e32 v32, 0
	s_addc_u32 s37, s37, 0
	v_lshl_add_u64 v[186:187], v[0:1], 0, s[22:23]
	s_mov_b32 s64, -2
	v_mov_b32_e32 v33, 0
	v_mov_b64_e32 v[34:35], 0
	v_mov_b64_e32 v[36:37], 0
	v_mov_b64_e32 v[38:39], 0
	v_mov_b64_e32 v[48:49], 0
	v_mov_b64_e32 v[50:51], 0
	v_mov_b64_e32 v[52:53], 0
	v_mov_b64_e32 v[54:55], 0
	v_mov_b64_e32 v[64:65], 0
	v_mov_b64_e32 v[66:67], 0
	v_mov_b64_e32 v[68:69], 0
	v_mov_b64_e32 v[70:71], 0
	v_mov_b64_e32 v[80:81], 0
	v_mov_b64_e32 v[82:83], 0
	v_mov_b64_e32 v[84:85], 0
	v_mov_b64_e32 v[86:87], 0
	v_mov_b64_e32 v[40:41], 0
	v_mov_b64_e32 v[42:43], 0
	v_mov_b64_e32 v[44:45], 0
	v_mov_b64_e32 v[46:47], 0
	v_mov_b64_e32 v[56:57], 0
	v_mov_b64_e32 v[58:59], 0
	v_mov_b64_e32 v[60:61], 0
	v_mov_b64_e32 v[62:63], 0
	v_mov_b64_e32 v[72:73], 0
	v_mov_b64_e32 v[74:75], 0
	v_mov_b64_e32 v[76:77], 0
	v_mov_b64_e32 v[78:79], 0
	v_mov_b64_e32 v[88:89], 0
	v_mov_b64_e32 v[90:91], 0
	v_mov_b64_e32 v[92:93], 0
	v_mov_b64_e32 v[94:95], 0
	v_mov_b64_e32 v[96:97], 0
	v_mov_b64_e32 v[98:99], 0
	v_mov_b64_e32 v[100:101], 0
	v_mov_b64_e32 v[102:103], 0
	v_mov_b64_e32 v[112:113], 0
	v_mov_b64_e32 v[114:115], 0
	v_mov_b64_e32 v[116:117], 0
	v_mov_b64_e32 v[118:119], 0
	v_mov_b64_e32 v[128:129], 0
	v_mov_b64_e32 v[130:131], 0
	v_mov_b64_e32 v[132:133], 0
	v_mov_b64_e32 v[134:135], 0
	v_mov_b64_e32 v[144:145], 0
	v_mov_b64_e32 v[146:147], 0
	v_mov_b64_e32 v[148:149], 0
	v_mov_b64_e32 v[150:151], 0
	v_mov_b64_e32 v[104:105], 0
	v_mov_b64_e32 v[106:107], 0
	v_mov_b64_e32 v[108:109], 0
	v_mov_b64_e32 v[110:111], 0
	v_mov_b64_e32 v[120:121], 0
	v_mov_b64_e32 v[122:123], 0
	v_mov_b64_e32 v[124:125], 0
	v_mov_b64_e32 v[126:127], 0
	v_mov_b64_e32 v[136:137], 0
	v_mov_b64_e32 v[138:139], 0
	v_mov_b64_e32 v[140:141], 0
	v_mov_b64_e32 v[142:143], 0
	v_mov_b64_e32 v[152:153], 0
	v_mov_b64_e32 v[154:155], 0
	v_mov_b64_e32 v[156:157], 0
	v_mov_b64_e32 v[158:159], 0

; #define PG8_STAGE(bufoff, gbase, o0, o1) do { \
;         __builtin_amdgcn_global_load_lds((const unsigned*)((const char*)(gbase) + (o0)), (LAS unsigned*)(lds + (bufoff) + ldsw), 16, 0, 0); \
;         __builtin_amdgcn_global_load_lds((const unsigned*)((const char*)(gbase) + (o1)), (LAS unsigned*)(lds + (bufoff) + ldsw + 8192), 16, 0, 0); } while (0)
; #define PG8_WAIT_V(n) asm volatile("s_waitcnt vmcnt(" #n ")" ::: "memory")
; #define PG8_BAR __builtin_amdgcn_s_barrier()
; #define PG8_ACC_INIT(unit) do { if constexpr (Epi::ACC_INIT) { E.init(acc, unit, wr, wc, fr, fq); } else { \
;         _Pragma("unroll") for (int a = 0; a < 2; ++a) _Pragma("unroll") for (int b = 0; b < 2; ++b) _Pragma("unroll") for (int m = 0; m < 4; ++m) _Pragma("unroll") for (int n = 0; n < 2; ++n) acc[a][b][m][n] = (f32x4){0.f, 0.f, 0.f, 0.f}; } } while (0)
; template <class Epi, class Sched, class Prob>
; __device__ __forceinline__ void gemm_phase(LAS unsigned char* lds, LAS unsigned char* lds_epi, const Prob g, const Sched& S, const Epi& E, int wid) {
;     ...
;     PG8_ACC_INIT(cur);
;     bf16x8 At[4][2], B0[2][2], B1[2][2];
;     const char* cA = g.a_base(cur); const char* cB = g.b_base(cur);
;     PG8_STAGE(PG8_SB(0, 0), cB, vB0, vB1); PG8_STAGE(PG8_SB(0, 1), cB + hstepB, vB0, vB1); PG8_STAGE(PG8_SA(0, 0), cA, cA00, cA01); PG8_STAGE(PG8_SA(0, 1), cA, cA10, cA11);
;     if (wr == 1) PG8_BAR;
;     PG8_WAIT_V(2); PG8_BAR;
;     PG8_STAGE(PG8_SB(1, 0), cB + kstep, vB0, vB1); PG8_STAGE(PG8_SA(1, 0), cA + kstep, cA00, cA01); PG8_STAGE(PG8_SB(1, 1), cB + hstepB + kstep, vB0, vB1);
;     PG8_WAIT_V(6); PG8_BAR;
.LBB0_2190:
	s_mov_b64 s[12:13], 0x80
	v_lshl_add_u64 v[6:7], v[6:7], 0, s[12:13]
	s_add_i32 m0, s25, 0x18000
	s_waitcnt vmcnt(2)
	s_barrier
	global_load_lds_dwordx4 v[6:7], off
	v_lshl_add_u64 v[2:3], v[2:3], 0, s[12:13]
	s_add_i32 m0, s25, 0x1a000
	s_add_i32 s29, s25, 0x8000
	s_add_i32 s30, s25, 0xa000
	global_load_lds_dwordx4 v[2:3], off
	v_lshl_add_u64 v[0:1], v[0:1], 0, s[12:13]
	s_mov_b32 m0, s29
	s_add_u32 s36, s10, 0xe0080
	global_load_lds_dwordx4 v[0:1], off
	v_lshl_add_u64 v[0:1], v[4:5], 0, s[12:13]
	s_mov_b32 m0, s30
	s_addc_u32 s37, s11, 0
	global_load_lds_dwordx4 v[0:1], off
	v_lshl_add_u64 v[0:1], s[36:37], 0, v[162:163]
	s_add_i32 m0, s25, 0x1c000
	s_mov_b32 s40, 0x1c000
	global_load_lds_dwordx4 v[0:1], off
	v_lshl_add_u64 v[0:1], s[36:37], 0, v[164:165]
	s_add_i32 m0, s25, 0x1e000
	s_add_u32 s36, s15, s21
	global_load_lds_dwordx4 v[0:1], off
	v_lshrrev_b32_e32 v1, 1, v200
	v_mul_lo_u32 v0, v203, s31
	s_addc_u32 s37, s14, 0
	v_mad_u64_u32 v[0:1], s[14:15], v1, s40, v[0:1]
	s_add_u32 s14, s8, s36
	s_addc_u32 s15, s9, s37
	s_add_i32 s17, s17, s18
	s_add_i32 s17, s17, s19
	v_and_b32_e32 v1, 1, v200
	s_add_i32 s17, s17, s20
	v_lshl_or_b32 v0, v1, 6, v0
	v_lshlrev_b32_e32 v1, 1, v206
	s_add_i32 s16, s17, s16
	v_add3_u32 v0, v0, v1, s35
	v_mov_b32_e32 v1, v163
	s_mul_hi_u32 s17, s16, 0xe00000
	s_mul_i32 s16, s16, 0xe00000
	v_lshl_add_u64 v[0:1], s[14:15], 0, v[0:1]
	s_mov_b64 s[36:37], 0x41000080
	s_add_u32 s16, s16, s34
	v_lshl_add_u64 v[174:175], v[0:1], 0, s[36:37]
	v_lshrrev_b32_e32 v1, 1, v199
	v_mul_lo_u32 v0, v201, s31
	s_addc_u32 s17, s17, s33
	v_mad_u64_u32 v[0:1], s[40:41], v1, s40, v[0:1]
	s_add_u32 s16, s16, s21
	v_and_b32_e32 v1, 1, v199
	s_addc_u32 s17, s17, 0
	v_lshl_or_b32 v0, v1, 6, v0
	v_lshlrev_b32_e32 v1, 1, v202
	s_add_u32 s16, s8, s16
	v_add3_u32 v0, v0, v1, s35
	v_mov_b32_e32 v1, v163
	s_addc_u32 s17, s9, s17
	v_lshl_add_u64 v[0:1], s[14:15], 0, v[0:1]
	s_add_u32 s31, s16, 0x27000100
	s_waitcnt vmcnt(6)
	v_lshl_add_u64 v[176:177], v[0:1], 0, s[36:37]
	s_addc_u32 s33, s17, 0
	s_add_i32 s37, 0, 0x10000
	s_add_i32 s41, 0, 0x14000
	s_add_i32 s43, 0, 0x18000
	s_add_i32 s45, 0, 0x1c000
	v_add_u32_e32 v161, s37, v204
	v_add_u32_e32 v186, s41, v204
	s_add_i32 s37, s37, s97
	s_add_i32 s41, s41, s97
	v_add_u32_e32 v188, s43, v204
	v_add_u32_e32 v189, s45, v204
	s_add_i32 s43, s43, s97
	s_add_i32 s45, s45, s97
	v_mov_b32_e32 v171, v163
	v_mov_b32_e32 v173, v163
	s_mov_b32 s34, -2
	s_mov_b64 s[16:17], 0
	v_add_u32_e32 v187, 0, v205
	s_add_i32 s35, s25, 0xc000
	s_add_i32 s36, s25, 0xe000
	s_add_i32 s40, s37, 0x2000
	s_add_i32 s42, s41, 0x2000
	s_add_i32 s44, s43, 0x2000
	s_add_i32 s46, s45, 0x2000
	v_mov_b64_e32 v[32:33], 0
	v_mov_b64_e32 v[34:35], 0
	v_mov_b64_e32 v[36:37], 0
	v_mov_b64_e32 v[38:39], 0
	v_mov_b64_e32 v[40:41], 0
	v_mov_b64_e32 v[42:43], 0
	v_mov_b64_e32 v[44:45], 0
	v_mov_b64_e32 v[46:47], 0
	v_mov_b64_e32 v[48:49], 0
	v_mov_b64_e32 v[50:51], 0
	v_mov_b64_e32 v[52:53], 0
	v_mov_b64_e32 v[54:55], 0
	v_mov_b64_e32 v[56:57], 0
	v_mov_b64_e32 v[58:59], 0
	v_mov_b64_e32 v[60:61], 0
	v_mov_b64_e32 v[62:63], 0
	v_mov_b64_e32 v[64:65], 0
	v_mov_b64_e32 v[66:67], 0
	v_mov_b64_e32 v[68:69], 0
	v_mov_b64_e32 v[70:71], 0
	v_mov_b64_e32 v[72:73], 0
	v_mov_b64_e32 v[74:75], 0
	v_mov_b64_e32 v[76:77], 0
	v_mov_b64_e32 v[78:79], 0
	v_mov_b64_e32 v[80:81], 0
	v_mov_b64_e32 v[82:83], 0
	v_mov_b64_e32 v[84:85], 0
	v_mov_b64_e32 v[86:87], 0
	v_mov_b64_e32 v[88:89], 0
	v_mov_b64_e32 v[90:91], 0
	v_mov_b64_e32 v[92:93], 0
	v_mov_b64_e32 v[94:95], 0
	v_mov_b64_e32 v[96:97], 0
	v_mov_b64_e32 v[98:99], 0
	v_mov_b64_e32 v[100:101], 0
	v_mov_b64_e32 v[102:103], 0
	v_mov_b64_e32 v[104:105], 0
	v_mov_b64_e32 v[106:107], 0
	v_mov_b64_e32 v[108:109], 0
	v_mov_b64_e32 v[110:111], 0
	v_mov_b64_e32 v[112:113], 0
	v_mov_b64_e32 v[114:115], 0
	v_mov_b64_e32 v[116:117], 0
	v_mov_b64_e32 v[118:119], 0
	v_mov_b64_e32 v[120:121], 0
	v_mov_b64_e32 v[122:123], 0
	v_mov_b64_e32 v[124:125], 0
	v_mov_b64_e32 v[126:127], 0
	v_mov_b64_e32 v[128:129], 0
	v_mov_b64_e32 v[130:131], 0
	v_mov_b64_e32 v[132:133], 0
	v_mov_b64_e32 v[134:135], 0
	v_mov_b64_e32 v[136:137], 0
	v_mov_b64_e32 v[138:139], 0
	v_mov_b64_e32 v[140:141], 0
	v_mov_b64_e32 v[142:143], 0
	v_mov_b64_e32 v[144:145], 0
	v_mov_b64_e32 v[146:147], 0
	v_mov_b64_e32 v[148:149], 0
	v_mov_b64_e32 v[150:151], 0
	v_mov_b64_e32 v[152:153], 0
	v_mov_b64_e32 v[154:155], 0
	v_mov_b64_e32 v[156:157], 0
	v_mov_b64_e32 v[158:159], 0
	s_barrier
